# prefetch-defeating wait ladders fixed in the dense weight conversion loop and the two RMS-norm row loops (counted waits keep the next item in flight); split-K tail epilogue gate-weight loads hoisted;
# speedup vs baseline: 1.0236x; 1.0236x over previous
.LBB0_48:
	v_mul_u32_u24_e32 v66, s6, v131
	v_lshlrev_b32_e32 v134, 2, v66
	v_lshl_add_u64 v[66:67], s[4:5], 0, v[134:135]
	v_lshlrev_b32_e32 v134, 2, v137
	v_lshl_add_u64 v[66:67], v[66:67], 0, v[134:135]
	s_lshl_b64 s[4:5], s[6:7], 4
	v_lshl_add_u64 v[74:75], v[66:67], 0, s[4:5]
	global_load_dwordx4 v[70:73], v[66:67], off nt
	s_nop 0
	global_load_dwordx4 v[66:69], v[74:75], off nt
	v_lshl_add_u64 v[74:75], v[74:75], 0, s[4:5]
	v_lshl_add_u64 v[82:83], v[74:75], 0, s[4:5]
	global_load_dwordx4 v[78:81], v[74:75], off nt
	s_nop 0
	global_load_dwordx4 v[74:77], v[82:83], off nt
	v_lshl_add_u64 v[82:83], v[82:83], 0, s[4:5]
	v_lshl_add_u64 v[90:91], v[82:83], 0, s[4:5]
	global_load_dwordx4 v[86:89], v[82:83], off nt
	s_nop 0
	global_load_dwordx4 v[82:85], v[90:91], off nt
	v_lshl_add_u64 v[90:91], v[90:91], 0, s[4:5]
	v_lshl_add_u64 v[98:99], v[90:91], 0, s[4:5]
	v_lshl_add_u64 v[102:103], v[98:99], 0, s[4:5]
	v_lshl_add_u64 v[106:107], v[102:103], 0, s[4:5]
	v_lshl_add_u64 v[110:111], v[106:107], 0, s[4:5]
	v_lshl_add_u64 v[114:115], v[110:111], 0, s[4:5]
	v_lshl_add_u64 v[118:119], v[114:115], 0, s[4:5]
	v_lshl_add_u64 v[122:123], v[118:119], 0, s[4:5]
	v_lshl_add_u64 v[126:127], v[122:123], 0, s[4:5]
	global_load_dwordx4 v[94:97], v[90:91], off nt
	s_nop 0
	global_load_dwordx4 v[90:93], v[98:99], off nt
	s_nop 0
	global_load_dwordx4 v[98:101], v[102:103], off nt
	s_nop 0
	global_load_dwordx4 v[102:105], v[106:107], off nt
	s_nop 0
	global_load_dwordx4 v[106:109], v[110:111], off nt
	s_nop 0
	global_load_dwordx4 v[110:113], v[114:115], off nt
	s_nop 0
	global_load_dwordx4 v[114:117], v[118:119], off nt
	s_nop 0
	global_load_dwordx4 v[118:121], v[122:123], off nt
	s_nop 0
	global_load_dwordx4 v[122:125], v[126:127], off nt
	v_lshl_add_u64 v[126:127], v[126:127], 0, s[4:5]
	global_load_dwordx4 v[126:129], v[126:127], off nt
	s_waitcnt lgkmcnt(0)
	v_add_u32_e32 v164, 0x410, v141
	v_add_u32_e32 v165, 0x418, v141
	v_add_u32_e32 v166, 0x820, v141
	v_add_u32_e32 v167, 0x828, v141
	v_add_u32_e32 v168, 0xc30, v141
	v_add_u32_e32 v169, 0xc38, v141
	v_add_u32_e32 v170, 0x1040, v141
	v_add_u32_e32 v171, 0x1048, v141
	v_add_u32_e32 v172, 0x1450, v141
	v_add_u32_e32 v173, 0x1458, v141
	v_add_u32_e32 v174, 0x1860, v141
	v_add_u32_e32 v175, 0x1868, v141
	v_add_u32_e32 v176, 0x1c70, v141
	v_add_u32_e32 v177, 0x1c78, v141
	v_add_u32_e32 v178, 0x2080, v141
	v_add_u32_e32 v179, 0x2088, v141
	v_add_u32_e32 v180, 0x2490, v141
	v_add_u32_e32 v181, 0x2498, v141
	v_add_u32_e32 v182, 0x28a0, v141
	v_add_u32_e32 v183, 0x28a8, v141
	v_add_u32_e32 v184, 0x2cb0, v141
	v_add_u32_e32 v185, 0x2cb8, v141
	v_add_u32_e32 v186, 0x30c0, v141
	v_add_u32_e32 v187, 0x30c8, v141
	v_add_u32_e32 v188, 0x34d0, v141
	v_add_u32_e32 v189, 0x34d8, v141
	v_add_u32_e32 v190, 0x38e0, v141
	v_add_u32_e32 v191, 0x38e8, v141
	v_add_u32_e32 v192, 0x3cf0, v141
	v_add_u32_e32 v193, 0x3cf8, v141
	s_waitcnt vmcnt(31)
	ds_write2_b32 v141, v2, v3 offset1:1
	ds_write2_b32 v141, v4, v5 offset0:2 offset1:3
	s_waitcnt vmcnt(30)
	ds_write2_b32 v164, v6, v7 offset1:1
	ds_write2_b32 v165, v8, v9 offset1:1
	s_waitcnt vmcnt(29)
	ds_write2_b32 v166, v10, v11 offset1:1
	ds_write2_b32 v167, v12, v13 offset1:1
	s_waitcnt vmcnt(28)
	ds_write2_b32 v168, v14, v15 offset1:1
	ds_write2_b32 v169, v16, v17 offset1:1
	s_waitcnt vmcnt(27)
	ds_write2_b32 v170, v18, v19 offset1:1
	ds_write2_b32 v171, v20, v21 offset1:1
	s_waitcnt vmcnt(26)
	ds_write2_b32 v172, v22, v23 offset1:1
	ds_write2_b32 v173, v24, v25 offset1:1
	s_waitcnt vmcnt(25)
	ds_write2_b32 v174, v26, v27 offset1:1
	ds_write2_b32 v175, v28, v29 offset1:1
	s_waitcnt vmcnt(24)
	ds_write2_b32 v176, v30, v31 offset1:1
	ds_write2_b32 v177, v32, v33 offset1:1
	s_waitcnt vmcnt(23)
	ds_write2_b32 v178, v34, v35 offset1:1
	ds_write2_b32 v179, v36, v37 offset1:1
	s_waitcnt vmcnt(22)
	ds_write2_b32 v180, v38, v39 offset1:1
	ds_write2_b32 v181, v40, v41 offset1:1
	s_waitcnt vmcnt(21)
	ds_write2_b32 v182, v42, v43 offset1:1
	ds_write2_b32 v183, v44, v45 offset1:1
	s_waitcnt vmcnt(20)
	ds_write2_b32 v184, v46, v47 offset1:1
	ds_write2_b32 v185, v48, v49 offset1:1
	s_waitcnt vmcnt(19)
	ds_write2_b32 v186, v50, v51 offset1:1
	ds_write2_b32 v187, v52, v53 offset1:1
	s_waitcnt vmcnt(18)
	ds_write2_b32 v188, v54, v55 offset1:1
	ds_write2_b32 v189, v56, v57 offset1:1
	s_waitcnt vmcnt(17)
	ds_write2_b32 v190, v58, v59 offset1:1
	ds_write2_b32 v191, v60, v61 offset1:1
	s_waitcnt vmcnt(16)
	ds_write2_b32 v192, v62, v63 offset1:1
	ds_write2_b32 v193, v64, v65 offset1:1
	s_branch .Lp0_lad_a

.Lp0_lad_a:
	s_waitcnt lgkmcnt(0)
	ds_read_b32 v194, v139
	s_cmp_eq_u32 s25, 0
	v_add_u32_e32 v149, 0x200, v139
	v_add_u32_e32 v147, 0x400, v139
	s_cbranch_scc1 .LBB0_75
	ds_read2_b32 v[160:161], v139 offset0:65 offset1:130
	ds_read2_b32 v[154:155], v149 offset0:67 offset1:132
	ds_read2_b32 v[152:153], v147 offset0:69 offset1:134
	ds_read_b32 v162, v139 offset:1820
	s_cmp_lg_u32 s79, 0
	s_cselect_b64 s[6:7], -1, 0
	s_and_b64 vcc, exec, s[6:7]
	v_add_u32_e32 v195, s78, v132
	s_cbranch_vccz .LBB0_183
	v_add_u32_e32 v134, s76, v130
	v_lshlrev_b32_e32 v156, 2, v134
	v_lshrrev_b32_e32 v157, 1, v134
	s_cmp_eq_u32 s23, 0
	v_and_b32_e32 v156, 16, v156
	v_and_b32_e32 v157, 12, v157
	v_and_b32_e32 v158, 0xffffffe3, v134
	v_or3_b32 v156, v157, v158, v156
	s_cselect_b64 vcc, -1, 0
	v_cndmask_b32_e32 v158, v156, v134, vcc
	v_ashrrev_i32_e32 v156, 7, v158
	v_ashrrev_i32_e32 v134, 7, v195
	v_mad_u64_u32 v[156:157], s[4:5], v156, s79, v[134:135]
	v_lshrrev_b32_e32 v134, 3, v158
	v_bfe_u32 v159, v195, 6, 1
	v_and_or_b32 v134, v134, 14, v159
	v_lshlrev_b32_e32 v159, 6, v158
	v_and_b32_e32 v163, 63, v195
	v_lshlrev_b32_e32 v158, 2, v158
	v_and_or_b32 v159, v159, s21, v163
	v_lshlrev_b32_e32 v134, 10, v134
	v_and_b32_e32 v158, 32, v158
	v_ashrrev_i32_e32 v157, 31, v156
	v_bitop3_b32 v134, v134, v159, v158 bitop3:0xf6
	v_lshlrev_b64 v[156:157], 14, v[156:157]
	v_mov_b64_e32 v[158:159], v[134:135]
	s_cbranch_execnz .LBB0_53

.LBB0_156:
	v_mul_u32_u24_e32 v2, s6, v131
	v_lshlrev_b32_e32 v134, 2, v2
	v_lshl_add_u64 v[2:3], s[4:5], 0, v[134:135]
	v_lshlrev_b32_e32 v134, 2, v137
	v_lshl_add_u64 v[2:3], v[2:3], 0, v[134:135]
	s_lshl_b64 s[4:5], s[6:7], 4
	v_lshl_add_u64 v[10:11], v[2:3], 0, s[4:5]
	global_load_dwordx4 v[2:5], v[2:3], off nt
	s_nop 0
	global_load_dwordx4 v[6:9], v[10:11], off nt
	v_lshl_add_u64 v[10:11], v[10:11], 0, s[4:5]
	v_lshl_add_u64 v[18:19], v[10:11], 0, s[4:5]
	global_load_dwordx4 v[10:13], v[10:11], off nt
	s_nop 0
	global_load_dwordx4 v[14:17], v[18:19], off nt
	v_lshl_add_u64 v[18:19], v[18:19], 0, s[4:5]
	v_lshl_add_u64 v[26:27], v[18:19], 0, s[4:5]
	global_load_dwordx4 v[18:21], v[18:19], off nt
	s_nop 0
	global_load_dwordx4 v[22:25], v[26:27], off nt
	v_lshl_add_u64 v[26:27], v[26:27], 0, s[4:5]
	v_lshl_add_u64 v[34:35], v[26:27], 0, s[4:5]
	v_lshl_add_u64 v[38:39], v[34:35], 0, s[4:5]
	v_lshl_add_u64 v[42:43], v[38:39], 0, s[4:5]
	v_lshl_add_u64 v[46:47], v[42:43], 0, s[4:5]
	v_lshl_add_u64 v[50:51], v[46:47], 0, s[4:5]
	v_lshl_add_u64 v[54:55], v[50:51], 0, s[4:5]
	v_lshl_add_u64 v[58:59], v[54:55], 0, s[4:5]
	v_lshl_add_u64 v[62:63], v[58:59], 0, s[4:5]
	global_load_dwordx4 v[26:29], v[26:27], off nt
	s_nop 0
	global_load_dwordx4 v[30:33], v[34:35], off nt
	s_nop 0
	global_load_dwordx4 v[34:37], v[38:39], off nt
	s_nop 0
	global_load_dwordx4 v[38:41], v[42:43], off nt
	s_nop 0
	global_load_dwordx4 v[42:45], v[46:47], off nt
	s_nop 0
	global_load_dwordx4 v[46:49], v[50:51], off nt
	s_nop 0
	global_load_dwordx4 v[50:53], v[54:55], off nt
	s_nop 0
	global_load_dwordx4 v[54:57], v[58:59], off nt
	s_nop 0
	global_load_dwordx4 v[58:61], v[62:63], off nt
	v_lshl_add_u64 v[62:63], v[62:63], 0, s[4:5]
	global_load_dwordx4 v[62:65], v[62:63], off nt
	s_waitcnt vmcnt(16)
	s_branch .Lp0_lad_b
.LBB0_157:
	s_waitcnt vmcnt(0)
.Lp0_lad_b:
	ds_write2_b32 v141, v70, v71 offset1:1
	ds_write2_b32 v141, v72, v73 offset0:2 offset1:3
	ds_write2_b32 v164, v66, v67 offset1:1
	ds_write2_b32 v165, v68, v69 offset1:1
	ds_write2_b32 v166, v78, v79 offset1:1
	ds_write2_b32 v167, v80, v81 offset1:1
	ds_write2_b32 v168, v74, v75 offset1:1
	ds_write2_b32 v169, v76, v77 offset1:1
	ds_write2_b32 v170, v86, v87 offset1:1
	ds_write2_b32 v171, v88, v89 offset1:1
	ds_write2_b32 v172, v82, v83 offset1:1
	ds_write2_b32 v173, v84, v85 offset1:1
	ds_write2_b32 v174, v94, v95 offset1:1
	ds_write2_b32 v175, v96, v97 offset1:1
	ds_write2_b32 v176, v90, v91 offset1:1
	ds_write2_b32 v177, v92, v93 offset1:1
	ds_write2_b32 v178, v98, v99 offset1:1
	ds_write2_b32 v179, v100, v101 offset1:1
	ds_write2_b32 v180, v102, v103 offset1:1
	ds_write2_b32 v181, v104, v105 offset1:1
	ds_write2_b32 v182, v106, v107 offset1:1
	ds_write2_b32 v183, v108, v109 offset1:1
	ds_write2_b32 v184, v110, v111 offset1:1
	ds_write2_b32 v185, v112, v113 offset1:1
	ds_write2_b32 v186, v114, v115 offset1:1
	ds_write2_b32 v187, v116, v117 offset1:1
	ds_write2_b32 v188, v118, v119 offset1:1
	ds_write2_b32 v189, v120, v121 offset1:1
	ds_write2_b32 v190, v122, v123 offset1:1
	ds_write2_b32 v191, v124, v125 offset1:1
	ds_write2_b32 v192, v126, v127 offset1:1
	ds_write2_b32 v193, v128, v129 offset1:1
	s_waitcnt lgkmcnt(0)
	ds_read_b32 v164, v139
	s_cmp_eq_u32 s29, 0
	s_cbranch_scc1 .LBB0_199
	ds_read2_b32 v[160:161], v139 offset0:65 offset1:130
	ds_read2_b32 v[154:155], v149 offset0:67 offset1:132
	s_waitcnt lgkmcnt(14)
	ds_read2_b32 v[152:153], v147 offset0:69 offset1:134
	ds_read_b32 v162, v139 offset:1820
	s_cmp_lg_u32 s27, 0
	s_cselect_b64 s[6:7], -1, 0
	s_and_b64 vcc, exec, s[6:7]
	v_add_u32_e32 v165, s84, v132
	s_cbranch_vccz .LBB0_255
	v_add_u32_e32 v134, s88, v130
	v_lshlrev_b32_e32 v156, 2, v134
	v_lshrrev_b32_e32 v157, 1, v134
	s_cmp_eq_u32 s28, 0
	v_and_b32_e32 v156, 16, v156
	v_and_b32_e32 v157, 12, v157
	v_and_b32_e32 v158, 0xffffffe3, v134
	v_or3_b32 v156, v157, v158, v156
	s_cselect_b64 vcc, -1, 0
	v_cndmask_b32_e32 v158, v156, v134, vcc
	v_ashrrev_i32_e32 v156, 7, v158
	v_ashrrev_i32_e32 v134, 7, v165
	v_mad_u64_u32 v[156:157], s[4:5], v156, s27, v[134:135]
	v_lshrrev_b32_e32 v134, 3, v158
	v_bfe_u32 v159, v165, 6, 1
	v_and_or_b32 v134, v134, 14, v159
	v_lshlrev_b32_e32 v159, 6, v158
	v_and_b32_e32 v163, 63, v165
	v_lshlrev_b32_e32 v158, 2, v158
	v_and_or_b32 v159, v159, s21, v163
	v_lshlrev_b32_e32 v134, 10, v134
	v_and_b32_e32 v158, 32, v158
	v_ashrrev_i32_e32 v157, 31, v156
	v_bitop3_b32 v134, v134, v159, v158 bitop3:0xf6
	v_lshlrev_b64 v[156:157], 14, v[156:157]
	v_mov_b64_e32 v[158:159], v[134:135]
	s_cbranch_execnz .LBB0_161

.LBB0_440:
	s_add_i32 s4, s6, s34
	s_cmpk_gt_i32 s4, 0x3fff
	s_cbranch_scc1 .LBB0_442
	s_ashr_i32 s5, s4, 31
	s_lshl_b64 s[0:1], s[4:5], 13
	v_lshl_add_u64 v[82:83], v[100:101], 0, s[0:1]
	global_load_dwordx4 v[78:81], v[82:83], off
	global_load_dwordx4 v[74:77], v[82:83], off offset:1024
	global_load_dwordx4 v[70:73], v[82:83], off offset:2048
	global_load_dwordx4 v[66:69], v[82:83], off offset:3072
	v_add_co_u32_e32 v82, vcc, 0x1000, v82
	s_nop 1
	v_addc_co_u32_e32 v83, vcc, 0, v83, vcc
	global_load_dwordx4 v[94:97], v[82:83], off
	global_load_dwordx4 v[90:93], v[82:83], off offset:1024
	global_load_dwordx4 v[86:89], v[82:83], off offset:2048
	s_nop 0
	global_load_dwordx4 v[82:85], v[82:83], off offset:3072
	s_waitcnt vmcnt(15)
	v_pk_mul_f32 v[130:131], v[34:35], v[34:35]
	s_waitcnt vmcnt(14)
	v_pk_mul_f32 v[132:133], v[38:39], v[38:39]
	v_pk_mul_f32 v[126:127], v[36:37], v[36:37]
	v_pk_mul_f32 v[128:129], v[40:41], v[40:41]
	v_mov_b32_e32 v134, v130
	v_mov_b32_e32 v135, v132
	v_mov_b32_e32 v132, v131
	s_waitcnt vmcnt(13)
	v_pk_mul_f32 v[122:123], v[44:45], v[44:45]
	v_pk_mul_f32 v[124:125], v[42:43], v[42:43]
	v_pk_add_f32 v[130:131], v[134:135], v[132:133]
	v_mov_b32_e32 v132, v126
	v_mov_b32_e32 v133, v128
	v_mov_b32_e32 v128, v127
	v_pk_add_f32 v[126:127], v[132:133], v[128:129]
	v_pk_mov_b32 v[128:129], v[124:125], v[122:123] op_sel:[1,0]
	v_mov_b32_e32 v125, v123
	v_pk_add_f32 v[122:123], v[128:129], v[124:125]
	v_pk_add_f32 v[126:127], v[130:131], v[126:127]
	v_pk_add_f32 v[122:123], v[122:123], v[122:123] op_sel_hi:[0,1]
	s_waitcnt vmcnt(12)
	v_mul_f32_e32 v122, v46, v46
	v_pk_fma_f32 v[124:125], v[46:47], v[46:47], v[122:123] op_sel_hi:[1,1,0]
	v_mul_f32_e32 v122, v48, v48
	v_pk_add_f32 v[126:127], v[126:127], v[126:127] op_sel_hi:[0,1]
	v_pk_fma_f32 v[128:129], v[48:49], v[48:49], v[122:123] op_sel_hi:[1,1,0]
	s_waitcnt vmcnt(11)
	v_mul_f32_e32 v124, v50, v50
	v_mul_f32_e32 v128, v51, v51
	v_mul_f32_e32 v122, v52, v52
	v_mul_f32_e32 v126, v53, v53
	s_waitcnt vmcnt(10)
	v_pk_mul_f32 v[118:119], v[56:57], v[56:57]
	v_pk_mul_f32 v[120:121], v[54:55], v[54:55]
	v_pk_add_f32 v[124:125], v[124:125], v[128:129]
	v_pk_add_f32 v[122:123], v[122:123], v[126:127]
	s_nop 0
	v_pk_add_f32 v[122:123], v[124:125], v[122:123]
	v_pk_mov_b32 v[124:125], v[120:121], v[118:119] op_sel:[1,0]
	v_mov_b32_e32 v121, v119
	v_pk_add_f32 v[118:119], v[124:125], v[120:121]
	v_pk_add_f32 v[122:123], v[122:123], v[122:123] op_sel_hi:[0,1]
	v_pk_add_f32 v[118:119], v[118:119], v[118:119] op_sel_hi:[0,1]
	s_waitcnt vmcnt(9)
	v_mul_f32_e32 v118, v58, v58
	v_pk_fma_f32 v[120:121], v[58:59], v[58:59], v[118:119] op_sel_hi:[1,1,0]
	v_mul_f32_e32 v118, v60, v60
	v_pk_fma_f32 v[124:125], v[60:61], v[60:61], v[118:119] op_sel_hi:[1,1,0]
	s_waitcnt vmcnt(8)
	s_branch .Lrms_lad_a0

.Lrms_lad_a0:
	v_mul_f32_e32 v120, v62, v62
	v_mul_f32_e32 v124, v63, v63
	v_mul_f32_e32 v118, v64, v64
	v_mul_f32_e32 v122, v65, v65
	v_pk_add_f32 v[120:121], v[120:121], v[124:125]
	v_pk_add_f32 v[118:119], v[118:119], v[122:123]
	s_nop 0
	v_pk_add_f32 v[118:119], v[120:121], v[118:119]
	s_nop 0
	v_add_f32_e32 v117, v118, v119
	s_nop 1
	v_add_f32_dpp v117, v117, v117 quad_perm:[1,0,3,2] row_mask:0xf bank_mask:0xf bound_ctrl:1
	s_nop 1
	v_add_f32_dpp v117, v117, v117 quad_perm:[2,3,0,1] row_mask:0xf bank_mask:0xf bound_ctrl:1
	s_nop 1
	v_add_f32_dpp v117, v117, v117 row_half_mirror row_mask:0xf bank_mask:0xf bound_ctrl:1
	s_nop 1
	v_add_f32_dpp v117, v117, v117 row_mirror row_mask:0xf bank_mask:0xf bound_ctrl:1
	s_nop 0
	v_readlane_b32 s5, v117, 16
	v_readlane_b32 s7, v117, 48
	v_readlane_b32 s0, v117, 0
	v_readlane_b32 s1, v117, 32
	v_mov_b32_e32 v118, s5
	v_mov_b32_e32 v119, s7
	v_pk_add_f32 v[118:119], s[0:1], v[118:119]
	s_ashr_i32 s7, s6, 31
	v_add_f32_e32 v117, v118, v119
	v_fmamk_f32 v117, v117, 0x3a000000, v114
	v_mul_f32_e32 v118, 0x4f800000, v117
	v_cmp_gt_f32_e32 vcc, s9, v117
	s_nop 1
	v_cndmask_b32_e32 v117, v117, v118, vcc
	v_sqrt_f32_e32 v118, v117
	s_nop 0
	v_add_u32_e32 v119, -1, v118
	v_fma_f32 v120, -v119, v118, v117
	v_cmp_ge_f32_e64 s[0:1], 0, v120
	v_add_u32_e32 v120, 1, v118
	s_nop 0
	v_cndmask_b32_e64 v119, v118, v119, s[0:1]
	v_fma_f32 v118, -v120, v118, v117
	v_cmp_lt_f32_e64 s[0:1], 0, v118
	s_nop 1
	v_cndmask_b32_e64 v118, v119, v120, s[0:1]
	v_mul_f32_e32 v119, 0x37800000, v118
	v_cndmask_b32_e32 v118, v118, v119, vcc
	v_cmp_class_f32_e32 vcc, v117, v115
	s_nop 1
	v_cndmask_b32_e32 v117, v118, v117, vcc
	v_div_scale_f32 v118, s[0:1], v117, v117, 1.0
	v_rcp_f32_e32 v119, v118
	s_nop 0
	v_fma_f32 v120, -v118, v119, 1.0
	v_fmac_f32_e32 v119, v120, v119
	v_div_scale_f32 v120, vcc, 1.0, v117, 1.0
	v_mul_f32_e32 v121, v120, v119
	v_fma_f32 v122, -v118, v121, v120
	v_fmac_f32_e32 v121, v122, v119
	v_fma_f32 v118, -v118, v121, v120
	v_div_fmas_f32 v118, v118, v119, v121
	v_div_fixup_f32 v118, v118, v117, 1.0
	v_pk_mul_f32 v[126:127], v[40:41], v[118:119] op_sel_hi:[1,0]
	v_pk_mul_f32 v[124:125], v[38:39], v[118:119] op_sel_hi:[1,0]
	v_pk_mul_f32 v[126:127], v[8:9], v[126:127]
	v_pk_mul_f32 v[120:121], v[34:35], v[118:119] op_sel_hi:[1,0]
	v_pk_mul_f32 v[122:123], v[36:37], v[118:119] op_sel_hi:[1,0]
	v_pk_mul_f32 v[124:125], v[6:7], v[124:125]
	v_max_f32_e64 v119, |v126|, |v127|
	v_pk_mul_f32 v[122:123], v[4:5], v[122:123]
	v_max3_f32 v119, |v124|, |v125|, v119
	v_pk_mul_f32 v[120:121], v[2:3], v[120:121]
	v_max_f32_e64 v117, |v122|, |v123|
	v_pk_mul_f32 v[130:131], v[44:45], v[118:119] op_sel_hi:[1,0]
	v_max3_f32 v117, |v120|, |v121|, v117
	v_pk_mul_f32 v[128:129], v[42:43], v[118:119] op_sel_hi:[1,0]
	v_pk_mul_f32 v[130:131], v[12:13], v[130:131]
	v_max3_f32 v117, v117, 0, v119
	v_pk_mul_f32 v[128:129], v[10:11], v[128:129]
	v_max_f32_e64 v119, |v130|, |v131|
	v_max3_f32 v119, |v128|, |v129|, v119
	v_pk_mul_f32 v[134:135], v[48:49], v[118:119] op_sel_hi:[1,0]
	v_pk_mul_f32 v[132:133], v[46:47], v[118:119] op_sel_hi:[1,0]
	v_pk_mul_f32 v[134:135], v[16:17], v[134:135]
	v_pk_mul_f32 v[132:133], v[14:15], v[132:133]
	v_max_f32_e64 v136, |v134|, |v135|
	v_max3_f32 v136, |v132|, |v133|, v136
	v_pk_mul_f32 v[138:139], v[52:53], v[118:119] op_sel_hi:[1,0]
	v_max3_f32 v117, v117, v119, v136
	v_pk_mul_f32 v[136:137], v[50:51], v[118:119] op_sel_hi:[1,0]
	v_pk_mul_f32 v[138:139], v[20:21], v[138:139]
	v_pk_mul_f32 v[136:137], v[18:19], v[136:137]
	v_max_f32_e64 v119, |v138|, |v139|
	v_max3_f32 v119, |v136|, |v137|, v119
	v_pk_mul_f32 v[142:143], v[56:57], v[118:119] op_sel_hi:[1,0]
	v_pk_mul_f32 v[140:141], v[54:55], v[118:119] op_sel_hi:[1,0]
	v_pk_mul_f32 v[142:143], v[24:25], v[142:143]
	v_pk_mul_f32 v[140:141], v[22:23], v[140:141]
	v_max_f32_e64 v144, |v142|, |v143|
	v_max3_f32 v144, |v140|, |v141|, v144
	v_pk_mul_f32 v[146:147], v[60:61], v[118:119] op_sel_hi:[1,0]
	v_max3_f32 v117, v117, v119, v144
	v_pk_mul_f32 v[144:145], v[58:59], v[118:119] op_sel_hi:[1,0]
	v_pk_mul_f32 v[146:147], v[28:29], v[146:147]
	v_pk_mul_f32 v[144:145], v[26:27], v[144:145]
	v_max_f32_e64 v119, |v146|, |v147|
	v_max3_f32 v150, |v144|, |v145|, v119
	v_pk_mul_f32 v[148:149], v[62:63], v[118:119] op_sel_hi:[1,0]
	v_pk_mul_f32 v[118:119], v[64:65], v[118:119] op_sel_hi:[1,0]
	v_pk_mul_f32 v[148:149], v[30:31], v[148:149]
	v_pk_mul_f32 v[118:119], v[32:33], v[118:119]
	s_nop 0
	v_max_f32_e64 v151, |v118|, |v119|
	v_max3_f32 v151, |v148|, |v149|, v151
	v_max3_f32 v117, v117, v150, v151
	s_nop 1
	v_mov_b32_dpp v150, v117 quad_perm:[1,0,3,2] row_mask:0xf bank_mask:0xf bound_ctrl:1
	v_max_f32_e32 v150, v150, v150
	v_max_f32_e32 v117, v117, v150
	s_nop 1
	v_mov_b32_dpp v150, v117 quad_perm:[2,3,0,1] row_mask:0xf bank_mask:0xf bound_ctrl:1
	v_max_f32_e32 v150, v150, v150
	v_max_f32_e32 v117, v117, v150
	s_nop 1
	v_mov_b32_dpp v150, v117 row_half_mirror row_mask:0xf bank_mask:0xf bound_ctrl:1
	v_max_f32_e32 v150, v150, v150
	v_max_f32_e32 v117, v117, v150
	s_nop 1
	v_mov_b32_dpp v150, v117 row_mirror row_mask:0xf bank_mask:0xf bound_ctrl:1
	v_max_f32_e32 v150, v150, v150
	v_max_f32_e32 v117, v117, v150
	s_nop 0
	v_readlane_b32 s0, v117, 0
	v_readlane_b32 s1, v117, 16
	s_nop 0
	v_max_f32_e64 v151, s0, s0
	v_max_f32_e64 v150, s1, s1
	v_readlane_b32 s0, v117, 32
	v_readlane_b32 s1, v117, 48
	v_max_f32_e32 v150, v151, v150
	v_max_f32_e64 v151, s0, s0
	v_max_f32_e64 v117, s1, s1
	v_max_f32_e32 v117, v151, v117
	v_max3_f32 v117, v150, v117, s10
	v_div_scale_f32 v150, s[0:1], v117, v117, s11
	v_rcp_f32_e32 v151, v150
	s_lshl_b64 s[0:1], s[6:7], 11
	v_fma_f32 v152, -v150, v151, 1.0
	v_fmac_f32_e32 v151, v152, v151
	v_div_scale_f32 v152, vcc, s11, v117, s11
	v_mul_f32_e32 v153, v152, v151
	v_fma_f32 v154, -v150, v153, v152
	v_fmac_f32_e32 v153, v154, v151
	v_fma_f32 v150, -v150, v153, v152
	v_div_fmas_f32 v150, v150, v151, v153
	v_div_fixup_f32 v150, v150, v117, s11
	v_mul_f32_e32 v120, v120, v150
	v_rndne_f32_e32 v120, v120
	v_mul_f32_e32 v121, v121, v150
	v_rndne_f32_e32 v121, v121
	v_mul_f32_e32 v122, v122, v150
	v_med3_f32 v120, v120, s14, v116
	v_rndne_f32_e32 v122, v122
	v_mul_f32_e32 v123, v123, v150
	v_med3_f32 v121, v121, s14, v116
	v_add_f32_e32 v120, 0x43000000, v120
	v_rndne_f32_e32 v123, v123
	v_med3_f32 v122, v122, s14, v116
	v_cvt_i32_f32_e32 v151, v120
	v_add_f32_e32 v120, 0x43000000, v121
	v_med3_f32 v123, v123, s14, v116
	v_cvt_i32_f32_e32 v152, v120
	v_add_f32_e32 v120, 0x43000000, v122
	v_cvt_i32_f32_sdwa v122, v120 dst_sel:WORD_1 dst_unused:UNUSED_PAD src0_sel:DWORD
	v_add_f32_e32 v120, 0x43000000, v123
	v_cvt_i32_f32_sdwa v123, v120 dst_sel:BYTE_3 dst_unused:UNUSED_PAD src0_sel:DWORD
	v_lshlrev_b32_e32 v152, 8, v152
	v_or3_b32 v122, v152, v151, v122
	v_lshl_add_u64 v[120:121], v[102:103], 0, s[0:1]
	v_bitop3_b32 v122, v122, s15, v123 bitop3:0x36
	v_mul_f32_e32 v123, v124, v150
	v_mul_f32_e32 v124, v125, v150
	v_rndne_f32_e32 v124, v124
	v_mul_f32_e32 v125, v126, v150
	v_rndne_f32_e32 v123, v123
	v_rndne_f32_e32 v125, v125
	v_med3_f32 v124, v124, s14, v116
	v_med3_f32 v123, v123, s14, v116
	v_med3_f32 v125, v125, s14, v116
	v_add_f32_e32 v124, 0x43000000, v124
	v_add_f32_e32 v123, 0x43000000, v123
	v_cvt_i32_f32_e32 v124, v124
	v_add_f32_e32 v125, 0x43000000, v125
	v_cvt_i32_f32_e32 v123, v123
	v_cvt_i32_f32_sdwa v125, v125 dst_sel:WORD_1 dst_unused:UNUSED_PAD src0_sel:DWORD
	v_mul_f32_e32 v126, v127, v150
	v_rndne_f32_e32 v126, v126
	global_store_dword v[120:121], v122, off
	v_lshlrev_b32_e32 v122, 8, v124
	v_mul_f32_e32 v124, v129, v150
	v_med3_f32 v126, v126, s14, v116
	v_or3_b32 v122, v122, v123, v125
	v_mul_f32_e32 v123, v128, v150
	v_rndne_f32_e32 v124, v124
	v_mul_f32_e32 v125, v130, v150
	v_add_f32_e32 v126, 0x43000000, v126
	v_rndne_f32_e32 v123, v123
	v_rndne_f32_e32 v125, v125
	v_med3_f32 v124, v124, s14, v116
	v_cvt_i32_f32_sdwa v126, v126 dst_sel:BYTE_3 dst_unused:UNUSED_PAD src0_sel:DWORD
	v_med3_f32 v123, v123, s14, v116
	v_med3_f32 v125, v125, s14, v116
	v_add_f32_e32 v124, 0x43000000, v124
	v_add_f32_e32 v123, 0x43000000, v123
	v_cvt_i32_f32_e32 v124, v124
	v_add_f32_e32 v125, 0x43000000, v125
	v_cvt_i32_f32_e32 v123, v123
	v_cvt_i32_f32_sdwa v125, v125 dst_sel:WORD_1 dst_unused:UNUSED_PAD src0_sel:DWORD
	v_bitop3_b32 v122, v122, s15, v126 bitop3:0x36
	v_mul_f32_e32 v126, v131, v150
	v_rndne_f32_e32 v126, v126
	global_store_dword v[120:121], v122, off offset:256
	v_lshlrev_b32_e32 v122, 8, v124
	v_mul_f32_e32 v124, v133, v150
	v_med3_f32 v126, v126, s14, v116
	v_or3_b32 v122, v122, v123, v125
	v_mul_f32_e32 v123, v132, v150
	v_rndne_f32_e32 v124, v124
	v_mul_f32_e32 v125, v134, v150
	v_add_f32_e32 v126, 0x43000000, v126
	v_rndne_f32_e32 v123, v123
	v_rndne_f32_e32 v125, v125
	v_med3_f32 v124, v124, s14, v116
	v_cvt_i32_f32_sdwa v126, v126 dst_sel:BYTE_3 dst_unused:UNUSED_PAD src0_sel:DWORD
	v_med3_f32 v123, v123, s14, v116
	v_med3_f32 v125, v125, s14, v116
	v_add_f32_e32 v124, 0x43000000, v124
	v_add_f32_e32 v123, 0x43000000, v123
	v_cvt_i32_f32_e32 v124, v124
	v_add_f32_e32 v125, 0x43000000, v125
	v_cvt_i32_f32_e32 v123, v123
	v_cvt_i32_f32_sdwa v125, v125 dst_sel:WORD_1 dst_unused:UNUSED_PAD src0_sel:DWORD
	v_bitop3_b32 v122, v122, s15, v126 bitop3:0x36
	v_mul_f32_e32 v126, v135, v150
	v_rndne_f32_e32 v126, v126
	global_store_dword v[120:121], v122, off offset:512
	v_lshlrev_b32_e32 v122, 8, v124
	v_mul_f32_e32 v124, v137, v150
	v_med3_f32 v126, v126, s14, v116
	v_or3_b32 v122, v122, v123, v125
	v_mul_f32_e32 v123, v136, v150
	v_rndne_f32_e32 v124, v124
	v_mul_f32_e32 v125, v138, v150
	v_add_f32_e32 v126, 0x43000000, v126
	v_rndne_f32_e32 v123, v123
	v_rndne_f32_e32 v125, v125
	v_med3_f32 v124, v124, s14, v116
	v_cvt_i32_f32_sdwa v126, v126 dst_sel:BYTE_3 dst_unused:UNUSED_PAD src0_sel:DWORD
	v_med3_f32 v123, v123, s14, v116
	v_med3_f32 v125, v125, s14, v116
	v_add_f32_e32 v124, 0x43000000, v124
	v_add_f32_e32 v123, 0x43000000, v123
	v_cvt_i32_f32_e32 v124, v124
	v_add_f32_e32 v125, 0x43000000, v125
	v_cvt_i32_f32_e32 v123, v123
	v_cvt_i32_f32_sdwa v125, v125 dst_sel:WORD_1 dst_unused:UNUSED_PAD src0_sel:DWORD
	v_bitop3_b32 v122, v122, s15, v126 bitop3:0x36
	v_mul_f32_e32 v126, v139, v150
	v_rndne_f32_e32 v126, v126
	global_store_dword v[120:121], v122, off offset:768
	v_lshlrev_b32_e32 v122, 8, v124
	v_mul_f32_e32 v124, v141, v150
	v_med3_f32 v126, v126, s14, v116
	v_or3_b32 v122, v122, v123, v125
	v_mul_f32_e32 v123, v140, v150
	v_rndne_f32_e32 v124, v124
	v_mul_f32_e32 v125, v142, v150
	v_add_f32_e32 v126, 0x43000000, v126
	v_rndne_f32_e32 v123, v123
	v_rndne_f32_e32 v125, v125
	v_med3_f32 v124, v124, s14, v116
	v_cvt_i32_f32_sdwa v126, v126 dst_sel:BYTE_3 dst_unused:UNUSED_PAD src0_sel:DWORD
	v_med3_f32 v123, v123, s14, v116
	v_med3_f32 v125, v125, s14, v116
	v_add_f32_e32 v124, 0x43000000, v124
	v_add_f32_e32 v123, 0x43000000, v123
	v_cvt_i32_f32_e32 v124, v124
	v_add_f32_e32 v125, 0x43000000, v125
	v_cvt_i32_f32_e32 v123, v123
	v_cvt_i32_f32_sdwa v125, v125 dst_sel:WORD_1 dst_unused:UNUSED_PAD src0_sel:DWORD
	v_bitop3_b32 v122, v122, s15, v126 bitop3:0x36
	v_mul_f32_e32 v126, v143, v150
	v_rndne_f32_e32 v126, v126
	global_store_dword v[120:121], v122, off offset:1024
	v_lshlrev_b32_e32 v122, 8, v124
	v_mul_f32_e32 v124, v145, v150
	v_med3_f32 v126, v126, s14, v116
	v_or3_b32 v122, v122, v123, v125
	v_mul_f32_e32 v123, v144, v150
	v_rndne_f32_e32 v124, v124
	v_mul_f32_e32 v125, v146, v150
	v_add_f32_e32 v126, 0x43000000, v126
	v_rndne_f32_e32 v123, v123
	v_rndne_f32_e32 v125, v125
	v_med3_f32 v124, v124, s14, v116
	v_cvt_i32_f32_sdwa v126, v126 dst_sel:BYTE_3 dst_unused:UNUSED_PAD src0_sel:DWORD
	v_med3_f32 v123, v123, s14, v116
	v_med3_f32 v125, v125, s14, v116
	v_add_f32_e32 v124, 0x43000000, v124
	v_add_f32_e32 v123, 0x43000000, v123
	v_cvt_i32_f32_e32 v124, v124
	v_add_f32_e32 v125, 0x43000000, v125
	v_cvt_i32_f32_e32 v123, v123
	v_cvt_i32_f32_sdwa v125, v125 dst_sel:WORD_1 dst_unused:UNUSED_PAD src0_sel:DWORD
	v_bitop3_b32 v122, v122, s15, v126 bitop3:0x36
	v_mul_f32_e32 v126, v147, v150
	v_rndne_f32_e32 v126, v126
	global_store_dword v[120:121], v122, off offset:1280
	v_lshlrev_b32_e32 v122, 8, v124
	v_mul_f32_e32 v124, v149, v150
	v_med3_f32 v126, v126, s14, v116
	v_or3_b32 v122, v122, v123, v125
	v_mul_f32_e32 v123, v148, v150
	v_rndne_f32_e32 v124, v124
	v_mul_f32_e32 v118, v118, v150
	v_add_f32_e32 v126, 0x43000000, v126
	v_rndne_f32_e32 v123, v123
	v_rndne_f32_e32 v118, v118
	v_mul_f32_e32 v119, v119, v150
	v_med3_f32 v124, v124, s14, v116
	v_cvt_i32_f32_sdwa v126, v126 dst_sel:BYTE_3 dst_unused:UNUSED_PAD src0_sel:DWORD
	v_rndne_f32_e32 v119, v119
	v_med3_f32 v123, v123, s14, v116
	v_med3_f32 v118, v118, s14, v116
	v_add_f32_e32 v124, 0x43000000, v124
	v_med3_f32 v119, v119, s14, v116
	v_add_f32_e32 v123, 0x43000000, v123
	v_cvt_i32_f32_e32 v124, v124
	v_add_f32_e32 v118, 0x43000000, v118
	v_cvt_i32_f32_e32 v123, v123
	v_cvt_i32_f32_sdwa v118, v118 dst_sel:WORD_1 dst_unused:UNUSED_PAD src0_sel:DWORD
	v_add_f32_e32 v119, 0x43000000, v119
	v_cvt_i32_f32_sdwa v119, v119 dst_sel:BYTE_3 dst_unused:UNUSED_PAD src0_sel:DWORD
	v_bitop3_b32 v122, v122, s15, v126 bitop3:0x36
	global_store_dword v[120:121], v122, off offset:1536
	v_lshlrev_b32_e32 v122, 8, v124
	v_or3_b32 v118, v122, v123, v118
	v_bitop3_b32 v118, v118, s15, v119 bitop3:0x36
	global_store_dword v[120:121], v118, off offset:1792
	s_and_saveexec_b64 s[0:1], s[2:3]
	s_cbranch_execnz .LBB0_444
	s_or_b64 exec, exec, s[0:1]
	s_cmpk_gt_i32 s4, 0x3fff
	s_mov_b64 s[0:1], -1
	s_cbranch_scc1 .LBB0_439
	s_branch .LBB0_445

.LBB0_445:
	s_add_i32 s0, s8, s6
	s_cmpk_gt_i32 s0, 0x3fff
	s_cbranch_scc1 .LBB0_447
	s_ashr_i32 s1, s0, 31
	s_lshl_b64 s[0:1], s[0:1], 13
	v_lshl_add_u64 v[50:51], v[100:101], 0, s[0:1]
	v_add_co_u32_e32 v62, vcc, 0x1000, v50
	global_load_dwordx4 v[34:37], v[50:51], off
	global_load_dwordx4 v[38:41], v[50:51], off offset:1024
	global_load_dwordx4 v[42:45], v[50:51], off offset:2048
	global_load_dwordx4 v[46:49], v[50:51], off offset:3072
	v_addc_co_u32_e32 v63, vcc, 0, v51, vcc
	global_load_dwordx4 v[50:53], v[62:63], off
	global_load_dwordx4 v[54:57], v[62:63], off offset:1024
	global_load_dwordx4 v[58:61], v[62:63], off offset:2048
	s_nop 0
	global_load_dwordx4 v[62:65], v[62:63], off offset:3072
	s_waitcnt vmcnt(8)
	s_branch .Lrms_lad_b0
.LBB0_447:
	s_waitcnt vmcnt(0)
.Lrms_lad_b0:
	v_mov_b32_e32 v120, v75
	v_mov_b32_e32 v121, v79
	v_mov_b32_e32 v118, v74
	v_mov_b32_e32 v119, v78
	v_pk_mul_f32 v[120:121], v[120:121], v[120:121]
	v_mov_b32_e32 v122, v77
	v_mov_b32_e32 v123, v81
	v_pk_fma_f32 v[118:119], v[118:119], v[118:119], v[120:121]
	v_mov_b32_e32 v120, v76
	v_mov_b32_e32 v121, v80
	v_pk_mul_f32 v[122:123], v[122:123], v[122:123]
	s_nop 0
	v_pk_fma_f32 v[120:121], v[120:121], v[120:121], v[122:123]
	v_pk_mul_f32 v[122:123], v[70:71], v[70:71]
	v_pk_add_f32 v[118:119], v[118:119], v[120:121]
	v_pk_mul_f32 v[120:121], v[72:73], v[72:73]
	v_pk_add_f32 v[118:119], v[118:119], v[118:119] op_sel_hi:[0,1]
	v_pk_mov_b32 v[124:125], v[122:123], v[120:121] op_sel:[1,0]
	v_mov_b32_e32 v123, v121
	v_mul_f32_e32 v118, v66, v66
	v_pk_add_f32 v[120:121], v[124:125], v[122:123]
	v_pk_fma_f32 v[122:123], v[66:67], v[66:67], v[118:119] op_sel_hi:[1,1,0]
	v_mul_f32_e32 v118, v68, v68
	v_pk_add_f32 v[120:121], v[120:121], v[120:121] op_sel_hi:[0,1]
	v_pk_fma_f32 v[124:125], v[68:69], v[68:69], v[118:119] op_sel_hi:[1,1,0]
	v_mul_f32_e32 v122, v94, v94
	v_mul_f32_e32 v124, v95, v95
	v_mul_f32_e32 v120, v96, v96
	v_mul_f32_e32 v118, v97, v97
	v_pk_add_f32 v[122:123], v[122:123], v[124:125]
	v_pk_add_f32 v[118:119], v[120:121], v[118:119]
	v_pk_mul_f32 v[120:121], v[92:93], v[92:93]
	v_pk_add_f32 v[118:119], v[122:123], v[118:119]
	v_pk_mul_f32 v[122:123], v[90:91], v[90:91]
	v_pk_add_f32 v[118:119], v[118:119], v[118:119] op_sel_hi:[0,1]
	v_pk_mov_b32 v[124:125], v[122:123], v[120:121] op_sel:[1,0]
	v_mov_b32_e32 v123, v121
	v_mul_f32_e32 v118, v86, v86
	v_pk_add_f32 v[120:121], v[124:125], v[122:123]
	v_pk_fma_f32 v[122:123], v[86:87], v[86:87], v[118:119] op_sel_hi:[1,1,0]
	v_mul_f32_e32 v118, v88, v88
	v_pk_add_f32 v[120:121], v[120:121], v[120:121] op_sel_hi:[0,1]
	v_pk_fma_f32 v[124:125], v[88:89], v[88:89], v[118:119] op_sel_hi:[1,1,0]
	v_mul_f32_e32 v122, v82, v82
	v_mul_f32_e32 v124, v83, v83
	v_mul_f32_e32 v120, v84, v84
	v_mul_f32_e32 v118, v85, v85
	v_pk_add_f32 v[122:123], v[122:123], v[124:125]
	v_pk_add_f32 v[118:119], v[120:121], v[118:119]
	s_nop 0
	v_pk_add_f32 v[118:119], v[122:123], v[118:119]
	s_nop 0
	v_add_f32_e32 v117, v118, v119
	s_nop 1
	v_add_f32_dpp v117, v117, v117 quad_perm:[1,0,3,2] row_mask:0xf bank_mask:0xf bound_ctrl:1
	s_nop 1
	v_add_f32_dpp v117, v117, v117 quad_perm:[2,3,0,1] row_mask:0xf bank_mask:0xf bound_ctrl:1
	s_nop 1
	v_add_f32_dpp v117, v117, v117 row_half_mirror row_mask:0xf bank_mask:0xf bound_ctrl:1
	s_nop 1
	v_add_f32_dpp v117, v117, v117 row_mirror row_mask:0xf bank_mask:0xf bound_ctrl:1
	s_nop 0
	v_readlane_b32 s5, v117, 16
	v_readlane_b32 s6, v117, 48
	v_readlane_b32 s0, v117, 0
	v_readlane_b32 s1, v117, 32
	v_mov_b32_e32 v118, s5
	v_mov_b32_e32 v119, s6
	v_pk_add_f32 v[118:119], s[0:1], v[118:119]
	s_ashr_i32 s5, s4, 31
	v_add_f32_e32 v117, v118, v119
	v_fmamk_f32 v117, v117, 0x3a000000, v114
	v_mul_f32_e32 v118, 0x4f800000, v117
	v_cmp_gt_f32_e32 vcc, s9, v117
	s_nop 1
	v_cndmask_b32_e32 v117, v117, v118, vcc
	v_sqrt_f32_e32 v118, v117
	s_nop 0
	v_add_u32_e32 v119, -1, v118
	v_fma_f32 v120, -v119, v118, v117
	v_cmp_ge_f32_e64 s[0:1], 0, v120
	v_add_u32_e32 v120, 1, v118
	s_nop 0
	v_cndmask_b32_e64 v119, v118, v119, s[0:1]
	v_fma_f32 v118, -v120, v118, v117
	v_cmp_lt_f32_e64 s[0:1], 0, v118
	s_nop 1
	v_cndmask_b32_e64 v118, v119, v120, s[0:1]
	v_mul_f32_e32 v119, 0x37800000, v118
	v_cndmask_b32_e32 v118, v118, v119, vcc
	v_cmp_class_f32_e32 vcc, v117, v115
	s_nop 1
	v_cndmask_b32_e32 v117, v118, v117, vcc
	v_div_scale_f32 v118, s[0:1], v117, v117, 1.0
	v_rcp_f32_e32 v119, v118
	s_nop 0
	v_fma_f32 v120, -v118, v119, 1.0
	v_fmac_f32_e32 v119, v120, v119
	v_div_scale_f32 v120, vcc, 1.0, v117, 1.0
	v_mul_f32_e32 v121, v120, v119
	v_fma_f32 v122, -v118, v121, v120
	v_fmac_f32_e32 v121, v122, v119
	v_fma_f32 v118, -v118, v121, v120
	v_div_fmas_f32 v118, v118, v119, v121
	v_div_fixup_f32 v118, v118, v117, 1.0
	v_pk_mul_f32 v[126:127], v[76:77], v[118:119] op_sel_hi:[1,0]
	v_pk_mul_f32 v[124:125], v[74:75], v[118:119] op_sel_hi:[1,0]
	v_pk_mul_f32 v[126:127], v[8:9], v[126:127]
	v_pk_mul_f32 v[120:121], v[78:79], v[118:119] op_sel_hi:[1,0]
	v_pk_mul_f32 v[122:123], v[80:81], v[118:119] op_sel_hi:[1,0]
	v_pk_mul_f32 v[124:125], v[6:7], v[124:125]
	v_max_f32_e64 v119, |v126|, |v127|
	v_pk_mul_f32 v[122:123], v[4:5], v[122:123]
	v_max3_f32 v119, |v124|, |v125|, v119
	v_pk_mul_f32 v[120:121], v[2:3], v[120:121]
	v_max_f32_e64 v117, |v122|, |v123|
	v_pk_mul_f32 v[130:131], v[72:73], v[118:119] op_sel_hi:[1,0]
	v_max3_f32 v117, |v120|, |v121|, v117
	v_pk_mul_f32 v[128:129], v[70:71], v[118:119] op_sel_hi:[1,0]
	v_pk_mul_f32 v[130:131], v[12:13], v[130:131]
	v_max3_f32 v117, v117, 0, v119
	v_pk_mul_f32 v[128:129], v[10:11], v[128:129]
	v_max_f32_e64 v119, |v130|, |v131|
	v_max3_f32 v119, |v128|, |v129|, v119
	v_pk_mul_f32 v[134:135], v[68:69], v[118:119] op_sel_hi:[1,0]
	v_pk_mul_f32 v[132:133], v[66:67], v[118:119] op_sel_hi:[1,0]
	v_pk_mul_f32 v[134:135], v[16:17], v[134:135]
	v_pk_mul_f32 v[132:133], v[14:15], v[132:133]
	v_max_f32_e64 v136, |v134|, |v135|
	v_max3_f32 v136, |v132|, |v133|, v136
	v_pk_mul_f32 v[138:139], v[96:97], v[118:119] op_sel_hi:[1,0]
	v_max3_f32 v117, v117, v119, v136
	v_pk_mul_f32 v[136:137], v[94:95], v[118:119] op_sel_hi:[1,0]
	v_pk_mul_f32 v[138:139], v[20:21], v[138:139]
	v_pk_mul_f32 v[136:137], v[18:19], v[136:137]
	v_max_f32_e64 v119, |v138|, |v139|
	v_max3_f32 v119, |v136|, |v137|, v119
	v_pk_mul_f32 v[142:143], v[92:93], v[118:119] op_sel_hi:[1,0]
	v_pk_mul_f32 v[140:141], v[90:91], v[118:119] op_sel_hi:[1,0]
	v_pk_mul_f32 v[142:143], v[24:25], v[142:143]
	v_pk_mul_f32 v[140:141], v[22:23], v[140:141]
	v_max_f32_e64 v144, |v142|, |v143|
	v_max3_f32 v144, |v140|, |v141|, v144
	v_pk_mul_f32 v[146:147], v[88:89], v[118:119] op_sel_hi:[1,0]
	v_max3_f32 v117, v117, v119, v144
	v_pk_mul_f32 v[144:145], v[86:87], v[118:119] op_sel_hi:[1,0]
	v_pk_mul_f32 v[146:147], v[28:29], v[146:147]
	v_pk_mul_f32 v[144:145], v[26:27], v[144:145]
	v_max_f32_e64 v119, |v146|, |v147|
	v_max3_f32 v150, |v144|, |v145|, v119
	v_pk_mul_f32 v[148:149], v[82:83], v[118:119] op_sel_hi:[1,0]
	v_pk_mul_f32 v[118:119], v[84:85], v[118:119] op_sel_hi:[1,0]
	v_pk_mul_f32 v[148:149], v[30:31], v[148:149]
	v_pk_mul_f32 v[118:119], v[32:33], v[118:119]
	s_nop 0
	v_max_f32_e64 v151, |v118|, |v119|
	v_max3_f32 v151, |v148|, |v149|, v151
	v_max3_f32 v117, v117, v150, v151
	s_nop 1
	v_mov_b32_dpp v150, v117 quad_perm:[1,0,3,2] row_mask:0xf bank_mask:0xf bound_ctrl:1
	v_max_f32_e32 v150, v150, v150
	v_max_f32_e32 v117, v117, v150
	s_nop 1
	v_mov_b32_dpp v150, v117 quad_perm:[2,3,0,1] row_mask:0xf bank_mask:0xf bound_ctrl:1
	v_max_f32_e32 v150, v150, v150
	v_max_f32_e32 v117, v117, v150
	s_nop 1
	v_mov_b32_dpp v150, v117 row_half_mirror row_mask:0xf bank_mask:0xf bound_ctrl:1
	v_max_f32_e32 v150, v150, v150
	v_max_f32_e32 v117, v117, v150
	s_nop 1
	v_mov_b32_dpp v150, v117 row_mirror row_mask:0xf bank_mask:0xf bound_ctrl:1
	v_max_f32_e32 v150, v150, v150
	v_max_f32_e32 v117, v117, v150
	s_nop 0
	v_readlane_b32 s0, v117, 0
	v_readlane_b32 s1, v117, 16
	s_nop 0
	v_max_f32_e64 v151, s0, s0
	v_max_f32_e64 v150, s1, s1
	v_readlane_b32 s0, v117, 32
	v_readlane_b32 s1, v117, 48
	v_max_f32_e32 v150, v151, v150
	v_max_f32_e64 v151, s0, s0
	v_max_f32_e64 v117, s1, s1
	v_max_f32_e32 v117, v151, v117
	v_max3_f32 v117, v150, v117, s10
	v_div_scale_f32 v150, s[0:1], v117, v117, s11
	v_rcp_f32_e32 v151, v150
	s_lshl_b64 s[0:1], s[4:5], 11
	v_fma_f32 v152, -v150, v151, 1.0
	v_fmac_f32_e32 v151, v152, v151
	v_div_scale_f32 v152, vcc, s11, v117, s11
	v_mul_f32_e32 v153, v152, v151
	v_fma_f32 v154, -v150, v153, v152
	v_fmac_f32_e32 v153, v154, v151
	v_fma_f32 v150, -v150, v153, v152
	v_div_fmas_f32 v150, v150, v151, v153
	v_div_fixup_f32 v150, v150, v117, s11
	v_mul_f32_e32 v120, v120, v150
	v_rndne_f32_e32 v120, v120
	v_mul_f32_e32 v121, v121, v150
	v_rndne_f32_e32 v121, v121
	v_mul_f32_e32 v122, v122, v150
	v_med3_f32 v120, v120, s14, v116
	v_rndne_f32_e32 v122, v122
	v_mul_f32_e32 v123, v123, v150
	v_med3_f32 v121, v121, s14, v116
	v_add_f32_e32 v120, 0x43000000, v120
	v_rndne_f32_e32 v123, v123
	v_med3_f32 v122, v122, s14, v116
	v_cvt_i32_f32_e32 v151, v120
	v_add_f32_e32 v120, 0x43000000, v121
	v_med3_f32 v123, v123, s14, v116
	v_cvt_i32_f32_e32 v152, v120
	v_add_f32_e32 v120, 0x43000000, v122
	v_cvt_i32_f32_sdwa v122, v120 dst_sel:WORD_1 dst_unused:UNUSED_PAD src0_sel:DWORD
	v_add_f32_e32 v120, 0x43000000, v123
	v_cvt_i32_f32_sdwa v123, v120 dst_sel:BYTE_3 dst_unused:UNUSED_PAD src0_sel:DWORD
	v_lshlrev_b32_e32 v152, 8, v152
	v_or3_b32 v122, v152, v151, v122
	v_lshl_add_u64 v[120:121], v[102:103], 0, s[0:1]
	v_bitop3_b32 v122, v122, s15, v123 bitop3:0x36
	v_mul_f32_e32 v123, v124, v150
	v_mul_f32_e32 v124, v125, v150
	v_rndne_f32_e32 v124, v124
	v_mul_f32_e32 v125, v126, v150
	v_rndne_f32_e32 v123, v123
	v_rndne_f32_e32 v125, v125
	v_med3_f32 v124, v124, s14, v116
	v_med3_f32 v123, v123, s14, v116
	v_med3_f32 v125, v125, s14, v116
	v_add_f32_e32 v124, 0x43000000, v124
	v_add_f32_e32 v123, 0x43000000, v123
	v_cvt_i32_f32_e32 v124, v124
	v_add_f32_e32 v125, 0x43000000, v125
	v_cvt_i32_f32_e32 v123, v123
	v_cvt_i32_f32_sdwa v125, v125 dst_sel:WORD_1 dst_unused:UNUSED_PAD src0_sel:DWORD
	v_mul_f32_e32 v126, v127, v150
	v_rndne_f32_e32 v126, v126
	global_store_dword v[120:121], v122, off
	v_lshlrev_b32_e32 v122, 8, v124
	v_mul_f32_e32 v124, v129, v150
	v_med3_f32 v126, v126, s14, v116
	v_or3_b32 v122, v122, v123, v125
	v_mul_f32_e32 v123, v128, v150
	v_rndne_f32_e32 v124, v124
	v_mul_f32_e32 v125, v130, v150
	v_add_f32_e32 v126, 0x43000000, v126
	v_rndne_f32_e32 v123, v123
	v_rndne_f32_e32 v125, v125
	v_med3_f32 v124, v124, s14, v116
	v_cvt_i32_f32_sdwa v126, v126 dst_sel:BYTE_3 dst_unused:UNUSED_PAD src0_sel:DWORD
	v_med3_f32 v123, v123, s14, v116
	v_med3_f32 v125, v125, s14, v116
	v_add_f32_e32 v124, 0x43000000, v124
	v_add_f32_e32 v123, 0x43000000, v123
	v_cvt_i32_f32_e32 v124, v124
	v_add_f32_e32 v125, 0x43000000, v125
	v_cvt_i32_f32_e32 v123, v123
	v_cvt_i32_f32_sdwa v125, v125 dst_sel:WORD_1 dst_unused:UNUSED_PAD src0_sel:DWORD
	v_bitop3_b32 v122, v122, s15, v126 bitop3:0x36
	v_mul_f32_e32 v126, v131, v150
	v_rndne_f32_e32 v126, v126
	global_store_dword v[120:121], v122, off offset:256
	v_lshlrev_b32_e32 v122, 8, v124
	v_mul_f32_e32 v124, v133, v150
	v_med3_f32 v126, v126, s14, v116
	v_or3_b32 v122, v122, v123, v125
	v_mul_f32_e32 v123, v132, v150
	v_rndne_f32_e32 v124, v124
	v_mul_f32_e32 v125, v134, v150
	v_add_f32_e32 v126, 0x43000000, v126
	v_rndne_f32_e32 v123, v123
	v_rndne_f32_e32 v125, v125
	v_med3_f32 v124, v124, s14, v116
	v_cvt_i32_f32_sdwa v126, v126 dst_sel:BYTE_3 dst_unused:UNUSED_PAD src0_sel:DWORD
	v_med3_f32 v123, v123, s14, v116
	v_med3_f32 v125, v125, s14, v116
	v_add_f32_e32 v124, 0x43000000, v124
	v_add_f32_e32 v123, 0x43000000, v123
	v_cvt_i32_f32_e32 v124, v124
	v_add_f32_e32 v125, 0x43000000, v125
	v_cvt_i32_f32_e32 v123, v123
	v_cvt_i32_f32_sdwa v125, v125 dst_sel:WORD_1 dst_unused:UNUSED_PAD src0_sel:DWORD
	v_bitop3_b32 v122, v122, s15, v126 bitop3:0x36
	v_mul_f32_e32 v126, v135, v150
	v_rndne_f32_e32 v126, v126
	global_store_dword v[120:121], v122, off offset:512
	v_lshlrev_b32_e32 v122, 8, v124
	v_mul_f32_e32 v124, v137, v150
	v_med3_f32 v126, v126, s14, v116
	v_or3_b32 v122, v122, v123, v125
	v_mul_f32_e32 v123, v136, v150
	v_rndne_f32_e32 v124, v124
	v_mul_f32_e32 v125, v138, v150
	v_add_f32_e32 v126, 0x43000000, v126
	v_rndne_f32_e32 v123, v123
	v_rndne_f32_e32 v125, v125
	v_med3_f32 v124, v124, s14, v116
	v_cvt_i32_f32_sdwa v126, v126 dst_sel:BYTE_3 dst_unused:UNUSED_PAD src0_sel:DWORD
	v_med3_f32 v123, v123, s14, v116
	v_med3_f32 v125, v125, s14, v116
	v_add_f32_e32 v124, 0x43000000, v124
	v_add_f32_e32 v123, 0x43000000, v123
	v_cvt_i32_f32_e32 v124, v124
	v_add_f32_e32 v125, 0x43000000, v125
	v_cvt_i32_f32_e32 v123, v123
	v_cvt_i32_f32_sdwa v125, v125 dst_sel:WORD_1 dst_unused:UNUSED_PAD src0_sel:DWORD
	v_bitop3_b32 v122, v122, s15, v126 bitop3:0x36
	v_mul_f32_e32 v126, v139, v150
	v_rndne_f32_e32 v126, v126
	global_store_dword v[120:121], v122, off offset:768
	v_lshlrev_b32_e32 v122, 8, v124
	v_mul_f32_e32 v124, v141, v150
	v_med3_f32 v126, v126, s14, v116
	v_or3_b32 v122, v122, v123, v125
	v_mul_f32_e32 v123, v140, v150
	v_rndne_f32_e32 v124, v124
	v_mul_f32_e32 v125, v142, v150
	v_add_f32_e32 v126, 0x43000000, v126
	v_rndne_f32_e32 v123, v123
	v_rndne_f32_e32 v125, v125
	v_med3_f32 v124, v124, s14, v116
	v_cvt_i32_f32_sdwa v126, v126 dst_sel:BYTE_3 dst_unused:UNUSED_PAD src0_sel:DWORD
	v_med3_f32 v123, v123, s14, v116
	v_med3_f32 v125, v125, s14, v116
	v_add_f32_e32 v124, 0x43000000, v124
	v_add_f32_e32 v123, 0x43000000, v123
	v_cvt_i32_f32_e32 v124, v124
	v_add_f32_e32 v125, 0x43000000, v125
	v_cvt_i32_f32_e32 v123, v123
	v_cvt_i32_f32_sdwa v125, v125 dst_sel:WORD_1 dst_unused:UNUSED_PAD src0_sel:DWORD
	v_bitop3_b32 v122, v122, s15, v126 bitop3:0x36
	v_mul_f32_e32 v126, v143, v150
	v_rndne_f32_e32 v126, v126
	global_store_dword v[120:121], v122, off offset:1024
	v_lshlrev_b32_e32 v122, 8, v124
	v_mul_f32_e32 v124, v145, v150
	v_med3_f32 v126, v126, s14, v116
	v_or3_b32 v122, v122, v123, v125
	v_mul_f32_e32 v123, v144, v150
	v_rndne_f32_e32 v124, v124
	v_mul_f32_e32 v125, v146, v150
	v_add_f32_e32 v126, 0x43000000, v126
	v_rndne_f32_e32 v123, v123
	v_rndne_f32_e32 v125, v125
	v_med3_f32 v124, v124, s14, v116
	v_cvt_i32_f32_sdwa v126, v126 dst_sel:BYTE_3 dst_unused:UNUSED_PAD src0_sel:DWORD
	v_med3_f32 v123, v123, s14, v116
	v_med3_f32 v125, v125, s14, v116
	v_add_f32_e32 v124, 0x43000000, v124
	v_add_f32_e32 v123, 0x43000000, v123
	v_cvt_i32_f32_e32 v124, v124
	v_add_f32_e32 v125, 0x43000000, v125
	v_cvt_i32_f32_e32 v123, v123
	v_cvt_i32_f32_sdwa v125, v125 dst_sel:WORD_1 dst_unused:UNUSED_PAD src0_sel:DWORD
	v_bitop3_b32 v122, v122, s15, v126 bitop3:0x36
	v_mul_f32_e32 v126, v147, v150
	v_rndne_f32_e32 v126, v126
	global_store_dword v[120:121], v122, off offset:1280
	v_lshlrev_b32_e32 v122, 8, v124
	v_mul_f32_e32 v124, v149, v150
	v_med3_f32 v126, v126, s14, v116
	v_or3_b32 v122, v122, v123, v125
	v_mul_f32_e32 v123, v148, v150
	v_rndne_f32_e32 v124, v124
	v_mul_f32_e32 v118, v118, v150
	v_add_f32_e32 v126, 0x43000000, v126
	v_rndne_f32_e32 v123, v123
	v_rndne_f32_e32 v118, v118
	v_mul_f32_e32 v119, v119, v150
	v_med3_f32 v124, v124, s14, v116
	v_cvt_i32_f32_sdwa v126, v126 dst_sel:BYTE_3 dst_unused:UNUSED_PAD src0_sel:DWORD
	v_rndne_f32_e32 v119, v119
	v_med3_f32 v123, v123, s14, v116
	v_med3_f32 v118, v118, s14, v116
	v_add_f32_e32 v124, 0x43000000, v124
	v_med3_f32 v119, v119, s14, v116
	v_add_f32_e32 v123, 0x43000000, v123
	v_cvt_i32_f32_e32 v124, v124
	v_add_f32_e32 v118, 0x43000000, v118
	v_cvt_i32_f32_e32 v123, v123
	v_cvt_i32_f32_sdwa v118, v118 dst_sel:WORD_1 dst_unused:UNUSED_PAD src0_sel:DWORD
	v_add_f32_e32 v119, 0x43000000, v119
	v_cvt_i32_f32_sdwa v119, v119 dst_sel:BYTE_3 dst_unused:UNUSED_PAD src0_sel:DWORD
	v_bitop3_b32 v122, v122, s15, v126 bitop3:0x36
	global_store_dword v[120:121], v122, off offset:1536
	v_lshlrev_b32_e32 v122, 8, v124
	v_or3_b32 v118, v122, v123, v118
	v_bitop3_b32 v118, v118, s15, v119 bitop3:0x36
	global_store_dword v[120:121], v118, off offset:1792
	s_and_saveexec_b64 s[0:1], s[2:3]
	s_cbranch_execz .LBB0_438
	s_lshl_b64 s[6:7], s[4:5], 2
	s_add_u32 s6, s38, s6
	s_addc_u32 s7, s39, s7
	v_mul_f32_e32 v117, 0x3c010204, v117
	global_store_dword v99, v117, s[6:7]
	s_branch .LBB0_438

.LBB0_456:
	s_add_i32 s4, s10, s18
	s_cmpk_gt_i32 s4, 0x3fff
	s_cbranch_scc1 .LBB0_458
	s_ashr_i32 s5, s4, 31
	s_lshl_b64 s[0:1], s[4:5], 13
	v_lshl_add_u64 v[82:83], v[100:101], 0, s[0:1]
	global_load_dwordx4 v[78:81], v[82:83], off
	global_load_dwordx4 v[74:77], v[82:83], off offset:1024
	global_load_dwordx4 v[70:73], v[82:83], off offset:2048
	global_load_dwordx4 v[66:69], v[82:83], off offset:3072
	v_add_co_u32_e32 v82, vcc, 0x1000, v82
	s_nop 1
	v_addc_co_u32_e32 v83, vcc, 0, v83, vcc
	global_load_dwordx4 v[94:97], v[82:83], off
	global_load_dwordx4 v[90:93], v[82:83], off offset:1024
	global_load_dwordx4 v[86:89], v[82:83], off offset:2048
	s_nop 0
	global_load_dwordx4 v[82:85], v[82:83], off offset:3072
	s_waitcnt vmcnt(15)
	v_pk_mul_f32 v[118:119], v[34:35], v[34:35]
	s_waitcnt vmcnt(14)
	v_pk_mul_f32 v[120:121], v[38:39], v[38:39]
	v_pk_mul_f32 v[114:115], v[36:37], v[36:37]
	v_pk_mul_f32 v[116:117], v[40:41], v[40:41]
	v_mov_b32_e32 v122, v118
	v_mov_b32_e32 v123, v120
	v_mov_b32_e32 v120, v119
	s_waitcnt vmcnt(13)
	v_pk_mul_f32 v[110:111], v[44:45], v[44:45]
	v_pk_mul_f32 v[112:113], v[42:43], v[42:43]
	v_pk_add_f32 v[118:119], v[122:123], v[120:121]
	v_mov_b32_e32 v120, v114
	v_mov_b32_e32 v121, v116
	v_mov_b32_e32 v116, v115
	v_pk_add_f32 v[114:115], v[120:121], v[116:117]
	v_pk_mov_b32 v[116:117], v[112:113], v[110:111] op_sel:[1,0]
	v_mov_b32_e32 v113, v111
	v_pk_add_f32 v[110:111], v[116:117], v[112:113]
	v_pk_add_f32 v[114:115], v[118:119], v[114:115]
	v_pk_add_f32 v[110:111], v[110:111], v[110:111] op_sel_hi:[0,1]
	s_waitcnt vmcnt(12)
	v_mul_f32_e32 v110, v46, v46
	v_pk_fma_f32 v[112:113], v[46:47], v[46:47], v[110:111] op_sel_hi:[1,1,0]
	v_mul_f32_e32 v110, v48, v48
	v_pk_add_f32 v[114:115], v[114:115], v[114:115] op_sel_hi:[0,1]
	v_pk_fma_f32 v[116:117], v[48:49], v[48:49], v[110:111] op_sel_hi:[1,1,0]
	s_waitcnt vmcnt(11)
	v_mul_f32_e32 v112, v50, v50
	v_mul_f32_e32 v116, v51, v51
	v_mul_f32_e32 v110, v52, v52
	v_mul_f32_e32 v114, v53, v53
	s_waitcnt vmcnt(10)
	v_pk_mul_f32 v[106:107], v[56:57], v[56:57]
	v_pk_mul_f32 v[108:109], v[54:55], v[54:55]
	v_pk_add_f32 v[112:113], v[112:113], v[116:117]
	v_pk_add_f32 v[110:111], v[110:111], v[114:115]
	s_nop 0
	v_pk_add_f32 v[110:111], v[112:113], v[110:111]
	v_pk_mov_b32 v[112:113], v[108:109], v[106:107] op_sel:[1,0]
	v_mov_b32_e32 v109, v107
	v_pk_add_f32 v[106:107], v[112:113], v[108:109]
	v_pk_add_f32 v[110:111], v[110:111], v[110:111] op_sel_hi:[0,1]
	v_pk_add_f32 v[106:107], v[106:107], v[106:107] op_sel_hi:[0,1]
	s_waitcnt vmcnt(9)
	v_mul_f32_e32 v106, v58, v58
	v_pk_fma_f32 v[108:109], v[58:59], v[58:59], v[106:107] op_sel_hi:[1,1,0]
	v_mul_f32_e32 v106, v60, v60
	v_pk_fma_f32 v[112:113], v[60:61], v[60:61], v[106:107] op_sel_hi:[1,1,0]
	s_waitcnt vmcnt(8)
	s_branch .Lrms_lad_a1

.Lrms_lad_a1:
	v_mul_f32_e32 v108, v62, v62
	v_mul_f32_e32 v112, v63, v63
	v_mul_f32_e32 v106, v64, v64
	v_mul_f32_e32 v110, v65, v65
	v_pk_add_f32 v[108:109], v[108:109], v[112:113]
	v_pk_add_f32 v[106:107], v[106:107], v[110:111]
	s_nop 0
	v_pk_add_f32 v[106:107], v[108:109], v[106:107]
	s_nop 0
	v_add_f32_e32 v106, v106, v107
	s_nop 1
	v_add_f32_dpp v106, v106, v106 quad_perm:[1,0,3,2] row_mask:0xf bank_mask:0xf bound_ctrl:1
	s_nop 1
	v_add_f32_dpp v106, v106, v106 quad_perm:[2,3,0,1] row_mask:0xf bank_mask:0xf bound_ctrl:1
	s_nop 1
	v_add_f32_dpp v106, v106, v106 row_half_mirror row_mask:0xf bank_mask:0xf bound_ctrl:1
	s_nop 1
	v_add_f32_dpp v106, v106, v106 row_mirror row_mask:0xf bank_mask:0xf bound_ctrl:1
	s_nop 0
	v_readlane_b32 s5, v106, 16
	v_readlane_b32 s6, v106, 48
	v_readlane_b32 s0, v106, 0
	v_readlane_b32 s1, v106, 32
	v_mov_b32_e32 v106, s5
	v_mov_b32_e32 v107, s6
	v_pk_add_f32 v[106:107], s[0:1], v[106:107]
	s_nop 0
	v_add_f32_e32 v106, v106, v107
	v_fmamk_f32 v106, v106, 0x3a000000, v98
	v_mul_f32_e32 v107, 0x4f800000, v106
	v_cmp_gt_f32_e32 vcc, s11, v106
	s_nop 1
	v_cndmask_b32_e32 v106, v106, v107, vcc
	v_sqrt_f32_e32 v107, v106
	s_nop 0
	v_add_u32_e32 v108, -1, v107
	v_fma_f32 v109, -v108, v107, v106
	v_cmp_ge_f32_e64 s[0:1], 0, v109
	v_add_u32_e32 v109, 1, v107
	s_nop 0
	v_cndmask_b32_e64 v108, v107, v108, s[0:1]
	v_fma_f32 v107, -v109, v107, v106
	v_cmp_lt_f32_e64 s[0:1], 0, v107
	s_nop 1
	v_cndmask_b32_e64 v107, v108, v109, s[0:1]
	v_mul_f32_e32 v108, 0x37800000, v107
	v_cndmask_b32_e32 v107, v107, v108, vcc
	v_cmp_class_f32_e32 vcc, v106, v104
	s_nop 1
	v_cndmask_b32_e32 v106, v107, v106, vcc
	v_div_scale_f32 v107, s[0:1], v106, v106, 1.0
	v_rcp_f32_e32 v108, v107
	s_nop 0
	v_fma_f32 v109, -v107, v108, 1.0
	v_fmac_f32_e32 v108, v109, v108
	v_div_scale_f32 v109, vcc, 1.0, v106, 1.0
	v_mul_f32_e32 v110, v109, v108
	v_fma_f32 v111, -v107, v110, v109
	v_fmac_f32_e32 v110, v111, v108
	v_fma_f32 v107, -v107, v110, v109
	v_div_fmas_f32 v107, v107, v108, v110
	v_div_fixup_f32 v106, v107, v106, 1.0
	v_pk_mul_f32 v[110:111], v[36:37], v[106:107] op_sel_hi:[1,0]
	v_pk_mul_f32 v[108:109], v[34:35], v[106:107] op_sel_hi:[1,0]
	v_pk_mul_f32 v[110:111], v[4:5], v[110:111]
	v_pk_mul_f32 v[108:109], v[2:3], v[108:109]
	v_max_f32_e64 v107, |v110|, |v111|
	v_max3_f32 v107, |v108|, |v109|, v107
	v_pk_mul_f32 v[114:115], v[40:41], v[106:107] op_sel_hi:[1,0]
	v_pk_mul_f32 v[112:113], v[38:39], v[106:107] op_sel_hi:[1,0]
	v_pk_mul_f32 v[114:115], v[8:9], v[114:115]
	v_pk_mul_f32 v[112:113], v[6:7], v[112:113]
	v_max_f32_e64 v116, |v114|, |v115|
	v_max3_f32 v116, |v112|, |v113|, v116
	v_max3_f32 v107, v107, 0, v116
	v_pk_mul_f32 v[118:119], v[44:45], v[106:107] op_sel_hi:[1,0]
	v_pk_mul_f32 v[116:117], v[42:43], v[106:107] op_sel_hi:[1,0]
	v_pk_mul_f32 v[118:119], v[12:13], v[118:119]
	v_pk_mul_f32 v[116:117], v[10:11], v[116:117]
	v_max_f32_e64 v120, |v118|, |v119|
	v_pk_mul_f32 v[122:123], v[48:49], v[106:107] op_sel_hi:[1,0]
	v_max3_f32 v124, |v116|, |v117|, v120
	v_pk_mul_f32 v[120:121], v[46:47], v[106:107] op_sel_hi:[1,0]
	v_pk_mul_f32 v[122:123], v[16:17], v[122:123]
	v_pk_mul_f32 v[120:121], v[14:15], v[120:121]
	v_max_f32_e64 v125, |v122|, |v123|
	v_max3_f32 v125, |v120|, |v121|, v125
	v_max3_f32 v107, v107, v124, v125
	v_pk_mul_f32 v[126:127], v[52:53], v[106:107] op_sel_hi:[1,0]
	v_pk_mul_f32 v[124:125], v[50:51], v[106:107] op_sel_hi:[1,0]
	v_pk_mul_f32 v[126:127], v[20:21], v[126:127]
	v_pk_mul_f32 v[124:125], v[18:19], v[124:125]
	v_max_f32_e64 v128, |v126|, |v127|
	v_pk_mul_f32 v[130:131], v[56:57], v[106:107] op_sel_hi:[1,0]
	v_max3_f32 v132, |v124|, |v125|, v128
	v_pk_mul_f32 v[128:129], v[54:55], v[106:107] op_sel_hi:[1,0]
	v_pk_mul_f32 v[130:131], v[24:25], v[130:131]
	v_pk_mul_f32 v[128:129], v[22:23], v[128:129]
	v_max_f32_e64 v133, |v130|, |v131|
	v_max3_f32 v133, |v128|, |v129|, v133
	v_pk_mul_f32 v[134:135], v[60:61], v[106:107] op_sel_hi:[1,0]
	v_max3_f32 v140, v107, v132, v133
	v_pk_mul_f32 v[132:133], v[58:59], v[106:107] op_sel_hi:[1,0]
	v_pk_mul_f32 v[134:135], v[28:29], v[134:135]
	v_pk_mul_f32 v[132:133], v[26:27], v[132:133]
	v_max_f32_e64 v107, |v134|, |v135|
	v_max3_f32 v141, |v132|, |v133|, v107
	v_pk_mul_f32 v[136:137], v[62:63], v[106:107] op_sel_hi:[1,0]
	v_pk_mul_f32 v[106:107], v[64:65], v[106:107] op_sel_hi:[1,0]
	v_pk_mul_f32 v[136:137], v[30:31], v[136:137]
	v_pk_mul_f32 v[138:139], v[32:33], v[106:107]
	s_nop 0
	v_max_f32_e64 v106, |v138|, |v139|
	v_max3_f32 v106, |v136|, |v137|, v106
	v_max3_f32 v106, v140, v141, v106
	s_nop 1
	v_mov_b32_dpp v107, v106 quad_perm:[1,0,3,2] row_mask:0xf bank_mask:0xf bound_ctrl:1
	v_max_f32_e32 v107, v107, v107
	v_max_f32_e32 v106, v106, v107
	s_nop 1
	v_mov_b32_dpp v107, v106 quad_perm:[2,3,0,1] row_mask:0xf bank_mask:0xf bound_ctrl:1
	v_max_f32_e32 v107, v107, v107
	v_max_f32_e32 v106, v106, v107
	s_nop 1
	v_mov_b32_dpp v107, v106 row_half_mirror row_mask:0xf bank_mask:0xf bound_ctrl:1
	v_max_f32_e32 v107, v107, v107
	v_max_f32_e32 v106, v106, v107
	s_nop 1
	v_mov_b32_dpp v107, v106 row_mirror row_mask:0xf bank_mask:0xf bound_ctrl:1
	v_max_f32_e32 v107, v107, v107
	v_max_f32_e32 v106, v106, v107
	s_nop 0
	v_readlane_b32 s0, v106, 0
	v_readlane_b32 s1, v106, 16
	s_nop 0
	v_max_f32_e64 v140, s0, s0
	v_max_f32_e64 v107, s1, s1
	v_readlane_b32 s0, v106, 32
	v_readlane_b32 s1, v106, 48
	v_max_f32_e32 v107, v140, v107
	v_max_f32_e64 v140, s0, s0
	v_max_f32_e64 v106, s1, s1
	v_max_f32_e32 v106, v140, v106
	v_max3_f32 v106, v107, v106, s14
	v_div_scale_f32 v107, s[0:1], v106, v106, s15
	v_rcp_f32_e32 v140, v107
	s_add_i32 s0, s18, 0xfffffe00
	s_ashr_i32 s1, s0, 31
	s_lshl_b64 s[6:7], s[0:1], 11
	v_fma_f32 v141, -v107, v140, 1.0
	v_fmac_f32_e32 v140, v141, v140
	v_div_scale_f32 v141, vcc, s15, v106, s15
	v_mul_f32_e32 v142, v141, v140
	v_fma_f32 v143, -v107, v142, v141
	v_fmac_f32_e32 v142, v143, v140
	v_fma_f32 v107, -v107, v142, v141
	v_div_fmas_f32 v107, v107, v140, v142
	v_div_fixup_f32 v107, v107, v106, s15
	v_mul_f32_e32 v108, v108, v107
	v_rndne_f32_e32 v108, v108
	v_mul_f32_e32 v109, v109, v107
	v_rndne_f32_e32 v109, v109
	v_mul_f32_e32 v110, v110, v107
	v_med3_f32 v108, v108, s16, v105
	v_rndne_f32_e32 v110, v110
	v_mul_f32_e32 v111, v111, v107
	v_med3_f32 v109, v109, s16, v105
	v_add_f32_e32 v108, 0x43000000, v108
	v_rndne_f32_e32 v111, v111
	v_med3_f32 v110, v110, s16, v105
	v_cvt_i32_f32_e32 v140, v108
	v_add_f32_e32 v108, 0x43000000, v109
	v_med3_f32 v111, v111, s16, v105
	v_cvt_i32_f32_e32 v141, v108
	v_add_f32_e32 v108, 0x43000000, v110
	v_cvt_i32_f32_sdwa v110, v108 dst_sel:WORD_1 dst_unused:UNUSED_PAD src0_sel:DWORD
	v_add_f32_e32 v108, 0x43000000, v111
	v_cvt_i32_f32_sdwa v111, v108 dst_sel:BYTE_3 dst_unused:UNUSED_PAD src0_sel:DWORD
	v_lshlrev_b32_e32 v141, 8, v141
	v_or3_b32 v110, v141, v140, v110
	v_lshl_add_u64 v[108:109], v[102:103], 0, s[6:7]
	v_bitop3_b32 v110, v110, s17, v111 bitop3:0x36
	v_mul_f32_e32 v111, v112, v107
	v_mul_f32_e32 v112, v113, v107
	v_rndne_f32_e32 v112, v112
	v_mul_f32_e32 v113, v114, v107
	v_rndne_f32_e32 v111, v111
	v_rndne_f32_e32 v113, v113
	v_med3_f32 v112, v112, s16, v105
	v_med3_f32 v111, v111, s16, v105
	v_med3_f32 v113, v113, s16, v105
	v_add_f32_e32 v112, 0x43000000, v112
	v_add_f32_e32 v111, 0x43000000, v111
	v_cvt_i32_f32_e32 v112, v112
	v_add_f32_e32 v113, 0x43000000, v113
	v_cvt_i32_f32_e32 v111, v111
	v_cvt_i32_f32_sdwa v113, v113 dst_sel:WORD_1 dst_unused:UNUSED_PAD src0_sel:DWORD
	v_mul_f32_e32 v114, v115, v107
	v_rndne_f32_e32 v114, v114
	global_store_dword v[108:109], v110, off
	v_lshlrev_b32_e32 v110, 8, v112
	v_mul_f32_e32 v112, v117, v107
	v_med3_f32 v114, v114, s16, v105
	v_or3_b32 v110, v110, v111, v113
	v_mul_f32_e32 v111, v116, v107
	v_rndne_f32_e32 v112, v112
	v_mul_f32_e32 v113, v118, v107
	v_add_f32_e32 v114, 0x43000000, v114
	v_rndne_f32_e32 v111, v111
	v_rndne_f32_e32 v113, v113
	v_med3_f32 v112, v112, s16, v105
	v_cvt_i32_f32_sdwa v114, v114 dst_sel:BYTE_3 dst_unused:UNUSED_PAD src0_sel:DWORD
	v_med3_f32 v111, v111, s16, v105
	v_med3_f32 v113, v113, s16, v105
	v_add_f32_e32 v112, 0x43000000, v112
	v_add_f32_e32 v111, 0x43000000, v111
	v_cvt_i32_f32_e32 v112, v112
	v_add_f32_e32 v113, 0x43000000, v113
	v_cvt_i32_f32_e32 v111, v111
	v_cvt_i32_f32_sdwa v113, v113 dst_sel:WORD_1 dst_unused:UNUSED_PAD src0_sel:DWORD
	v_bitop3_b32 v110, v110, s17, v114 bitop3:0x36
	v_mul_f32_e32 v114, v119, v107
	v_rndne_f32_e32 v114, v114
	global_store_dword v[108:109], v110, off offset:256
	v_lshlrev_b32_e32 v110, 8, v112
	v_mul_f32_e32 v112, v121, v107
	v_med3_f32 v114, v114, s16, v105
	v_or3_b32 v110, v110, v111, v113
	v_mul_f32_e32 v111, v120, v107
	v_rndne_f32_e32 v112, v112
	v_mul_f32_e32 v113, v122, v107
	v_add_f32_e32 v114, 0x43000000, v114
	v_rndne_f32_e32 v111, v111
	v_rndne_f32_e32 v113, v113
	v_med3_f32 v112, v112, s16, v105
	v_cvt_i32_f32_sdwa v114, v114 dst_sel:BYTE_3 dst_unused:UNUSED_PAD src0_sel:DWORD
	v_med3_f32 v111, v111, s16, v105
	v_med3_f32 v113, v113, s16, v105
	v_add_f32_e32 v112, 0x43000000, v112
	v_add_f32_e32 v111, 0x43000000, v111
	v_cvt_i32_f32_e32 v112, v112
	v_add_f32_e32 v113, 0x43000000, v113
	v_cvt_i32_f32_e32 v111, v111
	v_cvt_i32_f32_sdwa v113, v113 dst_sel:WORD_1 dst_unused:UNUSED_PAD src0_sel:DWORD
	v_bitop3_b32 v110, v110, s17, v114 bitop3:0x36
	v_mul_f32_e32 v114, v123, v107
	v_rndne_f32_e32 v114, v114
	global_store_dword v[108:109], v110, off offset:512
	v_lshlrev_b32_e32 v110, 8, v112
	v_mul_f32_e32 v112, v125, v107
	v_med3_f32 v114, v114, s16, v105
	v_or3_b32 v110, v110, v111, v113
	v_mul_f32_e32 v111, v124, v107
	v_rndne_f32_e32 v112, v112
	v_mul_f32_e32 v113, v126, v107
	v_add_f32_e32 v114, 0x43000000, v114
	v_rndne_f32_e32 v111, v111
	v_rndne_f32_e32 v113, v113
	v_med3_f32 v112, v112, s16, v105
	v_cvt_i32_f32_sdwa v114, v114 dst_sel:BYTE_3 dst_unused:UNUSED_PAD src0_sel:DWORD
	v_med3_f32 v111, v111, s16, v105
	v_med3_f32 v113, v113, s16, v105
	v_add_f32_e32 v112, 0x43000000, v112
	v_add_f32_e32 v111, 0x43000000, v111
	v_cvt_i32_f32_e32 v112, v112
	v_add_f32_e32 v113, 0x43000000, v113
	v_cvt_i32_f32_e32 v111, v111
	v_cvt_i32_f32_sdwa v113, v113 dst_sel:WORD_1 dst_unused:UNUSED_PAD src0_sel:DWORD
	v_bitop3_b32 v110, v110, s17, v114 bitop3:0x36
	v_mul_f32_e32 v114, v127, v107
	v_rndne_f32_e32 v114, v114
	global_store_dword v[108:109], v110, off offset:768
	v_lshlrev_b32_e32 v110, 8, v112
	v_mul_f32_e32 v112, v129, v107
	v_med3_f32 v114, v114, s16, v105
	v_or3_b32 v110, v110, v111, v113
	v_mul_f32_e32 v111, v128, v107
	v_rndne_f32_e32 v112, v112
	v_mul_f32_e32 v113, v130, v107
	v_add_f32_e32 v114, 0x43000000, v114
	v_rndne_f32_e32 v111, v111
	v_rndne_f32_e32 v113, v113
	v_med3_f32 v112, v112, s16, v105
	v_cvt_i32_f32_sdwa v114, v114 dst_sel:BYTE_3 dst_unused:UNUSED_PAD src0_sel:DWORD
	v_med3_f32 v111, v111, s16, v105
	v_med3_f32 v113, v113, s16, v105
	v_add_f32_e32 v112, 0x43000000, v112
	v_add_f32_e32 v111, 0x43000000, v111
	v_cvt_i32_f32_e32 v112, v112
	v_add_f32_e32 v113, 0x43000000, v113
	v_cvt_i32_f32_e32 v111, v111
	v_cvt_i32_f32_sdwa v113, v113 dst_sel:WORD_1 dst_unused:UNUSED_PAD src0_sel:DWORD
	v_bitop3_b32 v110, v110, s17, v114 bitop3:0x36
	v_mul_f32_e32 v114, v131, v107
	v_rndne_f32_e32 v114, v114
	global_store_dword v[108:109], v110, off offset:1024
	v_lshlrev_b32_e32 v110, 8, v112
	v_mul_f32_e32 v112, v133, v107
	v_med3_f32 v114, v114, s16, v105
	v_or3_b32 v110, v110, v111, v113
	v_mul_f32_e32 v111, v132, v107
	v_rndne_f32_e32 v112, v112
	v_mul_f32_e32 v113, v134, v107
	v_add_f32_e32 v114, 0x43000000, v114
	v_rndne_f32_e32 v111, v111
	v_rndne_f32_e32 v113, v113
	v_med3_f32 v112, v112, s16, v105
	v_cvt_i32_f32_sdwa v114, v114 dst_sel:BYTE_3 dst_unused:UNUSED_PAD src0_sel:DWORD
	v_med3_f32 v111, v111, s16, v105
	v_med3_f32 v113, v113, s16, v105
	v_add_f32_e32 v112, 0x43000000, v112
	v_add_f32_e32 v111, 0x43000000, v111
	v_cvt_i32_f32_e32 v112, v112
	v_add_f32_e32 v113, 0x43000000, v113
	v_cvt_i32_f32_e32 v111, v111
	v_cvt_i32_f32_sdwa v113, v113 dst_sel:WORD_1 dst_unused:UNUSED_PAD src0_sel:DWORD
	v_bitop3_b32 v110, v110, s17, v114 bitop3:0x36
	v_mul_f32_e32 v114, v135, v107
	v_rndne_f32_e32 v114, v114
	global_store_dword v[108:109], v110, off offset:1280
	v_lshlrev_b32_e32 v110, 8, v112
	v_mul_f32_e32 v112, v137, v107
	v_med3_f32 v114, v114, s16, v105
	v_or3_b32 v110, v110, v111, v113
	v_mul_f32_e32 v111, v136, v107
	v_rndne_f32_e32 v112, v112
	v_mul_f32_e32 v113, v138, v107
	v_add_f32_e32 v114, 0x43000000, v114
	v_rndne_f32_e32 v111, v111
	v_rndne_f32_e32 v113, v113
	v_mul_f32_e32 v107, v139, v107
	v_med3_f32 v112, v112, s16, v105
	v_cvt_i32_f32_sdwa v114, v114 dst_sel:BYTE_3 dst_unused:UNUSED_PAD src0_sel:DWORD
	v_rndne_f32_e32 v107, v107
	v_med3_f32 v111, v111, s16, v105
	v_med3_f32 v113, v113, s16, v105
	v_add_f32_e32 v112, 0x43000000, v112
	v_med3_f32 v107, v107, s16, v105
	v_add_f32_e32 v111, 0x43000000, v111
	v_cvt_i32_f32_e32 v112, v112
	v_add_f32_e32 v113, 0x43000000, v113
	v_cvt_i32_f32_e32 v111, v111
	v_cvt_i32_f32_sdwa v113, v113 dst_sel:WORD_1 dst_unused:UNUSED_PAD src0_sel:DWORD
	v_add_f32_e32 v107, 0x43000000, v107
	v_cvt_i32_f32_sdwa v107, v107 dst_sel:BYTE_3 dst_unused:UNUSED_PAD src0_sel:DWORD
	v_bitop3_b32 v110, v110, s17, v114 bitop3:0x36
	global_store_dword v[108:109], v110, off offset:1536
	v_lshlrev_b32_e32 v110, 8, v112
	v_or3_b32 v110, v110, v111, v113
	v_bitop3_b32 v107, v110, s17, v107 bitop3:0x36
	global_store_dword v[108:109], v107, off offset:1792
	s_and_saveexec_b64 s[6:7], s[2:3]
	s_cbranch_execnz .LBB0_460
	s_or_b64 exec, exec, s[6:7]
	s_cmpk_gt_i32 s4, 0x3fff
	s_mov_b64 s[0:1], -1
	s_cbranch_scc1 .LBB0_455
	s_branch .LBB0_461

.LBB0_461:
	s_add_i32 s0, s9, s18
	s_cmpk_gt_i32 s0, 0x3fff
	s_cbranch_scc1 .LBB0_463
	s_ashr_i32 s1, s0, 31
	s_lshl_b64 s[0:1], s[0:1], 13
	v_lshl_add_u64 v[50:51], v[100:101], 0, s[0:1]
	v_add_co_u32_e32 v62, vcc, 0x1000, v50
	global_load_dwordx4 v[34:37], v[50:51], off
	global_load_dwordx4 v[38:41], v[50:51], off offset:1024
	global_load_dwordx4 v[42:45], v[50:51], off offset:2048
	global_load_dwordx4 v[46:49], v[50:51], off offset:3072
	v_addc_co_u32_e32 v63, vcc, 0, v51, vcc
	global_load_dwordx4 v[50:53], v[62:63], off
	global_load_dwordx4 v[54:57], v[62:63], off offset:1024
	global_load_dwordx4 v[58:61], v[62:63], off offset:2048
	s_nop 0
	global_load_dwordx4 v[62:65], v[62:63], off offset:3072
	s_waitcnt vmcnt(8)
	s_branch .Lrms_lad_b1
.LBB0_463:
	s_waitcnt vmcnt(0)
.Lrms_lad_b1:
	v_mov_b32_e32 v108, v75
	v_mov_b32_e32 v109, v79
	v_mov_b32_e32 v106, v74
	v_mov_b32_e32 v107, v78
	v_pk_mul_f32 v[108:109], v[108:109], v[108:109]
	v_mov_b32_e32 v110, v77
	v_mov_b32_e32 v111, v81
	v_pk_fma_f32 v[106:107], v[106:107], v[106:107], v[108:109]
	v_mov_b32_e32 v108, v76
	v_mov_b32_e32 v109, v80
	v_pk_mul_f32 v[110:111], v[110:111], v[110:111]
	s_nop 0
	v_pk_fma_f32 v[108:109], v[108:109], v[108:109], v[110:111]
	v_pk_mul_f32 v[110:111], v[70:71], v[70:71]
	v_pk_add_f32 v[106:107], v[106:107], v[108:109]
	v_pk_mul_f32 v[108:109], v[72:73], v[72:73]
	v_pk_add_f32 v[106:107], v[106:107], v[106:107] op_sel_hi:[0,1]
	v_pk_mov_b32 v[112:113], v[110:111], v[108:109] op_sel:[1,0]
	v_mov_b32_e32 v111, v109
	v_mul_f32_e32 v106, v66, v66
	v_pk_add_f32 v[108:109], v[112:113], v[110:111]
	v_pk_fma_f32 v[110:111], v[66:67], v[66:67], v[106:107] op_sel_hi:[1,1,0]
	v_mul_f32_e32 v106, v68, v68
	v_pk_add_f32 v[108:109], v[108:109], v[108:109] op_sel_hi:[0,1]
	v_pk_fma_f32 v[112:113], v[68:69], v[68:69], v[106:107] op_sel_hi:[1,1,0]
	v_mul_f32_e32 v110, v94, v94
	v_mul_f32_e32 v112, v95, v95
	v_mul_f32_e32 v108, v96, v96
	v_mul_f32_e32 v106, v97, v97
	v_pk_add_f32 v[110:111], v[110:111], v[112:113]
	v_pk_add_f32 v[106:107], v[108:109], v[106:107]
	v_pk_mul_f32 v[108:109], v[92:93], v[92:93]
	v_pk_add_f32 v[106:107], v[110:111], v[106:107]
	v_pk_mul_f32 v[110:111], v[90:91], v[90:91]
	v_pk_add_f32 v[106:107], v[106:107], v[106:107] op_sel_hi:[0,1]
	v_pk_mov_b32 v[112:113], v[110:111], v[108:109] op_sel:[1,0]
	v_mov_b32_e32 v111, v109
	v_mul_f32_e32 v106, v86, v86
	v_pk_add_f32 v[108:109], v[112:113], v[110:111]
	v_pk_fma_f32 v[110:111], v[86:87], v[86:87], v[106:107] op_sel_hi:[1,1,0]
	v_mul_f32_e32 v106, v88, v88
	v_pk_add_f32 v[108:109], v[108:109], v[108:109] op_sel_hi:[0,1]
	v_pk_fma_f32 v[112:113], v[88:89], v[88:89], v[106:107] op_sel_hi:[1,1,0]
	v_mul_f32_e32 v110, v82, v82
	v_mul_f32_e32 v112, v83, v83
	v_mul_f32_e32 v108, v84, v84
	v_mul_f32_e32 v106, v85, v85
	v_pk_add_f32 v[110:111], v[110:111], v[112:113]
	v_pk_add_f32 v[106:107], v[108:109], v[106:107]
	s_nop 0
	v_pk_add_f32 v[106:107], v[110:111], v[106:107]
	s_nop 0
	v_add_f32_e32 v106, v106, v107
	s_nop 1
	v_add_f32_dpp v106, v106, v106 quad_perm:[1,0,3,2] row_mask:0xf bank_mask:0xf bound_ctrl:1
	s_nop 1
	v_add_f32_dpp v106, v106, v106 quad_perm:[2,3,0,1] row_mask:0xf bank_mask:0xf bound_ctrl:1
	s_nop 1
	v_add_f32_dpp v106, v106, v106 row_half_mirror row_mask:0xf bank_mask:0xf bound_ctrl:1
	s_nop 1
	v_add_f32_dpp v106, v106, v106 row_mirror row_mask:0xf bank_mask:0xf bound_ctrl:1
	s_nop 0
	v_readlane_b32 s5, v106, 16
	v_readlane_b32 s6, v106, 48
	v_readlane_b32 s0, v106, 0
	v_readlane_b32 s1, v106, 32
	v_mov_b32_e32 v106, s5
	v_mov_b32_e32 v107, s6
	v_pk_add_f32 v[106:107], s[0:1], v[106:107]
	s_ashr_i32 s5, s4, 31
	v_add_f32_e32 v106, v106, v107
	v_fmamk_f32 v106, v106, 0x3a000000, v98
	v_mul_f32_e32 v107, 0x4f800000, v106
	v_cmp_gt_f32_e32 vcc, s11, v106
	s_nop 1
	v_cndmask_b32_e32 v106, v106, v107, vcc
	v_sqrt_f32_e32 v107, v106
	s_nop 0
	v_add_u32_e32 v108, -1, v107
	v_fma_f32 v109, -v108, v107, v106
	v_cmp_ge_f32_e64 s[0:1], 0, v109
	v_add_u32_e32 v109, 1, v107
	s_nop 0
	v_cndmask_b32_e64 v108, v107, v108, s[0:1]
	v_fma_f32 v107, -v109, v107, v106
	v_cmp_lt_f32_e64 s[0:1], 0, v107
	s_nop 1
	v_cndmask_b32_e64 v107, v108, v109, s[0:1]
	v_mul_f32_e32 v108, 0x37800000, v107
	v_cndmask_b32_e32 v107, v107, v108, vcc
	v_cmp_class_f32_e32 vcc, v106, v104
	s_nop 1
	v_cndmask_b32_e32 v106, v107, v106, vcc
	v_div_scale_f32 v107, s[0:1], v106, v106, 1.0
	v_rcp_f32_e32 v108, v107
	s_nop 0
	v_fma_f32 v109, -v107, v108, 1.0
	v_fmac_f32_e32 v108, v109, v108
	v_div_scale_f32 v109, vcc, 1.0, v106, 1.0
	v_mul_f32_e32 v110, v109, v108
	v_fma_f32 v111, -v107, v110, v109
	v_fmac_f32_e32 v110, v111, v108
	v_fma_f32 v107, -v107, v110, v109
	v_div_fmas_f32 v107, v107, v108, v110
	v_div_fixup_f32 v106, v107, v106, 1.0
	v_pk_mul_f32 v[110:111], v[80:81], v[106:107] op_sel_hi:[1,0]
	v_pk_mul_f32 v[108:109], v[78:79], v[106:107] op_sel_hi:[1,0]
	v_pk_mul_f32 v[110:111], v[4:5], v[110:111]
	v_pk_mul_f32 v[108:109], v[2:3], v[108:109]
	v_max_f32_e64 v107, |v110|, |v111|
	v_max3_f32 v107, |v108|, |v109|, v107
	v_pk_mul_f32 v[114:115], v[76:77], v[106:107] op_sel_hi:[1,0]
	v_pk_mul_f32 v[112:113], v[74:75], v[106:107] op_sel_hi:[1,0]
	v_pk_mul_f32 v[114:115], v[8:9], v[114:115]
	v_pk_mul_f32 v[112:113], v[6:7], v[112:113]
	v_max_f32_e64 v116, |v114|, |v115|
	v_max3_f32 v116, |v112|, |v113|, v116
	v_max3_f32 v107, v107, 0, v116
	v_pk_mul_f32 v[118:119], v[72:73], v[106:107] op_sel_hi:[1,0]
	v_pk_mul_f32 v[116:117], v[70:71], v[106:107] op_sel_hi:[1,0]
	v_pk_mul_f32 v[118:119], v[12:13], v[118:119]
	v_pk_mul_f32 v[116:117], v[10:11], v[116:117]
	v_max_f32_e64 v120, |v118|, |v119|
	v_pk_mul_f32 v[122:123], v[68:69], v[106:107] op_sel_hi:[1,0]
	v_max3_f32 v124, |v116|, |v117|, v120
	v_pk_mul_f32 v[120:121], v[66:67], v[106:107] op_sel_hi:[1,0]
	v_pk_mul_f32 v[122:123], v[16:17], v[122:123]
	v_pk_mul_f32 v[120:121], v[14:15], v[120:121]
	v_max_f32_e64 v125, |v122|, |v123|
	v_max3_f32 v125, |v120|, |v121|, v125
	v_max3_f32 v107, v107, v124, v125
	v_pk_mul_f32 v[126:127], v[96:97], v[106:107] op_sel_hi:[1,0]
	v_pk_mul_f32 v[124:125], v[94:95], v[106:107] op_sel_hi:[1,0]
	v_pk_mul_f32 v[126:127], v[20:21], v[126:127]
	v_pk_mul_f32 v[124:125], v[18:19], v[124:125]
	v_max_f32_e64 v128, |v126|, |v127|
	v_pk_mul_f32 v[130:131], v[92:93], v[106:107] op_sel_hi:[1,0]
	v_max3_f32 v132, |v124|, |v125|, v128
	v_pk_mul_f32 v[128:129], v[90:91], v[106:107] op_sel_hi:[1,0]
	v_pk_mul_f32 v[130:131], v[24:25], v[130:131]
	v_pk_mul_f32 v[128:129], v[22:23], v[128:129]
	v_max_f32_e64 v133, |v130|, |v131|
	v_max3_f32 v133, |v128|, |v129|, v133
	v_pk_mul_f32 v[134:135], v[88:89], v[106:107] op_sel_hi:[1,0]
	v_max3_f32 v140, v107, v132, v133
	v_pk_mul_f32 v[132:133], v[86:87], v[106:107] op_sel_hi:[1,0]
	v_pk_mul_f32 v[134:135], v[28:29], v[134:135]
	v_pk_mul_f32 v[132:133], v[26:27], v[132:133]
	v_max_f32_e64 v107, |v134|, |v135|
	v_max3_f32 v141, |v132|, |v133|, v107
	v_pk_mul_f32 v[136:137], v[82:83], v[106:107] op_sel_hi:[1,0]
	v_pk_mul_f32 v[106:107], v[84:85], v[106:107] op_sel_hi:[1,0]
	v_pk_mul_f32 v[136:137], v[30:31], v[136:137]
	v_pk_mul_f32 v[138:139], v[32:33], v[106:107]
	s_nop 0
	v_max_f32_e64 v106, |v138|, |v139|
	v_max3_f32 v106, |v136|, |v137|, v106
	v_max3_f32 v106, v140, v141, v106
	s_nop 1
	v_mov_b32_dpp v107, v106 quad_perm:[1,0,3,2] row_mask:0xf bank_mask:0xf bound_ctrl:1
	v_max_f32_e32 v107, v107, v107
	v_max_f32_e32 v106, v106, v107
	s_nop 1
	v_mov_b32_dpp v107, v106 quad_perm:[2,3,0,1] row_mask:0xf bank_mask:0xf bound_ctrl:1
	v_max_f32_e32 v107, v107, v107
	v_max_f32_e32 v106, v106, v107
	s_nop 1
	v_mov_b32_dpp v107, v106 row_half_mirror row_mask:0xf bank_mask:0xf bound_ctrl:1
	v_max_f32_e32 v107, v107, v107
	v_max_f32_e32 v106, v106, v107
	s_nop 1
	v_mov_b32_dpp v107, v106 row_mirror row_mask:0xf bank_mask:0xf bound_ctrl:1
	v_max_f32_e32 v107, v107, v107
	v_max_f32_e32 v106, v106, v107
	s_nop 0
	v_readlane_b32 s0, v106, 0
	v_readlane_b32 s1, v106, 16
	s_nop 0
	v_max_f32_e64 v140, s0, s0
	v_max_f32_e64 v107, s1, s1
	v_readlane_b32 s0, v106, 32
	v_readlane_b32 s1, v106, 48
	v_max_f32_e32 v107, v140, v107
	v_max_f32_e64 v140, s0, s0
	v_max_f32_e64 v106, s1, s1
	v_max_f32_e32 v106, v140, v106
	v_max3_f32 v106, v107, v106, s14
	v_div_scale_f32 v107, s[0:1], v106, v106, s15
	v_rcp_f32_e32 v140, v107
	s_lshl_b64 s[0:1], s[4:5], 11
	v_fma_f32 v141, -v107, v140, 1.0
	v_fmac_f32_e32 v140, v141, v140
	v_div_scale_f32 v141, vcc, s15, v106, s15
	v_mul_f32_e32 v142, v141, v140
	v_fma_f32 v143, -v107, v142, v141
	v_fmac_f32_e32 v142, v143, v140
	v_fma_f32 v107, -v107, v142, v141
	v_div_fmas_f32 v107, v107, v140, v142
	v_div_fixup_f32 v107, v107, v106, s15
	v_mul_f32_e32 v108, v108, v107
	v_rndne_f32_e32 v108, v108
	v_mul_f32_e32 v109, v109, v107
	v_rndne_f32_e32 v109, v109
	v_mul_f32_e32 v110, v110, v107
	v_med3_f32 v108, v108, s16, v105
	v_rndne_f32_e32 v110, v110
	v_mul_f32_e32 v111, v111, v107
	v_med3_f32 v109, v109, s16, v105
	v_add_f32_e32 v108, 0x43000000, v108
	v_rndne_f32_e32 v111, v111
	v_med3_f32 v110, v110, s16, v105
	v_cvt_i32_f32_e32 v140, v108
	v_add_f32_e32 v108, 0x43000000, v109
	v_med3_f32 v111, v111, s16, v105
	v_cvt_i32_f32_e32 v141, v108
	v_add_f32_e32 v108, 0x43000000, v110
	v_cvt_i32_f32_sdwa v110, v108 dst_sel:WORD_1 dst_unused:UNUSED_PAD src0_sel:DWORD
	v_add_f32_e32 v108, 0x43000000, v111
	v_cvt_i32_f32_sdwa v111, v108 dst_sel:BYTE_3 dst_unused:UNUSED_PAD src0_sel:DWORD
	v_lshlrev_b32_e32 v141, 8, v141
	v_or3_b32 v110, v141, v140, v110
	v_lshl_add_u64 v[108:109], v[102:103], 0, s[0:1]
	v_bitop3_b32 v110, v110, s17, v111 bitop3:0x36
	v_mul_f32_e32 v111, v112, v107
	v_mul_f32_e32 v112, v113, v107
	v_rndne_f32_e32 v112, v112
	v_mul_f32_e32 v113, v114, v107
	v_rndne_f32_e32 v111, v111
	v_rndne_f32_e32 v113, v113
	v_med3_f32 v112, v112, s16, v105
	v_med3_f32 v111, v111, s16, v105
	v_med3_f32 v113, v113, s16, v105
	v_add_f32_e32 v112, 0x43000000, v112
	v_add_f32_e32 v111, 0x43000000, v111
	v_cvt_i32_f32_e32 v112, v112
	v_add_f32_e32 v113, 0x43000000, v113
	v_cvt_i32_f32_e32 v111, v111
	v_cvt_i32_f32_sdwa v113, v113 dst_sel:WORD_1 dst_unused:UNUSED_PAD src0_sel:DWORD
	v_mul_f32_e32 v114, v115, v107
	v_rndne_f32_e32 v114, v114
	global_store_dword v[108:109], v110, off
	v_lshlrev_b32_e32 v110, 8, v112
	v_mul_f32_e32 v112, v117, v107
	v_med3_f32 v114, v114, s16, v105
	v_or3_b32 v110, v110, v111, v113
	v_mul_f32_e32 v111, v116, v107
	v_rndne_f32_e32 v112, v112
	v_mul_f32_e32 v113, v118, v107
	v_add_f32_e32 v114, 0x43000000, v114
	v_rndne_f32_e32 v111, v111
	v_rndne_f32_e32 v113, v113
	v_med3_f32 v112, v112, s16, v105
	v_cvt_i32_f32_sdwa v114, v114 dst_sel:BYTE_3 dst_unused:UNUSED_PAD src0_sel:DWORD
	v_med3_f32 v111, v111, s16, v105
	v_med3_f32 v113, v113, s16, v105
	v_add_f32_e32 v112, 0x43000000, v112
	v_add_f32_e32 v111, 0x43000000, v111
	v_cvt_i32_f32_e32 v112, v112
	v_add_f32_e32 v113, 0x43000000, v113
	v_cvt_i32_f32_e32 v111, v111
	v_cvt_i32_f32_sdwa v113, v113 dst_sel:WORD_1 dst_unused:UNUSED_PAD src0_sel:DWORD
	v_bitop3_b32 v110, v110, s17, v114 bitop3:0x36
	v_mul_f32_e32 v114, v119, v107
	v_rndne_f32_e32 v114, v114
	global_store_dword v[108:109], v110, off offset:256
	v_lshlrev_b32_e32 v110, 8, v112
	v_mul_f32_e32 v112, v121, v107
	v_med3_f32 v114, v114, s16, v105
	v_or3_b32 v110, v110, v111, v113
	v_mul_f32_e32 v111, v120, v107
	v_rndne_f32_e32 v112, v112
	v_mul_f32_e32 v113, v122, v107
	v_add_f32_e32 v114, 0x43000000, v114
	v_rndne_f32_e32 v111, v111
	v_rndne_f32_e32 v113, v113
	v_med3_f32 v112, v112, s16, v105
	v_cvt_i32_f32_sdwa v114, v114 dst_sel:BYTE_3 dst_unused:UNUSED_PAD src0_sel:DWORD
	v_med3_f32 v111, v111, s16, v105
	v_med3_f32 v113, v113, s16, v105
	v_add_f32_e32 v112, 0x43000000, v112
	v_add_f32_e32 v111, 0x43000000, v111
	v_cvt_i32_f32_e32 v112, v112
	v_add_f32_e32 v113, 0x43000000, v113
	v_cvt_i32_f32_e32 v111, v111
	v_cvt_i32_f32_sdwa v113, v113 dst_sel:WORD_1 dst_unused:UNUSED_PAD src0_sel:DWORD
	v_bitop3_b32 v110, v110, s17, v114 bitop3:0x36
	v_mul_f32_e32 v114, v123, v107
	v_rndne_f32_e32 v114, v114
	global_store_dword v[108:109], v110, off offset:512
	v_lshlrev_b32_e32 v110, 8, v112
	v_mul_f32_e32 v112, v125, v107
	v_med3_f32 v114, v114, s16, v105
	v_or3_b32 v110, v110, v111, v113
	v_mul_f32_e32 v111, v124, v107
	v_rndne_f32_e32 v112, v112
	v_mul_f32_e32 v113, v126, v107
	v_add_f32_e32 v114, 0x43000000, v114
	v_rndne_f32_e32 v111, v111
	v_rndne_f32_e32 v113, v113
	v_med3_f32 v112, v112, s16, v105
	v_cvt_i32_f32_sdwa v114, v114 dst_sel:BYTE_3 dst_unused:UNUSED_PAD src0_sel:DWORD
	v_med3_f32 v111, v111, s16, v105
	v_med3_f32 v113, v113, s16, v105
	v_add_f32_e32 v112, 0x43000000, v112
	v_add_f32_e32 v111, 0x43000000, v111
	v_cvt_i32_f32_e32 v112, v112
	v_add_f32_e32 v113, 0x43000000, v113
	v_cvt_i32_f32_e32 v111, v111
	v_cvt_i32_f32_sdwa v113, v113 dst_sel:WORD_1 dst_unused:UNUSED_PAD src0_sel:DWORD
	v_bitop3_b32 v110, v110, s17, v114 bitop3:0x36
	v_mul_f32_e32 v114, v127, v107
	v_rndne_f32_e32 v114, v114
	global_store_dword v[108:109], v110, off offset:768
	v_lshlrev_b32_e32 v110, 8, v112
	v_mul_f32_e32 v112, v129, v107
	v_med3_f32 v114, v114, s16, v105
	v_or3_b32 v110, v110, v111, v113
	v_mul_f32_e32 v111, v128, v107
	v_rndne_f32_e32 v112, v112
	v_mul_f32_e32 v113, v130, v107
	v_add_f32_e32 v114, 0x43000000, v114
	v_rndne_f32_e32 v111, v111
	v_rndne_f32_e32 v113, v113
	v_med3_f32 v112, v112, s16, v105
	v_cvt_i32_f32_sdwa v114, v114 dst_sel:BYTE_3 dst_unused:UNUSED_PAD src0_sel:DWORD
	v_med3_f32 v111, v111, s16, v105
	v_med3_f32 v113, v113, s16, v105
	v_add_f32_e32 v112, 0x43000000, v112
	v_add_f32_e32 v111, 0x43000000, v111
	v_cvt_i32_f32_e32 v112, v112
	v_add_f32_e32 v113, 0x43000000, v113
	v_cvt_i32_f32_e32 v111, v111
	v_cvt_i32_f32_sdwa v113, v113 dst_sel:WORD_1 dst_unused:UNUSED_PAD src0_sel:DWORD
	v_bitop3_b32 v110, v110, s17, v114 bitop3:0x36
	v_mul_f32_e32 v114, v131, v107
	v_rndne_f32_e32 v114, v114
	global_store_dword v[108:109], v110, off offset:1024
	v_lshlrev_b32_e32 v110, 8, v112
	v_mul_f32_e32 v112, v133, v107
	v_med3_f32 v114, v114, s16, v105
	v_or3_b32 v110, v110, v111, v113
	v_mul_f32_e32 v111, v132, v107
	v_rndne_f32_e32 v112, v112
	v_mul_f32_e32 v113, v134, v107
	v_add_f32_e32 v114, 0x43000000, v114
	v_rndne_f32_e32 v111, v111
	v_rndne_f32_e32 v113, v113
	v_med3_f32 v112, v112, s16, v105
	v_cvt_i32_f32_sdwa v114, v114 dst_sel:BYTE_3 dst_unused:UNUSED_PAD src0_sel:DWORD
	v_med3_f32 v111, v111, s16, v105
	v_med3_f32 v113, v113, s16, v105
	v_add_f32_e32 v112, 0x43000000, v112
	v_add_f32_e32 v111, 0x43000000, v111
	v_cvt_i32_f32_e32 v112, v112
	v_add_f32_e32 v113, 0x43000000, v113
	v_cvt_i32_f32_e32 v111, v111
	v_cvt_i32_f32_sdwa v113, v113 dst_sel:WORD_1 dst_unused:UNUSED_PAD src0_sel:DWORD
	v_bitop3_b32 v110, v110, s17, v114 bitop3:0x36
	v_mul_f32_e32 v114, v135, v107
	v_rndne_f32_e32 v114, v114
	global_store_dword v[108:109], v110, off offset:1280
	v_lshlrev_b32_e32 v110, 8, v112
	v_mul_f32_e32 v112, v137, v107
	v_med3_f32 v114, v114, s16, v105
	v_or3_b32 v110, v110, v111, v113
	v_mul_f32_e32 v111, v136, v107
	v_rndne_f32_e32 v112, v112
	v_mul_f32_e32 v113, v138, v107
	v_add_f32_e32 v114, 0x43000000, v114
	v_rndne_f32_e32 v111, v111
	v_rndne_f32_e32 v113, v113
	v_mul_f32_e32 v107, v139, v107
	v_med3_f32 v112, v112, s16, v105
	v_cvt_i32_f32_sdwa v114, v114 dst_sel:BYTE_3 dst_unused:UNUSED_PAD src0_sel:DWORD
	v_rndne_f32_e32 v107, v107
	v_med3_f32 v111, v111, s16, v105
	v_med3_f32 v113, v113, s16, v105
	v_add_f32_e32 v112, 0x43000000, v112
	v_med3_f32 v107, v107, s16, v105
	v_add_f32_e32 v111, 0x43000000, v111
	v_cvt_i32_f32_e32 v112, v112
	v_add_f32_e32 v113, 0x43000000, v113
	v_cvt_i32_f32_e32 v111, v111
	v_cvt_i32_f32_sdwa v113, v113 dst_sel:WORD_1 dst_unused:UNUSED_PAD src0_sel:DWORD
	v_add_f32_e32 v107, 0x43000000, v107
	v_cvt_i32_f32_sdwa v107, v107 dst_sel:BYTE_3 dst_unused:UNUSED_PAD src0_sel:DWORD
	v_bitop3_b32 v110, v110, s17, v114 bitop3:0x36
	global_store_dword v[108:109], v110, off offset:1536
	v_lshlrev_b32_e32 v110, 8, v112
	v_or3_b32 v110, v110, v111, v113
	v_bitop3_b32 v107, v110, s17, v107 bitop3:0x36
	global_store_dword v[108:109], v107, off offset:1792
	s_and_saveexec_b64 s[0:1], s[2:3]
	s_cbranch_execz .LBB0_454
	s_lshl_b64 s[4:5], s[4:5], 2
	s_add_u32 s4, s38, s4
	s_addc_u32 s5, s39, s5
	v_mul_f32_e32 v106, 0x3c010204, v106
	global_store_dword v99, v106, s[4:5]
	s_branch .LBB0_454

.LBB0_1370:
	s_waitcnt lgkmcnt(0)
	global_load_dwordx4 v[6:9], v[2:3], off offset:-16
	global_load_dwordx4 v[10:13], v[2:3], off
	v_lshl_add_u64 v[2:3], v[2:3], 0, s[2:3]
	global_load_dwordx4 v[14:17], v[2:3], off offset:-16
	global_load_dwordx4 v[18:21], v[2:3], off
	v_lshl_add_u64 v[2:3], v[2:3], 0, s[2:3]
	global_load_dwordx4 v[22:25], v[2:3], off offset:-16
	global_load_dwordx4 v[26:29], v[2:3], off
	v_lshl_add_u64 v[2:3], v[2:3], 0, s[2:3]
	global_load_dwordx4 v[30:33], v[2:3], off offset:-16
	global_load_dwordx4 v[230:233], v[2:3], off
	v_lshl_add_u64 v[2:3], v[2:3], 0, s[2:3]
	s_waitcnt vmcnt(7)
	ds_write2st64_b32 v5, v6, v7 offset1:32
	ds_write2st64_b32 v5, v8, v9 offset0:64 offset1:96
	s_waitcnt vmcnt(6)
	ds_write2st64_b32 v5, v10, v11 offset0:128 offset1:160
	ds_write2st64_b32 v5, v12, v13 offset0:192 offset1:224
	v_add_u32_e32 v5, 0x800, v5
	s_waitcnt vmcnt(5)
	ds_write2st64_b32 v5, v14, v15 offset1:32
	ds_write2st64_b32 v5, v16, v17 offset0:64 offset1:96
	s_waitcnt vmcnt(4)
	ds_write2st64_b32 v5, v18, v19 offset0:128 offset1:160
	ds_write2st64_b32 v5, v20, v21 offset0:192 offset1:224
	v_add_u32_e32 v5, 0x800, v5
	s_waitcnt vmcnt(3)
	ds_write2st64_b32 v5, v22, v23 offset1:32
	ds_write2st64_b32 v5, v24, v25 offset0:64 offset1:96
	s_waitcnt vmcnt(2)
	ds_write2st64_b32 v5, v26, v27 offset0:128 offset1:160
	ds_write2st64_b32 v5, v28, v29 offset0:192 offset1:224
	v_add_u32_e32 v5, 0x800, v5
	s_waitcnt vmcnt(1)
	ds_write2st64_b32 v5, v30, v31 offset1:32
	ds_write2st64_b32 v5, v32, v33 offset0:64 offset1:96
	s_waitcnt vmcnt(0)
	ds_write2st64_b32 v5, v230, v231 offset0:128 offset1:160
	ds_write2st64_b32 v5, v232, v233 offset0:192 offset1:224
	v_add_u32_e32 v5, 0x800, v5
	v_add_u32_e32 v4, 0x800, v4
	s_or_b64 exec, exec, s[0:1]
	s_add_i32 s0, 0, 0x10000
	v_cmp_gt_u32_e64 s[2:3], 8, v0
	v_lshl_add_u32 v110, v0, 2, s0
	s_and_saveexec_b64 s[0:1], s[2:3]
	v_mov_b32_e32 v2, 0
	ds_write_b32 v110, v2
	s_or_b64 exec, exec, s[0:1]
	s_cmpk_lg_i32 s13, 0x100
	s_waitcnt lgkmcnt(0)
	s_barrier
	s_cbranch_scc1 .LBB0_1388
	v_readlane_b32 s9, v251, 28
	s_lshl_b32 s0, s12, 6
	s_lshl_b32 s1, s9, 3
	s_add_i32 s0, s1, s0
	s_ashr_i32 s1, s0, 31
	s_lshl_b64 s[6:7], s[0:1], 12
	s_add_u32 s4, s22, s6
	v_readlane_b32 s60, v251, 11
	s_addc_u32 s5, s23, s7
	v_lshlrev_b32_e32 v38, 3, v1
	v_lshlrev_b32_e32 v34, 4, v1
	v_mov_b32_e32 v35, 0
	v_readlane_b32 s98, v251, 2
	v_readlane_b32 s99, v251, 3
	s_nop 4
	global_load_dwordx4 v[234:237], v35, s[98:99] offset:16
	global_load_dwordx4 v[238:241], v35, s[98:99]
	v_readlane_b32 s64, v251, 15
	v_readlane_b32 s65, v251, 16
	global_load_dwordx2 v[44:45], v38, s[4:5]
	global_load_dwordx2 v[48:49], v38, s[4:5] offset:512
	global_load_dwordx2 v[52:53], v38, s[4:5] offset:1024
	global_load_dwordx2 v[56:57], v38, s[4:5] offset:1536
	global_load_dwordx2 v[60:61], v38, s[4:5] offset:2048
	global_load_dwordx2 v[64:65], v38, s[4:5] offset:2560
	global_load_dwordx2 v[68:69], v38, s[4:5] offset:3072
	global_load_dwordx2 v[72:73], v38, s[4:5] offset:3584
	s_mov_b64 s[26:27], 0x2000
	s_movk_i32 s4, 0x3000
	v_lshl_add_u64 v[2:3], s[64:65], 0, v[34:35]
	v_lshl_add_u64 v[36:37], v[2:3], 0, s[26:27]
	v_add_co_u32_e32 v40, vcc, s4, v2
	v_mov_b32_e32 v39, v35
	s_nop 0
	v_addc_co_u32_e32 v41, vcc, 0, v3, vcc
	global_load_dwordx4 v[2:5], v[36:37], off offset:1024
	global_load_dwordx4 v[6:9], v[36:37], off offset:2048
	global_load_dwordx4 v[10:13], v[36:37], off offset:3072
	global_load_dwordx4 v[14:17], v[40:41], off offset:-4096
	global_load_dwordx4 v[18:21], v[40:41], off
	global_load_dwordx4 v[22:25], v[40:41], off offset:1024
	global_load_dwordx4 v[26:29], v[40:41], off offset:2048
	global_load_dwordx4 v[30:33], v[40:41], off offset:3072
	s_lshl_b32 s8, s12, 7
	s_lshl_b32 s9, s9, 4
	v_lshl_add_u64 v[36:37], s[22:23], 0, v[38:39]
	v_or_b32_e32 v38, s6, v38
	v_mov_b32_e32 v39, s7
	s_lshl_b64 s[6:7], s[0:1], 11
	s_lshl_b64 s[28:29], s[0:1], 2
	s_lshl_b32 s1, s0, 1
	s_or_b32 s33, s0, 2
	s_add_i32 s0, s8, s9
	v_readlane_b32 s61, v251, 12
	v_readlane_b32 s62, v251, 13
	s_or_b32 s38, s1, 2
	s_ashr_i32 s1, s0, 31
	s_mov_b32 s10, 0
	v_cmp_eq_u32_e64 s[4:5], 0, v1
	s_mov_b32 s11, 0x5b301000
	v_add_u32_e32 v34, 0, v34
	v_lshl_or_b32 v40, v1, 2, s6
	v_mov_b32_e32 v41, s7
	s_lshl_b64 s[42:43], s[0:1], 2
	v_mov_b32_e32 v111, 0x358637bd
	s_mov_b32 s35, 0xf800000
	v_mov_b32_e32 v112, 0x260
	s_mov_b32 s60, 0xc3e00000
	s_mov_b32 s61, 0x30b00000
	s_mov_b32 s62, 0xff61b1e6
	v_mov_b32_e32 v113, 0x100000
	v_mov_b32_e32 v114, 0x110000
	s_mov_b64 s[44:45], 0x1000
	v_mov_b32_e32 v115, 0x43e00000
	v_mov_b32_e32 v116, 0xff61b1e6
	v_readlane_b32 s63, v251, 14
	v_readlane_b32 s66, v251, 17
	v_readlane_b32 s67, v251, 18
	v_readlane_b32 s68, v251, 19
	v_readlane_b32 s69, v251, 20
	v_readlane_b32 s70, v251, 21
	v_readlane_b32 s71, v251, 22
	v_readlane_b32 s72, v251, 23
	v_readlane_b32 s73, v251, 24
	v_readlane_b32 s74, v251, 25
	v_readlane_b32 s75, v251, 26
	s_waitcnt vmcnt(15)
	v_lshlrev_b32_e32 v42, 16, v44
	v_and_b32_e32 v43, 0xffff0000, v44
	v_lshlrev_b32_e32 v46, 16, v45
	v_and_b32_e32 v47, 0xffff0000, v45
	s_waitcnt vmcnt(14)
	v_lshlrev_b32_e32 v44, 16, v48
	v_and_b32_e32 v45, 0xffff0000, v48
	v_lshlrev_b32_e32 v50, 16, v49
	v_and_b32_e32 v51, 0xffff0000, v49
	s_waitcnt vmcnt(13)
	v_lshlrev_b32_e32 v48, 16, v52
	v_and_b32_e32 v49, 0xffff0000, v52
	v_lshlrev_b32_e32 v54, 16, v53
	v_and_b32_e32 v55, 0xffff0000, v53
	s_waitcnt vmcnt(12)
	v_lshlrev_b32_e32 v52, 16, v56
	v_and_b32_e32 v53, 0xffff0000, v56
	v_lshlrev_b32_e32 v58, 16, v57
	v_and_b32_e32 v59, 0xffff0000, v57
	s_waitcnt vmcnt(11)
	v_lshlrev_b32_e32 v56, 16, v60
	v_and_b32_e32 v57, 0xffff0000, v60
	v_lshlrev_b32_e32 v62, 16, v61
	v_and_b32_e32 v63, 0xffff0000, v61
	s_waitcnt vmcnt(10)
	v_lshlrev_b32_e32 v60, 16, v64
	v_and_b32_e32 v61, 0xffff0000, v64
	v_lshlrev_b32_e32 v66, 16, v65
	v_and_b32_e32 v67, 0xffff0000, v65
	s_waitcnt vmcnt(9)
	v_lshlrev_b32_e32 v64, 16, v68
	v_and_b32_e32 v65, 0xffff0000, v68
	v_lshlrev_b32_e32 v70, 16, v69
	v_and_b32_e32 v71, 0xffff0000, v69
	s_waitcnt vmcnt(8)
	v_lshlrev_b32_e32 v68, 16, v72
	v_and_b32_e32 v69, 0xffff0000, v72
	v_lshlrev_b32_e32 v72, 16, v73
	v_and_b32_e32 v73, 0xffff0000, v73
	s_branch .LBB0_1376

.LBB0_1376:
	v_mov_b32_e32 v78, v43
	v_mov_b32_e32 v79, v45
	v_mov_b32_e32 v76, v42
	v_mov_b32_e32 v77, v44
	v_pk_mul_f32 v[78:79], v[78:79], v[78:79]
	v_mov_b32_e32 v80, v47
	v_mov_b32_e32 v81, v51
	v_pk_fma_f32 v[76:77], v[76:77], v[76:77], v[78:79]
	v_mov_b32_e32 v78, v46
	v_mov_b32_e32 v79, v50
	v_pk_mul_f32 v[80:81], v[80:81], v[80:81]
	v_lshl_add_u64 v[74:75], s[56:57], 0, v[38:39]
	v_pk_fma_f32 v[78:79], v[78:79], v[78:79], v[80:81]
	v_pk_mul_f32 v[80:81], v[48:49], v[48:49]
	v_pk_add_f32 v[76:77], v[76:77], v[78:79]
	v_pk_mul_f32 v[78:79], v[54:55], v[54:55]
	v_pk_add_f32 v[76:77], v[76:77], v[76:77] op_sel:[0,1] op_sel_hi:[1,0]
	v_pk_mov_b32 v[82:83], v[80:81], v[78:79] op_sel:[1,0]
	v_mov_b32_e32 v81, v79
	v_pk_add_f32 v[78:79], v[82:83], v[80:81]
	v_mul_f32_e32 v80, v56, v56
	v_mul_f32_e32 v81, v57, v57
	v_pk_add_f32 v[78:79], v[78:79], v[78:79] op_sel:[0,1] op_sel_hi:[1,0]
	v_mov_b32_e32 v77, v80
	v_mov_b32_e32 v79, v81
	v_pk_add_f32 v[76:77], v[76:77], v[78:79]
	v_mul_f32_e32 v78, v53, v53
	v_mul_f32_e32 v80, v59, v59
	v_mul_f32_e32 v82, v62, v62
	v_mul_f32_e32 v83, v63, v63
	v_pk_fma_f32 v[78:79], v[52:53], v[52:53], v[78:79] op_sel_hi:[1,1,0]
	v_pk_fma_f32 v[80:81], v[58:59], v[58:59], v[80:81] op_sel_hi:[1,1,0]
	v_mov_b32_e32 v79, v82
	v_mov_b32_e32 v81, v83
	v_pk_add_f32 v[78:79], v[78:79], v[80:81]
	v_pk_mul_f32 v[80:81], v[60:61], v[60:61]
	v_pk_add_f32 v[76:77], v[76:77], v[78:79]
	v_pk_mul_f32 v[78:79], v[66:67], v[66:67]
	v_pk_add_f32 v[76:77], v[76:77], v[76:77] op_sel:[0,1] op_sel_hi:[1,0]
	v_pk_mov_b32 v[82:83], v[80:81], v[78:79] op_sel:[1,0]
	v_mov_b32_e32 v81, v79
	v_pk_add_f32 v[78:79], v[82:83], v[80:81]
	v_mul_f32_e32 v80, v68, v68
	v_mul_f32_e32 v81, v69, v69
	v_pk_add_f32 v[78:79], v[78:79], v[78:79] op_sel:[0,1] op_sel_hi:[1,0]
	v_mov_b32_e32 v77, v80
	v_mov_b32_e32 v79, v81
	v_pk_add_f32 v[76:77], v[76:77], v[78:79]
	v_mul_f32_e32 v78, v65, v65
	v_mul_f32_e32 v80, v71, v71
	v_mul_f32_e32 v82, v72, v72
	v_mul_f32_e32 v83, v73, v73
	v_pk_fma_f32 v[78:79], v[64:65], v[64:65], v[78:79] op_sel_hi:[1,1,0]
	v_pk_fma_f32 v[80:81], v[70:71], v[70:71], v[80:81] op_sel_hi:[1,1,0]
	v_mov_b32_e32 v79, v82
	v_mov_b32_e32 v81, v83
	v_pk_add_f32 v[78:79], v[78:79], v[80:81]
	v_add_co_u32_e32 v74, vcc, s11, v74
	v_pk_add_f32 v[76:77], v[76:77], v[78:79]
	s_nop 0
	v_addc_co_u32_e32 v75, vcc, 0, v75, vcc
	v_add_f32_e32 v76, v76, v77
	global_load_dwordx2 v[90:91], v[74:75], off
	global_load_dwordx2 v[88:89], v[74:75], off offset:512
	global_load_dwordx2 v[82:83], v[74:75], off offset:1024
	global_load_dwordx2 v[80:81], v[74:75], off offset:1536
	v_add_f32_dpp v76, v76, v76 quad_perm:[1,0,3,2] row_mask:0xf bank_mask:0xf bound_ctrl:1
	v_mov_b32_e32 v96, 0
	v_mov_b32_e32 v97, 0
	v_add_f32_dpp v76, v76, v76 quad_perm:[2,3,0,1] row_mask:0xf bank_mask:0xf bound_ctrl:1
	v_mov_b32_e32 v98, 0
	s_nop 0
	v_add_f32_dpp v76, v76, v76 row_half_mirror row_mask:0xf bank_mask:0xf bound_ctrl:1
	s_nop 1
	v_add_f32_dpp v76, v76, v76 row_mirror row_mask:0xf bank_mask:0xf bound_ctrl:1
	s_nop 0
	v_readlane_b32 s6, v76, 16
	v_readlane_b32 s7, v76, 48
	v_readlane_b32 s0, v76, 0
	v_readlane_b32 s1, v76, 32
	v_mov_b32_e32 v76, s6
	v_mov_b32_e32 v77, s7
	v_pk_add_f32 v[76:77], s[0:1], v[76:77]
	s_nop 0
	v_add_f32_e32 v76, v76, v77
	v_fmamk_f32 v76, v76, 0x3a000000, v111
	v_mul_f32_e32 v77, 0x4f800000, v76
	v_cmp_gt_f32_e32 vcc, s35, v76
	s_nop 1
	v_cndmask_b32_e32 v76, v76, v77, vcc
	v_sqrt_f32_e32 v77, v76
	s_nop 0
	v_add_u32_e32 v78, -1, v77
	v_fma_f32 v79, -v78, v77, v76
	v_cmp_ge_f32_e64 s[0:1], 0, v79
	v_add_u32_e32 v79, 1, v77
	s_nop 0
	v_cndmask_b32_e64 v78, v77, v78, s[0:1]
	v_fma_f32 v77, -v79, v77, v76
	v_cmp_lt_f32_e64 s[0:1], 0, v77
	s_nop 1
	v_cndmask_b32_e64 v77, v78, v79, s[0:1]
	v_mul_f32_e32 v78, 0x37800000, v77
	v_cndmask_b32_e32 v77, v77, v78, vcc
	v_cmp_class_f32_e32 vcc, v76, v112
	s_nop 1
	v_cndmask_b32_e32 v92, v77, v76, vcc
	v_div_scale_f32 v93, s[0:1], v92, v92, 1.0
	v_rcp_f32_e32 v94, v93
	global_load_dwordx2 v[86:87], v[74:75], off offset:2048
	global_load_dwordx2 v[84:85], v[74:75], off offset:2560
	global_load_dwordx2 v[78:79], v[74:75], off offset:3072
	global_load_dwordx2 v[76:77], v[74:75], off offset:3584
	v_fma_f32 v74, -v93, v94, 1.0
	v_fmac_f32_e32 v94, v74, v94
	v_div_scale_f32 v74, vcc, 1.0, v92, 1.0
	v_mul_f32_e32 v75, v74, v94
	v_fma_f32 v95, -v93, v75, v74
	v_fmac_f32_e32 v75, v95, v94
	v_fma_f32 v74, -v93, v75, v74
	v_div_fmas_f32 v74, v74, v94, v75
	v_div_fixup_f32 v92, v74, v92, 1.0
	v_pk_mul_f32 v[42:43], v[92:93], v[42:43] op_sel_hi:[0,1]
	s_waitcnt vmcnt(12)
	v_pk_mul_f32 v[42:43], v[42:43], v[14:15]
	v_pk_mul_f32 v[46:47], v[92:93], v[46:47] op_sel_hi:[0,1]
	v_med3_f32 v93, v42, s60, v115
	v_med3_f32 v94, v43, s60, v115
	v_mov_b32_e32 v95, 0
	v_cvt_pk_fp8_f32 v95, v93, v94
	v_pk_mul_f32 v[46:47], v[46:47], v[16:17]
	v_lshl_add_u64 v[74:75], s[56:57], 0, v[40:41]
	v_med3_f32 v93, v46, s60, v115
	v_med3_f32 v94, v47, s60, v115
	v_cvt_pk_fp8_f32 v95, v93, v94 op_sel:[0,0,1]
	v_add_co_u32_e32 v74, vcc, s61, v74
	v_pk_mul_f32 v[44:45], v[92:93], v[44:45] op_sel_hi:[0,1]
	s_nop 0
	v_addc_co_u32_e32 v75, vcc, 0, v75, vcc
	v_pk_mul_f32 v[44:45], v[44:45], v[2:3]
	global_store_dword v[74:75], v95, off
	v_pk_mul_f32 v[50:51], v[92:93], v[50:51] op_sel_hi:[0,1]
	v_med3_f32 v93, v44, s60, v115
	v_med3_f32 v94, v45, s60, v115
	v_mov_b32_e32 v95, 0
	v_cvt_pk_fp8_f32 v95, v93, v94
	v_pk_mul_f32 v[50:51], v[50:51], v[4:5]
	s_nop 0
	v_med3_f32 v93, v50, s60, v115
	v_pk_mul_f32 v[48:49], v[92:93], v[48:49] op_sel_hi:[0,1]
	v_med3_f32 v94, v51, s60, v115
	v_pk_mul_f32 v[48:49], v[48:49], v[6:7]
	v_cvt_pk_fp8_f32 v95, v93, v94 op_sel:[0,0,1]
	v_pk_mul_f32 v[54:55], v[92:93], v[54:55] op_sel_hi:[0,1]
	v_med3_f32 v93, v48, s60, v115
	v_med3_f32 v94, v49, s60, v115
	v_cvt_pk_fp8_f32 v96, v93, v94
	v_pk_mul_f32 v[54:55], v[54:55], v[8:9]
	s_nop 0
	v_med3_f32 v93, v54, s60, v115
	v_pk_mul_f32 v[52:53], v[92:93], v[52:53] op_sel_hi:[0,1]
	v_med3_f32 v94, v55, s60, v115
	v_pk_mul_f32 v[52:53], v[52:53], v[10:11]
	v_cvt_pk_fp8_f32 v96, v93, v94 op_sel:[0,0,1]
	v_pk_mul_f32 v[58:59], v[92:93], v[58:59] op_sel_hi:[0,1]
	v_med3_f32 v93, v52, s60, v115
	v_med3_f32 v94, v53, s60, v115
	v_cvt_pk_fp8_f32 v97, v93, v94
	v_pk_mul_f32 v[58:59], v[58:59], v[12:13]
	s_nop 0
	v_med3_f32 v93, v58, s60, v115
	v_pk_mul_f32 v[56:57], v[92:93], v[56:57] op_sel_hi:[0,1]
	v_med3_f32 v94, v59, s60, v115
	s_waitcnt vmcnt(12)
	v_pk_mul_f32 v[56:57], v[56:57], v[18:19]
	v_cvt_pk_fp8_f32 v97, v93, v94 op_sel:[0,0,1]
	v_pk_mul_f32 v[62:63], v[92:93], v[62:63] op_sel_hi:[0,1]
	v_med3_f32 v93, v56, s60, v115
	v_med3_f32 v94, v57, s60, v115
	v_cvt_pk_fp8_f32 v98, v93, v94
	v_pk_mul_f32 v[62:63], v[62:63], v[20:21]
	s_nop 0
	v_med3_f32 v93, v62, s60, v115
	v_med3_f32 v94, v63, s60, v115
	v_pk_mul_f32 v[60:61], v[92:93], v[60:61] op_sel_hi:[0,1]
	v_cvt_pk_fp8_f32 v98, v93, v94 op_sel:[0,0,1]
	s_waitcnt vmcnt(11)
	v_pk_mul_f32 v[60:61], v[60:61], v[22:23]
	global_store_dword v[74:75], v95, off offset:256
	global_store_dword v[74:75], v96, off offset:512
	global_store_dword v[74:75], v97, off offset:768
	global_store_dword v[74:75], v98, off offset:1024
	v_pk_mul_f32 v[66:67], v[92:93], v[66:67] op_sel_hi:[0,1]
	v_med3_f32 v93, v60, s60, v115
	v_med3_f32 v94, v61, s60, v115
	v_mov_b32_e32 v96, 0
	v_cvt_pk_fp8_f32 v96, v93, v94
	v_pk_mul_f32 v[66:67], v[66:67], v[24:25]
	v_mov_b32_e32 v97, 0
	v_med3_f32 v93, v66, s60, v115
	v_pk_mul_f32 v[64:65], v[92:93], v[64:65] op_sel_hi:[0,1]
	v_med3_f32 v94, v67, s60, v115
	s_waitcnt vmcnt(14)
	v_pk_mul_f32 v[64:65], v[64:65], v[26:27]
	v_cvt_pk_fp8_f32 v96, v93, v94 op_sel:[0,0,1]
	v_pk_mul_f32 v[70:71], v[92:93], v[70:71] op_sel_hi:[0,1]
	v_med3_f32 v93, v64, s60, v115
	v_med3_f32 v94, v65, s60, v115
	v_cvt_pk_fp8_f32 v97, v93, v94
	v_pk_mul_f32 v[70:71], v[70:71], v[28:29]
	v_mov_b32_e32 v98, 0
	v_med3_f32 v93, v70, s60, v115
	v_pk_mul_f32 v[68:69], v[92:93], v[68:69] op_sel_hi:[0,1]
	v_med3_f32 v94, v71, s60, v115
	s_waitcnt vmcnt(13)
	v_pk_mul_f32 v[68:69], v[68:69], v[30:31]
	v_cvt_pk_fp8_f32 v97, v93, v94 op_sel:[0,0,1]
	v_pk_mul_f32 v[72:73], v[92:93], v[72:73] op_sel_hi:[0,1]
	v_med3_f32 v92, v68, s60, v115
	v_med3_f32 v93, v69, s60, v115
	v_cvt_pk_fp8_f32 v98, v92, v93
	v_pk_mul_f32 v[72:73], v[72:73], v[32:33]
	s_nop 0
	v_med3_f32 v92, v72, s60, v115
	v_med3_f32 v93, v73, s60, v115
	v_cvt_pk_fp8_f32 v98, v92, v93 op_sel:[0,0,1]
	ds_read_b128 v[92:95], v34
	global_store_dword v[74:75], v96, off offset:1280
	global_store_dword v[74:75], v97, off offset:1536
	global_store_dword v[74:75], v98, off offset:1792
	ds_read_b128 v[96:99], v34 offset:1024
	s_waitcnt lgkmcnt(1)
	v_mul_f32_e32 v93, v93, v43
	v_fmac_f32_e32 v93, v92, v42
	v_mul_f32_e32 v92, v95, v47
	v_fmac_f32_e32 v92, v94, v46
	v_add_f32_e32 v92, v93, v92
	v_add_f32_e32 v100, 0, v92
	ds_read_b128 v[92:95], v34 offset:2048
	s_waitcnt lgkmcnt(1)
	v_mul_f32_e32 v97, v97, v45
	v_fmac_f32_e32 v97, v96, v44
	v_mul_f32_e32 v96, v99, v51
	v_fmac_f32_e32 v96, v98, v50
	v_add_f32_e32 v96, v97, v96
	v_add_f32_e32 v100, v100, v96
	ds_read_b128 v[96:99], v34 offset:3072
	s_waitcnt lgkmcnt(1)
	v_mul_f32_e32 v93, v93, v49
	v_fmac_f32_e32 v93, v92, v48
	v_mul_f32_e32 v92, v95, v55
	v_fmac_f32_e32 v92, v94, v54
	v_add_f32_e32 v92, v93, v92
	v_add_f32_e32 v100, v100, v92
	ds_read_b128 v[92:95], v34 offset:4096
	s_waitcnt lgkmcnt(1)
	v_mul_f32_e32 v97, v97, v53
	v_fmac_f32_e32 v97, v96, v52
	v_mul_f32_e32 v96, v99, v59
	v_fmac_f32_e32 v96, v98, v58
	v_add_f32_e32 v96, v97, v96
	v_add_f32_e32 v100, v100, v96
	ds_read_b128 v[96:99], v34 offset:5120
	s_waitcnt lgkmcnt(1)
	v_mul_f32_e32 v93, v93, v57
	v_fmac_f32_e32 v93, v92, v56
	v_mul_f32_e32 v92, v95, v63
	v_fmac_f32_e32 v92, v94, v62
	v_add_f32_e32 v92, v93, v92
	v_add_f32_e32 v100, v100, v92
	ds_read_b128 v[92:95], v34 offset:6144
	s_waitcnt lgkmcnt(1)
	v_mul_f32_e32 v97, v97, v61
	v_fmac_f32_e32 v97, v96, v60
	v_mul_f32_e32 v96, v99, v67
	v_fmac_f32_e32 v96, v98, v66
	v_add_f32_e32 v96, v97, v96
	v_add_f32_e32 v100, v100, v96
	ds_read_b128 v[96:99], v34 offset:7168
	s_waitcnt lgkmcnt(1)
	v_mul_f32_e32 v93, v93, v65
	v_fmac_f32_e32 v93, v92, v64
	v_mul_f32_e32 v92, v95, v71
	v_fmac_f32_e32 v92, v94, v70
	v_add_f32_e32 v92, v93, v92
	s_waitcnt lgkmcnt(0)
	v_mul_f32_e32 v93, v97, v69
	v_mul_f32_e32 v94, v99, v73
	v_fmac_f32_e32 v93, v96, v68
	v_fmac_f32_e32 v94, v98, v72
	v_add_f32_e32 v92, v100, v92
	v_add_f32_e32 v93, v93, v94
	v_add_f32_e32 v92, v92, v93
	s_nop 1
	v_add_f32_dpp v92, v92, v92 quad_perm:[1,0,3,2] row_mask:0xf bank_mask:0xf bound_ctrl:1
	s_nop 1
	v_add_f32_dpp v92, v92, v92 quad_perm:[2,3,0,1] row_mask:0xf bank_mask:0xf bound_ctrl:1
	s_nop 1
	v_add_f32_dpp v92, v92, v92 row_half_mirror row_mask:0xf bank_mask:0xf bound_ctrl:1
	s_nop 1
	v_add_f32_dpp v96, v92, v92 row_mirror row_mask:0xf bank_mask:0xf bound_ctrl:1
	ds_read_b128 v[92:95], v34 offset:8192
	v_readlane_b32 s0, v96, 0
	v_readlane_b32 s39, v96, 16
	v_readlane_b32 s1, v96, 32
	v_readlane_b32 s52, v96, 48
	ds_read_b128 v[96:99], v34 offset:9216
	s_waitcnt lgkmcnt(1)
	v_mul_f32_e32 v93, v93, v43
	v_fmac_f32_e32 v93, v92, v42
	v_mul_f32_e32 v92, v95, v47
	v_fmac_f32_e32 v92, v94, v46
	v_add_f32_e32 v92, v93, v92
	s_waitcnt lgkmcnt(0)
	v_mul_f32_e32 v97, v97, v45
	v_add_f32_e32 v100, 0, v92
	v_fmac_f32_e32 v97, v96, v44
	v_mul_f32_e32 v96, v99, v51
	ds_read_b128 v[92:95], v34 offset:10240
	v_fmac_f32_e32 v96, v98, v50
	v_add_f32_e32 v96, v97, v96
	v_add_f32_e32 v100, v100, v96
	ds_read_b128 v[96:99], v34 offset:11264
	s_waitcnt lgkmcnt(1)
	v_mul_f32_e32 v93, v93, v49
	v_fmac_f32_e32 v93, v92, v48
	v_mul_f32_e32 v92, v95, v55
	v_fmac_f32_e32 v92, v94, v54
	v_add_f32_e32 v92, v93, v92
	s_waitcnt lgkmcnt(0)
	v_mul_f32_e32 v97, v97, v53
	v_add_f32_e32 v100, v100, v92
	v_fmac_f32_e32 v97, v96, v52
	v_mul_f32_e32 v96, v99, v59
	ds_read_b128 v[92:95], v34 offset:12288
	v_fmac_f32_e32 v96, v98, v58
	v_add_f32_e32 v96, v97, v96
	v_add_f32_e32 v100, v100, v96
	ds_read_b128 v[96:99], v34 offset:13312
	s_waitcnt lgkmcnt(1)
	v_mul_f32_e32 v93, v93, v57
	v_fmac_f32_e32 v93, v92, v56
	v_mul_f32_e32 v92, v95, v63
	v_fmac_f32_e32 v92, v94, v62
	v_add_f32_e32 v92, v93, v92
	s_waitcnt lgkmcnt(0)
	v_mul_f32_e32 v97, v97, v61
	v_add_f32_e32 v100, v100, v92
	v_fmac_f32_e32 v97, v96, v60
	v_mul_f32_e32 v96, v99, v67
	ds_read_b128 v[92:95], v34 offset:14336
	v_fmac_f32_e32 v96, v98, v66
	v_add_f32_e32 v96, v97, v96
	v_add_f32_e32 v100, v100, v96
	ds_read_b128 v[96:99], v34 offset:15360
	s_waitcnt lgkmcnt(1)
	v_mul_f32_e32 v93, v93, v65
	v_fmac_f32_e32 v93, v92, v64
	v_mul_f32_e32 v92, v95, v71
	v_fmac_f32_e32 v92, v94, v70
	v_add_f32_e32 v92, v93, v92
	s_waitcnt lgkmcnt(0)
	v_mul_f32_e32 v93, v97, v69
	v_mul_f32_e32 v94, v99, v73
	v_fmac_f32_e32 v93, v96, v68
	v_fmac_f32_e32 v94, v98, v72
	v_add_f32_e32 v92, v100, v92
	v_add_f32_e32 v93, v93, v94
	v_add_f32_e32 v92, v92, v93
	s_nop 1
	v_add_f32_dpp v92, v92, v92 quad_perm:[1,0,3,2] row_mask:0xf bank_mask:0xf bound_ctrl:1
	s_nop 1
	v_add_f32_dpp v92, v92, v92 quad_perm:[2,3,0,1] row_mask:0xf bank_mask:0xf bound_ctrl:1
	s_nop 1
	v_add_f32_dpp v92, v92, v92 row_half_mirror row_mask:0xf bank_mask:0xf bound_ctrl:1
	s_nop 1
	v_add_f32_dpp v96, v92, v92 row_mirror row_mask:0xf bank_mask:0xf bound_ctrl:1
	ds_read_b128 v[92:95], v34 offset:16384
	v_readlane_b32 s6, v96, 0
	v_readlane_b32 s53, v96, 16
	v_readlane_b32 s7, v96, 32
	v_readlane_b32 s63, v96, 48
	ds_read_b128 v[96:99], v34 offset:17408
	s_waitcnt lgkmcnt(1)
	v_mul_f32_e32 v93, v93, v43
	v_fmac_f32_e32 v93, v92, v42
	v_mul_f32_e32 v92, v95, v47
	v_fmac_f32_e32 v92, v94, v46
	v_add_f32_e32 v92, v93, v92
	s_waitcnt lgkmcnt(0)
	v_mul_f32_e32 v97, v97, v45
	v_add_f32_e32 v100, 0, v92
	v_fmac_f32_e32 v97, v96, v44
	v_mul_f32_e32 v96, v99, v51
	ds_read_b128 v[92:95], v34 offset:18432
	v_fmac_f32_e32 v96, v98, v50
	v_add_f32_e32 v96, v97, v96
	v_add_f32_e32 v100, v100, v96
	ds_read_b128 v[96:99], v34 offset:19456
	s_waitcnt lgkmcnt(1)
	v_mul_f32_e32 v93, v93, v49
	v_fmac_f32_e32 v93, v92, v48
	v_mul_f32_e32 v92, v95, v55
	v_fmac_f32_e32 v92, v94, v54
	v_add_f32_e32 v92, v93, v92
	s_waitcnt lgkmcnt(0)
	v_mul_f32_e32 v97, v97, v53
	v_add_f32_e32 v100, v100, v92
	v_fmac_f32_e32 v97, v96, v52
	v_mul_f32_e32 v96, v99, v59
	ds_read_b128 v[92:95], v34 offset:20480
	v_fmac_f32_e32 v96, v98, v58
	v_add_f32_e32 v96, v97, v96
	v_add_f32_e32 v100, v100, v96
	ds_read_b128 v[96:99], v34 offset:21504
	s_waitcnt lgkmcnt(1)
	v_mul_f32_e32 v93, v93, v57
	v_fmac_f32_e32 v93, v92, v56
	v_mul_f32_e32 v92, v95, v63
	v_fmac_f32_e32 v92, v94, v62
	v_add_f32_e32 v92, v93, v92
	s_waitcnt lgkmcnt(0)
	v_mul_f32_e32 v97, v97, v61
	v_add_f32_e32 v100, v100, v92
	v_fmac_f32_e32 v97, v96, v60
	v_mul_f32_e32 v96, v99, v67
	ds_read_b128 v[92:95], v34 offset:22528
	v_fmac_f32_e32 v96, v98, v66
	v_add_f32_e32 v96, v97, v96
	v_add_f32_e32 v100, v100, v96
	ds_read_b128 v[96:99], v34 offset:23552
	s_waitcnt lgkmcnt(1)
	v_mul_f32_e32 v93, v93, v65
	v_fmac_f32_e32 v93, v92, v64
	v_mul_f32_e32 v92, v95, v71
	v_fmac_f32_e32 v92, v94, v70
	v_add_f32_e32 v92, v93, v92
	s_waitcnt lgkmcnt(0)
	v_mul_f32_e32 v93, v97, v69
	v_mul_f32_e32 v94, v99, v73
	v_fmac_f32_e32 v93, v96, v68
	v_fmac_f32_e32 v94, v98, v72
	v_add_f32_e32 v92, v100, v92
	v_add_f32_e32 v93, v93, v94
	v_add_f32_e32 v92, v92, v93
	s_nop 1
	v_add_f32_dpp v92, v92, v92 quad_perm:[1,0,3,2] row_mask:0xf bank_mask:0xf bound_ctrl:1
	s_nop 1
	v_add_f32_dpp v92, v92, v92 quad_perm:[2,3,0,1] row_mask:0xf bank_mask:0xf bound_ctrl:1
	s_nop 1
	v_add_f32_dpp v92, v92, v92 row_half_mirror row_mask:0xf bank_mask:0xf bound_ctrl:1
	s_nop 1
	v_add_f32_dpp v96, v92, v92 row_mirror row_mask:0xf bank_mask:0xf bound_ctrl:1
	ds_read_b128 v[92:95], v34 offset:24576
	v_readlane_b32 s8, v96, 0
	v_readlane_b32 s64, v96, 16
	v_readlane_b32 s9, v96, 32
	v_readlane_b32 s65, v96, 48
	ds_read_b128 v[96:99], v34 offset:25600
	s_waitcnt lgkmcnt(1)
	v_mul_f32_e32 v93, v93, v43
	v_fmac_f32_e32 v93, v92, v42
	v_mul_f32_e32 v92, v95, v47
	v_fmac_f32_e32 v92, v94, v46
	v_add_f32_e32 v92, v93, v92
	s_waitcnt lgkmcnt(0)
	v_mul_f32_e32 v97, v97, v45
	v_add_f32_e32 v100, 0, v92
	v_fmac_f32_e32 v97, v96, v44
	v_mul_f32_e32 v96, v99, v51
	ds_read_b128 v[92:95], v34 offset:26624
	v_fmac_f32_e32 v96, v98, v50
	v_add_f32_e32 v96, v97, v96
	v_add_f32_e32 v100, v100, v96
	ds_read_b128 v[96:99], v34 offset:27648
	s_waitcnt lgkmcnt(1)
	v_mul_f32_e32 v93, v93, v49
	v_fmac_f32_e32 v93, v92, v48
	v_mul_f32_e32 v92, v95, v55
	v_fmac_f32_e32 v92, v94, v54
	v_add_f32_e32 v92, v93, v92
	s_waitcnt lgkmcnt(0)
	v_mul_f32_e32 v97, v97, v53
	v_add_f32_e32 v100, v100, v92
	v_fmac_f32_e32 v97, v96, v52
	v_mul_f32_e32 v96, v99, v59
	ds_read_b128 v[92:95], v34 offset:28672
	v_fmac_f32_e32 v96, v98, v58
	v_add_f32_e32 v96, v97, v96
	v_add_f32_e32 v100, v100, v96
	ds_read_b128 v[96:99], v34 offset:29696
	s_waitcnt lgkmcnt(1)
	v_mul_f32_e32 v93, v93, v57
	v_fmac_f32_e32 v93, v92, v56
	v_mul_f32_e32 v92, v95, v63
	v_fmac_f32_e32 v92, v94, v62
	v_add_f32_e32 v92, v93, v92
	s_waitcnt lgkmcnt(0)
	v_mul_f32_e32 v97, v97, v61
	v_add_f32_e32 v100, v100, v92
	v_fmac_f32_e32 v97, v96, v60
	v_mul_f32_e32 v96, v99, v67
	ds_read_b128 v[92:95], v34 offset:30720
	v_fmac_f32_e32 v96, v98, v66
	v_add_f32_e32 v96, v97, v96
	v_add_f32_e32 v100, v100, v96
	ds_read_b128 v[96:99], v34 offset:31744
	s_waitcnt lgkmcnt(1)
	v_mul_f32_e32 v93, v93, v65
	v_fmac_f32_e32 v93, v92, v64
	v_mul_f32_e32 v92, v95, v71
	v_fmac_f32_e32 v92, v94, v70
	v_add_f32_e32 v92, v93, v92
	s_waitcnt lgkmcnt(0)
	v_mul_f32_e32 v93, v97, v69
	v_mul_f32_e32 v94, v99, v73
	v_fmac_f32_e32 v93, v96, v68
	v_fmac_f32_e32 v94, v98, v72
	v_add_f32_e32 v92, v100, v92
	v_add_f32_e32 v93, v93, v94
	v_add_f32_e32 v92, v92, v93
	s_nop 1
	v_add_f32_dpp v92, v92, v92 quad_perm:[1,0,3,2] row_mask:0xf bank_mask:0xf bound_ctrl:1
	s_nop 1
	v_add_f32_dpp v92, v92, v92 quad_perm:[2,3,0,1] row_mask:0xf bank_mask:0xf bound_ctrl:1
	s_nop 1
	v_add_f32_dpp v92, v92, v92 row_half_mirror row_mask:0xf bank_mask:0xf bound_ctrl:1
	s_nop 1
	v_add_f32_dpp v96, v92, v92 row_mirror row_mask:0xf bank_mask:0xf bound_ctrl:1
	ds_read_b128 v[92:95], v34 offset:32768
	v_readlane_b32 s14, v96, 0
	v_readlane_b32 s66, v96, 16
	v_readlane_b32 s15, v96, 32
	v_readlane_b32 s67, v96, 48
	ds_read_b128 v[96:99], v34 offset:33792
	s_waitcnt lgkmcnt(1)
	v_mul_f32_e32 v93, v93, v43
	v_fmac_f32_e32 v93, v92, v42
	v_mul_f32_e32 v92, v95, v47
	v_fmac_f32_e32 v92, v94, v46
	v_add_f32_e32 v92, v93, v92
	s_waitcnt lgkmcnt(0)
	v_mul_f32_e32 v97, v97, v45
	v_add_f32_e32 v100, 0, v92
	v_fmac_f32_e32 v97, v96, v44
	v_mul_f32_e32 v96, v99, v51
	ds_read_b128 v[92:95], v34 offset:34816
	v_fmac_f32_e32 v96, v98, v50
	v_add_f32_e32 v96, v97, v96
	v_add_f32_e32 v100, v100, v96
	ds_read_b128 v[96:99], v34 offset:35840
	s_waitcnt lgkmcnt(1)
	v_mul_f32_e32 v93, v93, v49
	v_fmac_f32_e32 v93, v92, v48
	v_mul_f32_e32 v92, v95, v55
	v_fmac_f32_e32 v92, v94, v54
	v_add_f32_e32 v92, v93, v92
	s_waitcnt lgkmcnt(0)
	v_mul_f32_e32 v97, v97, v53
	v_add_f32_e32 v100, v100, v92
	v_fmac_f32_e32 v97, v96, v52
	v_mul_f32_e32 v96, v99, v59
	ds_read_b128 v[92:95], v34 offset:36864
	v_fmac_f32_e32 v96, v98, v58
	v_add_f32_e32 v96, v97, v96
	v_add_f32_e32 v100, v100, v96
	ds_read_b128 v[96:99], v34 offset:37888
	s_waitcnt lgkmcnt(1)
	v_mul_f32_e32 v93, v93, v57
	v_fmac_f32_e32 v93, v92, v56
	v_mul_f32_e32 v92, v95, v63
	v_fmac_f32_e32 v92, v94, v62
	v_add_f32_e32 v92, v93, v92
	s_waitcnt lgkmcnt(0)
	v_mul_f32_e32 v97, v97, v61
	v_add_f32_e32 v100, v100, v92
	v_fmac_f32_e32 v97, v96, v60
	v_mul_f32_e32 v96, v99, v67
	ds_read_b128 v[92:95], v34 offset:38912
	v_fmac_f32_e32 v96, v98, v66
	v_add_f32_e32 v96, v97, v96
	v_add_f32_e32 v100, v100, v96
	ds_read_b128 v[96:99], v34 offset:39936
	s_waitcnt lgkmcnt(1)
	v_mul_f32_e32 v93, v93, v65
	v_fmac_f32_e32 v93, v92, v64
	v_mul_f32_e32 v92, v95, v71
	v_fmac_f32_e32 v92, v94, v70
	v_add_f32_e32 v92, v93, v92
	s_waitcnt lgkmcnt(0)
	v_mul_f32_e32 v93, v97, v69
	v_mul_f32_e32 v94, v99, v73
	v_fmac_f32_e32 v93, v96, v68
	v_fmac_f32_e32 v94, v98, v72
	v_add_f32_e32 v92, v100, v92
	v_add_f32_e32 v93, v93, v94
	v_add_f32_e32 v92, v92, v93
	s_nop 1
	v_add_f32_dpp v92, v92, v92 quad_perm:[1,0,3,2] row_mask:0xf bank_mask:0xf bound_ctrl:1
	s_nop 1
	v_add_f32_dpp v92, v92, v92 quad_perm:[2,3,0,1] row_mask:0xf bank_mask:0xf bound_ctrl:1
	s_nop 1
	v_add_f32_dpp v92, v92, v92 row_half_mirror row_mask:0xf bank_mask:0xf bound_ctrl:1
	s_nop 1
	v_add_f32_dpp v96, v92, v92 row_mirror row_mask:0xf bank_mask:0xf bound_ctrl:1
	ds_read_b128 v[92:95], v34 offset:40960
	v_readlane_b32 s16, v96, 0
	v_readlane_b32 s69, v96, 16
	v_readlane_b32 s17, v96, 32
	v_readlane_b32 s70, v96, 48
	ds_read_b128 v[96:99], v34 offset:41984
	s_waitcnt lgkmcnt(1)
	v_mul_f32_e32 v93, v93, v43
	v_fmac_f32_e32 v93, v92, v42
	v_mul_f32_e32 v92, v95, v47
	v_fmac_f32_e32 v92, v94, v46
	v_add_f32_e32 v92, v93, v92
	s_waitcnt lgkmcnt(0)
	v_mul_f32_e32 v97, v97, v45
	v_add_f32_e32 v100, 0, v92
	v_fmac_f32_e32 v97, v96, v44
	v_mul_f32_e32 v96, v99, v51
	ds_read_b128 v[92:95], v34 offset:43008
	v_fmac_f32_e32 v96, v98, v50
	v_add_f32_e32 v96, v97, v96
	v_add_f32_e32 v100, v100, v96
	ds_read_b128 v[96:99], v34 offset:44032
	s_waitcnt lgkmcnt(1)
	v_mul_f32_e32 v93, v93, v49
	v_fmac_f32_e32 v93, v92, v48
	v_mul_f32_e32 v92, v95, v55
	v_fmac_f32_e32 v92, v94, v54
	v_add_f32_e32 v92, v93, v92
	s_waitcnt lgkmcnt(0)
	v_mul_f32_e32 v97, v97, v53
	v_add_f32_e32 v100, v100, v92
	v_fmac_f32_e32 v97, v96, v52
	v_mul_f32_e32 v96, v99, v59
	ds_read_b128 v[92:95], v34 offset:45056
	v_fmac_f32_e32 v96, v98, v58
	v_add_f32_e32 v96, v97, v96
	v_add_f32_e32 v100, v100, v96
	ds_read_b128 v[96:99], v34 offset:46080
	s_waitcnt lgkmcnt(1)
	v_mul_f32_e32 v93, v93, v57
	v_fmac_f32_e32 v93, v92, v56
	v_mul_f32_e32 v92, v95, v63
	v_fmac_f32_e32 v92, v94, v62
	v_add_f32_e32 v92, v93, v92
	s_waitcnt lgkmcnt(0)
	v_mul_f32_e32 v97, v97, v61
	v_add_f32_e32 v100, v100, v92
	v_fmac_f32_e32 v97, v96, v60
	v_mul_f32_e32 v96, v99, v67
	ds_read_b128 v[92:95], v34 offset:47104
	v_fmac_f32_e32 v96, v98, v66
	v_add_f32_e32 v96, v97, v96
	v_add_f32_e32 v100, v100, v96
	ds_read_b128 v[96:99], v34 offset:48128
	s_waitcnt lgkmcnt(1)
	v_mul_f32_e32 v93, v93, v65
	v_fmac_f32_e32 v93, v92, v64
	v_mul_f32_e32 v92, v95, v71
	v_fmac_f32_e32 v92, v94, v70
	v_add_f32_e32 v92, v93, v92
	s_waitcnt lgkmcnt(0)
	v_mul_f32_e32 v93, v97, v69
	v_mul_f32_e32 v94, v99, v73
	v_fmac_f32_e32 v93, v96, v68
	v_fmac_f32_e32 v94, v98, v72
	v_add_f32_e32 v92, v100, v92
	v_add_f32_e32 v93, v93, v94
	v_add_f32_e32 v92, v92, v93
	s_nop 1
	v_add_f32_dpp v92, v92, v92 quad_perm:[1,0,3,2] row_mask:0xf bank_mask:0xf bound_ctrl:1
	s_nop 1
	v_add_f32_dpp v92, v92, v92 quad_perm:[2,3,0,1] row_mask:0xf bank_mask:0xf bound_ctrl:1
	s_nop 1
	v_add_f32_dpp v92, v92, v92 row_half_mirror row_mask:0xf bank_mask:0xf bound_ctrl:1
	s_nop 1
	v_add_f32_dpp v96, v92, v92 row_mirror row_mask:0xf bank_mask:0xf bound_ctrl:1
	ds_read_b128 v[92:95], v34 offset:49152
	v_readlane_b32 s18, v96, 0
	v_readlane_b32 s71, v96, 16
	v_readlane_b32 s19, v96, 32
	v_readlane_b32 s72, v96, 48
	ds_read_b128 v[96:99], v34 offset:50176
	s_waitcnt lgkmcnt(1)
	v_mul_f32_e32 v93, v93, v43
	v_fmac_f32_e32 v93, v92, v42
	v_mul_f32_e32 v92, v95, v47
	v_fmac_f32_e32 v92, v94, v46
	v_add_f32_e32 v92, v93, v92
	s_waitcnt lgkmcnt(0)
	v_mul_f32_e32 v97, v97, v45
	v_add_f32_e32 v100, 0, v92
	v_fmac_f32_e32 v97, v96, v44
	v_mul_f32_e32 v96, v99, v51
	ds_read_b128 v[92:95], v34 offset:51200
	v_fmac_f32_e32 v96, v98, v50
	v_add_f32_e32 v96, v97, v96
	v_add_f32_e32 v100, v100, v96
	ds_read_b128 v[96:99], v34 offset:52224
	s_waitcnt lgkmcnt(1)
	v_mul_f32_e32 v93, v93, v49
	v_fmac_f32_e32 v93, v92, v48
	v_mul_f32_e32 v92, v95, v55
	v_fmac_f32_e32 v92, v94, v54
	v_add_f32_e32 v92, v93, v92
	s_waitcnt lgkmcnt(0)
	v_mul_f32_e32 v97, v97, v53
	v_add_f32_e32 v100, v100, v92
	v_fmac_f32_e32 v97, v96, v52
	v_mul_f32_e32 v96, v99, v59
	ds_read_b128 v[92:95], v34 offset:53248
	v_fmac_f32_e32 v96, v98, v58
	v_add_f32_e32 v96, v97, v96
	v_add_f32_e32 v100, v100, v96
	ds_read_b128 v[96:99], v34 offset:54272
	s_waitcnt lgkmcnt(1)
	v_mul_f32_e32 v93, v93, v57
	v_fmac_f32_e32 v93, v92, v56
	v_mul_f32_e32 v92, v95, v63
	v_fmac_f32_e32 v92, v94, v62
	v_add_f32_e32 v92, v93, v92
	s_waitcnt lgkmcnt(0)
	v_mul_f32_e32 v97, v97, v61
	v_add_f32_e32 v100, v100, v92
	v_fmac_f32_e32 v97, v96, v60
	v_mul_f32_e32 v96, v99, v67
	ds_read_b128 v[92:95], v34 offset:55296
	v_fmac_f32_e32 v96, v98, v66
	v_add_f32_e32 v96, v97, v96
	v_add_f32_e32 v100, v100, v96
	ds_read_b128 v[96:99], v34 offset:56320
	s_waitcnt lgkmcnt(1)
	v_mul_f32_e32 v93, v93, v65
	v_fmac_f32_e32 v93, v92, v64
	v_mul_f32_e32 v92, v95, v71
	v_fmac_f32_e32 v92, v94, v70
	v_add_f32_e32 v92, v93, v92
	s_waitcnt lgkmcnt(0)
	v_mul_f32_e32 v93, v97, v69
	v_mul_f32_e32 v94, v99, v73
	v_fmac_f32_e32 v93, v96, v68
	v_fmac_f32_e32 v94, v98, v72
	v_add_f32_e32 v92, v100, v92
	v_add_f32_e32 v93, v93, v94
	v_add_f32_e32 v92, v92, v93
	s_nop 1
	v_add_f32_dpp v92, v92, v92 quad_perm:[1,0,3,2] row_mask:0xf bank_mask:0xf bound_ctrl:1
	s_nop 1
	v_add_f32_dpp v92, v92, v92 quad_perm:[2,3,0,1] row_mask:0xf bank_mask:0xf bound_ctrl:1
	s_nop 1
	v_add_f32_dpp v92, v92, v92 row_half_mirror row_mask:0xf bank_mask:0xf bound_ctrl:1
	s_nop 1
	v_add_f32_dpp v96, v92, v92 row_mirror row_mask:0xf bank_mask:0xf bound_ctrl:1
	ds_read_b128 v[92:95], v34 offset:57344
	v_readlane_b32 s20, v96, 0
	v_readlane_b32 s73, v96, 16
	v_readlane_b32 s21, v96, 32
	v_readlane_b32 s74, v96, 48
	ds_read_b128 v[96:99], v34 offset:58368
	s_waitcnt lgkmcnt(1)
	v_mul_f32_e32 v93, v93, v43
	v_fmac_f32_e32 v93, v92, v42
	v_mul_f32_e32 v92, v95, v47
	v_fmac_f32_e32 v92, v94, v46
	v_add_f32_e32 v92, v93, v92
	s_waitcnt lgkmcnt(0)
	v_mul_f32_e32 v97, v97, v45
	v_add_f32_e32 v100, 0, v92
	v_fmac_f32_e32 v97, v96, v44
	v_mul_f32_e32 v96, v99, v51
	ds_read_b128 v[92:95], v34 offset:59392
	v_fmac_f32_e32 v96, v98, v50
	v_add_f32_e32 v96, v97, v96
	v_add_f32_e32 v100, v100, v96
	ds_read_b128 v[96:99], v34 offset:60416
	s_waitcnt lgkmcnt(1)
	v_mul_f32_e32 v93, v93, v49
	v_fmac_f32_e32 v93, v92, v48
	v_mul_f32_e32 v92, v95, v55
	v_fmac_f32_e32 v92, v94, v54
	v_add_f32_e32 v92, v93, v92
	s_waitcnt lgkmcnt(0)
	v_mul_f32_e32 v97, v97, v53
	v_add_f32_e32 v100, v100, v92
	v_fmac_f32_e32 v97, v96, v52
	v_mul_f32_e32 v96, v99, v59
	ds_read_b128 v[92:95], v34 offset:61440
	v_fmac_f32_e32 v96, v98, v58
	v_add_f32_e32 v96, v97, v96
	v_add_f32_e32 v100, v100, v96
	ds_read_b128 v[96:99], v34 offset:62464
	s_waitcnt lgkmcnt(1)
	v_mul_f32_e32 v93, v93, v57
	v_fmac_f32_e32 v93, v92, v56
	v_mul_f32_e32 v92, v95, v63
	v_fmac_f32_e32 v92, v94, v62
	v_add_f32_e32 v92, v93, v92
	s_waitcnt lgkmcnt(0)
	v_mul_f32_e32 v97, v97, v61
	v_add_f32_e32 v100, v100, v92
	v_fmac_f32_e32 v97, v96, v60
	v_mul_f32_e32 v96, v99, v67
	ds_read_b128 v[92:95], v34 offset:63488
	v_fmac_f32_e32 v96, v98, v66
	v_add_f32_e32 v96, v97, v96
	v_add_f32_e32 v100, v100, v96
	ds_read_b128 v[96:99], v34 offset:64512
	s_waitcnt lgkmcnt(1)
	v_mul_f32_e32 v93, v93, v65
	v_fmac_f32_e32 v93, v92, v64
	v_mul_f32_e32 v92, v95, v71
	v_fmac_f32_e32 v92, v94, v70
	v_add_f32_e32 v92, v93, v92
	s_waitcnt lgkmcnt(0)
	v_mul_f32_e32 v93, v97, v69
	v_mul_f32_e32 v94, v99, v73
	v_fmac_f32_e32 v93, v96, v68
	v_fmac_f32_e32 v94, v98, v72
	v_add_f32_e32 v92, v100, v92
	v_add_f32_e32 v93, v93, v94
	v_add_f32_e32 v92, v92, v93
	s_nop 1
	v_add_f32_dpp v92, v92, v92 quad_perm:[1,0,3,2] row_mask:0xf bank_mask:0xf bound_ctrl:1
	s_nop 1
	v_add_f32_dpp v92, v92, v92 quad_perm:[2,3,0,1] row_mask:0xf bank_mask:0xf bound_ctrl:1
	s_nop 1
	v_add_f32_dpp v92, v92, v92 row_half_mirror row_mask:0xf bank_mask:0xf bound_ctrl:1
	s_nop 1
	v_add_f32_dpp v92, v92, v92 row_mirror row_mask:0xf bank_mask:0xf bound_ctrl:1
	s_nop 0
	v_readlane_b32 s50, v92, 0
	v_readlane_b32 s75, v92, 16
	v_readlane_b32 s51, v92, 32
	v_readlane_b32 s76, v92, 48
	s_and_saveexec_b64 s[46:47], s[4:5]
	s_cbranch_execz .LBB0_1381
	v_readlane_b32 s80, v251, 0
	v_readlane_b32 s82, v251, 2
	v_readlane_b32 s83, v251, 3
	s_nop 4
	v_mov_b32_e32 v92, v234
	v_mov_b32_e32 v93, v235
	v_mov_b32_e32 v94, v236
	v_mov_b32_e32 v95, v237
	v_mov_b32_e32 v96, v238
	v_mov_b32_e32 v97, v239
	v_mov_b32_e32 v98, v240
	v_mov_b32_e32 v99, v241
	v_mov_b32_e32 v100, s75
	v_mov_b32_e32 v101, s76
	v_mov_b32_e32 v120, s53
	v_mov_b32_e32 v121, s63
	v_mov_b32_e32 v122, s39
	v_mov_b32_e32 v123, s52
	v_mov_b32_e32 v102, s73
	v_mov_b32_e32 v103, s74
	v_mov_b32_e32 v104, s71
	v_mov_b32_e32 v105, s72
	v_mov_b32_e32 v106, s69
	v_mov_b32_e32 v107, s70
	v_pk_add_f32 v[100:101], s[50:51], v[100:101]
	v_pk_add_f32 v[120:121], s[6:7], v[120:121]
	v_pk_add_f32 v[122:123], s[0:1], v[122:123]
	v_pk_add_f32 v[102:103], s[20:21], v[102:103]
	v_pk_add_f32 v[104:105], s[18:19], v[104:105]
	v_pk_add_f32 v[106:107], s[16:17], v[106:107]
	v_add_f32_e32 v117, v100, v101
	v_mov_b32_e32 v100, v122
	v_mov_b32_e32 v101, v120
	v_mov_b32_e32 v120, v123
	v_mov_b32_e32 v118, s64
	v_mov_b32_e32 v119, s65
	v_add_f32_e32 v102, v102, v103
	v_add_f32_e32 v103, v104, v105
	v_add_f32_e32 v104, v106, v107
	v_pk_add_f32 v[100:101], v[100:101], v[120:121]
	v_pk_add_f32 v[118:119], s[8:9], v[118:119]
	v_mov_b32_e32 v108, s66
	v_mov_b32_e32 v109, s67
	v_add_f32_e32 v106, v118, v119
	v_pk_add_f32 v[108:109], s[14:15], v[108:109]
	s_mov_b64 s[48:49], exec
	v_add_f32_e32 v105, v108, v109
	v_readlane_b32 s81, v251, 1
	v_readlane_b32 s84, v251, 4
	v_readlane_b32 s85, v251, 5
	v_readlane_b32 s86, v251, 6
	v_readlane_b32 s87, v251, 7
	s_waitcnt vmcnt(0)
	v_add_f32_e32 v94, v94, v102
	v_add_f32_e32 v102, v93, v103
	v_add_f32_e32 v103, v92, v104
	v_pk_add_f32 v[92:93], v[96:97], v[100:101]
	v_add_f32_e32 v98, v98, v106
	v_cmp_gt_f32_e32 vcc, v93, v92
	v_add_f32_e32 v99, v99, v105
	v_add_f32_e32 v95, v95, v117
	v_cndmask_b32_e32 v96, v92, v93, vcc
	v_cmp_gt_f32_e64 s[6:7], v98, v96
	v_cndmask_b32_e64 v97, 0, 1, vcc
	v_cmp_nlt_f32_e64 s[0:1], s62, v92
	v_cndmask_b32_e64 v96, v96, v98, s[6:7]
	v_cmp_gt_f32_e32 vcc, v99, v96
	v_readfirstlane_b32 s39, v97
	s_nop 0
	v_cndmask_b32_e32 v96, v96, v99, vcc
	v_cmp_gt_f32_e64 s[8:9], v103, v96
	s_nop 1
	v_cndmask_b32_e64 v96, v96, v103, s[8:9]
	v_cmp_gt_f32_e64 s[14:15], v102, v96
	s_nop 1
	v_cndmask_b32_e64 v96, v96, v102, s[14:15]
	v_cmp_gt_f32_e64 s[16:17], v94, v96
	s_nop 1
	v_cndmask_b32_e64 v96, v96, v94, s[16:17]
	v_cmp_ngt_f32_e64 s[18:19], v95, v96
	s_and_b64 s[20:21], s[18:19], s[16:17]
	s_and_b64 s[6:7], s[6:7], exec
	s_cselect_b32 s39, 2, s39
	s_and_b64 s[6:7], vcc, exec
	s_cselect_b32 s39, 3, s39
	s_and_b64 s[6:7], s[8:9], exec
	s_cselect_b32 s8, 4, s39
	s_and_b64 s[6:7], s[14:15], exec
	s_cselect_b32 s8, 5, s8
	s_and_b64 s[6:7], s[16:17], exec
	s_cselect_b32 s8, 6, s8
	s_and_b64 s[6:7], s[18:19], exec
	s_cselect_b32 s39, s8, 7
	s_cmp_lg_u32 s39, 5
	s_cselect_b64 s[16:17], -1, 0
	s_cmp_lg_u32 s39, 4
	s_cselect_b64 s[14:15], -1, 0
	s_cmp_lg_u32 s39, 3
	s_cselect_b64 s[8:9], -1, 0
	s_cmp_lg_u32 s39, 2
	s_cselect_b64 s[6:7], -1, 0
	s_cmp_lg_u32 s39, 1
	s_cselect_b64 s[50:51], -1, 0
	s_cmp_eq_u32 s39, 0
	s_cselect_b64 s[52:53], -1, 0
	s_or_b64 vcc, s[52:53], s[0:1]
	v_cndmask_b32_e32 v92, v92, v116, vcc
	v_cmp_gt_f32_e64 s[0:1], v93, v92
	v_cndmask_b32_e64 v97, 0, -1, vcc
	s_and_b64 vcc, s[50:51], s[0:1]
	v_cndmask_b32_e32 v92, v92, v93, vcc
	v_cmp_gt_f32_e64 s[0:1], v98, v92
	s_and_b64 s[0:1], s[6:7], s[0:1]
	v_cndmask_b32_e64 v96, v95, v96, s[18:19]
	v_cndmask_b32_e64 v92, v92, v98, s[0:1]
	v_cmp_gt_f32_e64 s[6:7], v99, v92
	s_and_b64 s[6:7], s[8:9], s[6:7]
	v_readfirstlane_b32 s50, v97
	v_cndmask_b32_e64 v92, v92, v99, s[6:7]
	v_cmp_gt_f32_e64 s[8:9], v103, v92
	s_and_b64 s[8:9], s[14:15], s[8:9]
	s_nop 0
	v_cndmask_b32_e64 v92, v92, v103, s[8:9]
	v_cmp_gt_f32_e64 s[14:15], v102, v92
	s_and_b64 s[14:15], s[16:17], s[14:15]
	s_nop 0
	v_cndmask_b32_e64 v92, v92, v102, s[14:15]
	v_cmp_ngt_f32_e64 s[16:17], v94, v92
	s_or_b64 s[16:17], s[20:21], s[16:17]
	s_nop 0
	v_cndmask_b32_e64 v92, v94, v92, s[16:17]
	v_cmp_gt_f32_e64 s[20:21], v95, v92
	s_and_b64 s[18:19], s[18:19], s[20:21]
	v_cndmask_b32_e64 v92, v92, v95, s[18:19]
	v_sub_f32_e32 v92, v92, v96
	v_mul_f32_e32 v92, 0x3fb8aa3b, v92
	v_exp_f32_e32 v92, v92
	s_and_b64 s[20:21], vcc, exec
	s_cselect_b32 s20, 1, s50
	s_and_b64 s[0:1], s[0:1], exec
	v_add_f32_e32 v92, 1.0, v92
	v_div_scale_f32 v93, s[0:1], v92, v92, 1.0
	v_rcp_f32_e32 v94, v93
	s_cselect_b32 s20, 2, s20
	s_and_b64 s[0:1], s[6:7], exec
	s_cselect_b32 s6, 3, s20
	s_and_b64 s[0:1], s[8:9], exec
	s_cselect_b32 s6, 4, s6
	s_and_b64 s[0:1], s[14:15], exec
	s_cselect_b32 s6, 5, s6
	s_and_b64 s[0:1], s[16:17], exec
	v_fma_f32 v95, -v93, v94, 1.0
	s_cselect_b32 s6, s6, 6
	s_and_b64 s[0:1], s[18:19], exec
	v_fmac_f32_e32 v94, v95, v94
	v_div_scale_f32 v95, vcc, 1.0, v92, 1.0
	s_cselect_b32 s6, 7, s6
	v_mul_f32_e32 v96, v95, v94
	v_fma_f32 v97, -v93, v96, v95
	s_lshl_b32 s0, s6, 8
	v_fmac_f32_e32 v96, v97, v94
	s_add_i32 s7, s0, s39
	v_fma_f32 v93, -v93, v96, v95
	s_add_u32 s0, s56, s28
	v_div_fmas_f32 v93, v93, v94, v96
	s_addc_u32 s1, s57, s29
	v_mov_b32_e32 v94, s7
	v_div_fixup_f32 v92, v93, v92, 1.0
	global_store_dword v113, v94, s[0:1]
	s_add_u32 s0, s56, s42
	v_sub_f32_e32 v93, 1.0, v92
	s_addc_u32 s1, s57, s43
	global_store_dwordx2 v114, v[92:93], s[0:1]
	v_mbcnt_lo_u32_b32 v92, s48, 0
	v_mbcnt_hi_u32_b32 v92, s49, v92
	v_cmp_eq_u32_e32 vcc, 0, v92
	s_and_saveexec_b64 s[0:1], vcc
	s_cbranch_execz .LBB0_1379
	s_lshl_b32 s7, s39, 2
	s_add_i32 s7, s7, 0
	s_add_i32 s7, s7, 0x10000
	s_bcnt1_i32_b64 s8, s[48:49]
	v_mov_b32_e32 v92, s7
	v_mov_b32_e32 v93, s8
	ds_add_u32 v92, v93

.LBB0_1383:
	s_waitcnt vmcnt(15)
	v_lshlrev_b32_e32 v92, 16, v90
	v_and_b32_e32 v93, 0xffff0000, v90
	v_lshlrev_b32_e32 v90, 16, v91
	v_and_b32_e32 v91, 0xffff0000, v91
	s_waitcnt vmcnt(14)
	v_lshlrev_b32_e32 v95, 16, v89
	v_lshlrev_b32_e32 v94, 16, v88
	v_and_b32_e32 v89, 0xffff0000, v89
	v_and_b32_e32 v88, 0xffff0000, v88
	s_waitcnt vmcnt(12)
	v_lshlrev_b32_e32 v119, 16, v80
	v_and_b32_e32 v121, 0xffff0000, v80
	s_waitcnt vmcnt(8)
	v_lshlrev_b32_e32 v109, 16, v76
	v_and_b32_e32 v107, 0xffff0000, v76
	v_mul_f32_e32 v76, v91, v91
	v_mul_f32_e32 v80, v93, v93
	v_lshlrev_b32_e32 v122, 16, v81
	v_and_b32_e32 v123, 0xffff0000, v81
	v_lshlrev_b32_e32 v96, 16, v78
	v_and_b32_e32 v97, 0xffff0000, v78
	v_lshlrev_b32_e32 v102, 16, v79
	v_and_b32_e32 v103, 0xffff0000, v79
	v_lshlrev_b32_e32 v104, 16, v77
	v_and_b32_e32 v105, 0xffff0000, v77
	v_pk_fma_f32 v[76:77], v[90:91], v[90:91], v[76:77] op_sel_hi:[1,1,0]
	v_pk_mul_f32 v[78:79], v[88:89], v[88:89]
	v_pk_fma_f32 v[80:81], v[92:93], v[92:93], v[80:81] op_sel_hi:[1,1,0]
	v_lshlrev_b32_e32 v98, 16, v82
	v_and_b32_e32 v99, 0xffff0000, v82
	v_lshlrev_b32_e32 v100, 16, v83
	v_and_b32_e32 v101, 0xffff0000, v83
	v_pk_fma_f32 v[78:79], v[94:95], v[94:95], v[78:79]
	v_mov_b32_e32 v118, v80
	v_mov_b32_e32 v82, v76
	v_mov_b32_e32 v83, v119
	v_lshlrev_b32_e32 v128, 16, v84
	v_and_b32_e32 v130, 0xffff0000, v84
	v_mul_f32_e32 v84, v121, v121
	v_pk_add_f32 v[76:77], v[80:81], v[76:77]
	v_pk_mul_f32 v[80:81], v[118:119], v[82:83]
	v_pk_add_f32 v[78:79], v[78:79], v[78:79] op_sel:[0,1] op_sel_hi:[1,0]
	v_mov_b32_e32 v77, v81
	v_mov_b32_e32 v79, v84
	v_pk_add_f32 v[76:77], v[76:77], v[78:79]
	v_mul_f32_e32 v78, v99, v99
	v_mul_f32_e32 v80, v101, v101
	v_lshlrev_b32_e32 v124, 16, v86
	v_and_b32_e32 v126, 0xffff0000, v86
	v_lshlrev_b32_e32 v129, 16, v85
	v_and_b32_e32 v131, 0xffff0000, v85
	v_mul_f32_e32 v85, v122, v122
	v_mul_f32_e32 v86, v123, v123
	v_pk_fma_f32 v[78:79], v[98:99], v[98:99], v[78:79] op_sel_hi:[1,1,0]
	v_pk_fma_f32 v[80:81], v[100:101], v[100:101], v[80:81] op_sel_hi:[1,1,0]
	v_mov_b32_e32 v79, v85
	v_mov_b32_e32 v81, v86
	v_and_b32_e32 v127, 0xffff0000, v87
	v_pk_add_f32 v[78:79], v[78:79], v[80:81]
	v_lshlrev_b32_e32 v125, 16, v87
	v_pk_add_f32 v[76:77], v[76:77], v[78:79]
	v_pk_mul_f32 v[78:79], v[126:127], v[126:127]
	v_pk_add_f32 v[76:77], v[76:77], v[76:77] op_sel:[0,1] op_sel_hi:[1,0]
	v_pk_fma_f32 v[78:79], v[124:125], v[124:125], v[78:79]
	v_pk_mul_f32 v[80:81], v[130:131], v[130:131]
	v_pk_add_f32 v[78:79], v[78:79], v[78:79] op_sel:[0,1] op_sel_hi:[1,0]
	v_mov_b32_e32 v108, v76
	v_mov_b32_e32 v82, v78
	v_mov_b32_e32 v83, v109
	v_pk_fma_f32 v[80:81], v[128:129], v[128:129], v[80:81]
	v_pk_add_f32 v[76:77], v[76:77], v[78:79]
	v_pk_mul_f32 v[78:79], v[108:109], v[82:83]
	v_mul_f32_e32 v84, v107, v107
	v_mov_b32_e32 v77, v79
	v_pk_add_f32 v[78:79], v[80:81], v[80:81] op_sel:[0,1] op_sel_hi:[1,0]
	v_mul_f32_e32 v80, v103, v103
	v_mov_b32_e32 v79, v84
	v_pk_add_f32 v[76:77], v[76:77], v[78:79]
	v_mul_f32_e32 v78, v97, v97
	v_mul_f32_e32 v85, v104, v104
	v_mul_f32_e32 v86, v105, v105
	v_pk_fma_f32 v[78:79], v[96:97], v[96:97], v[78:79] op_sel_hi:[1,1,0]
	v_pk_fma_f32 v[80:81], v[102:103], v[102:103], v[80:81] op_sel_hi:[1,1,0]
	v_mov_b32_e32 v79, v85
	v_mov_b32_e32 v81, v86
	v_pk_add_f32 v[78:79], v[78:79], v[80:81]
	v_mov_b32_e32 v82, 0
	v_pk_add_f32 v[76:77], v[76:77], v[78:79]
	v_mov_b32_e32 v106, 0
	v_add_f32_e32 v76, v76, v77
	v_mov_b32_e32 v120, v119
	v_mov_b32_e32 v117, 0
	v_add_f32_dpp v76, v76, v76 quad_perm:[1,0,3,2] row_mask:0xf bank_mask:0xf bound_ctrl:1
	s_nop 1
	v_add_f32_dpp v76, v76, v76 quad_perm:[2,3,0,1] row_mask:0xf bank_mask:0xf bound_ctrl:1
	s_nop 1
	v_add_f32_dpp v76, v76, v76 row_half_mirror row_mask:0xf bank_mask:0xf bound_ctrl:1
	s_nop 1
	v_add_f32_dpp v76, v76, v76 row_mirror row_mask:0xf bank_mask:0xf bound_ctrl:1
	s_nop 0
	v_readlane_b32 s6, v76, 16
	v_readlane_b32 s7, v76, 48
	v_readlane_b32 s0, v76, 0
	v_readlane_b32 s1, v76, 32
	v_mov_b32_e32 v76, s6
	v_mov_b32_e32 v77, s7
	v_pk_add_f32 v[76:77], s[0:1], v[76:77]
	s_nop 0
	v_add_f32_e32 v76, v76, v77
	v_fmamk_f32 v76, v76, 0x3a000000, v111
	v_mul_f32_e32 v77, 0x4f800000, v76
	v_cmp_gt_f32_e32 vcc, s35, v76
	s_nop 1
	v_cndmask_b32_e32 v76, v76, v77, vcc
	v_sqrt_f32_e32 v77, v76
	s_nop 0
	v_add_u32_e32 v78, -1, v77
	v_fma_f32 v79, -v78, v77, v76
	v_cmp_ge_f32_e64 s[0:1], 0, v79
	v_add_u32_e32 v79, 1, v77
	s_nop 0
	v_cndmask_b32_e64 v78, v77, v78, s[0:1]
	v_fma_f32 v77, -v79, v77, v76
	v_cmp_lt_f32_e64 s[0:1], 0, v77
	s_nop 1
	v_cndmask_b32_e64 v77, v78, v79, s[0:1]
	v_mul_f32_e32 v78, 0x37800000, v77
	v_cndmask_b32_e32 v77, v77, v78, vcc
	v_cmp_class_f32_e32 vcc, v76, v112
	s_nop 1
	v_cndmask_b32_e32 v76, v77, v76, vcc
	v_div_scale_f32 v77, s[0:1], v76, v76, 1.0
	v_rcp_f32_e32 v78, v77
	s_nop 0
	v_fma_f32 v79, -v77, v78, 1.0
	v_fmac_f32_e32 v78, v79, v78
	v_div_scale_f32 v79, vcc, 1.0, v76, 1.0
	v_mul_f32_e32 v80, v79, v78
	v_fma_f32 v81, -v77, v80, v79
	v_fmac_f32_e32 v80, v81, v78
	v_fma_f32 v77, -v77, v80, v79
	v_div_fmas_f32 v77, v77, v78, v80
	v_div_fixup_f32 v108, v77, v76, 1.0
	v_pk_mul_f32 v[76:77], v[108:109], v[92:93] op_sel_hi:[0,1]
	v_pk_mul_f32 v[76:77], v[76:77], v[14:15]
	v_pk_mul_f32 v[78:79], v[108:109], v[90:91] op_sel_hi:[0,1]
	v_med3_f32 v80, v76, s60, v115
	v_med3_f32 v81, v77, s60, v115
	v_cvt_pk_fp8_f32 v82, v80, v81
	v_pk_mul_f32 v[78:79], v[78:79], v[16:17]
	v_pk_mul_f32 v[86:87], v[108:109], v[100:101] op_sel_hi:[0,1]
	v_med3_f32 v80, v78, s60, v115
	v_med3_f32 v81, v79, s60, v115
	v_cvt_pk_fp8_f32 v82, v80, v81 op_sel:[0,0,1]
	v_mov_b32_e32 v80, v94
	v_mov_b32_e32 v81, v88
	v_pk_mul_f32 v[80:81], v[108:109], v[80:81] op_sel_hi:[0,1]
	v_pk_mul_f32 v[84:85], v[80:81], v[2:3]
	v_mov_b32_e32 v88, v95
	v_med3_f32 v80, v84, s60, v115
	v_med3_f32 v81, v85, s60, v115
	v_cvt_pk_fp8_f32 v106, v80, v81
	global_store_dword v[74:75], v82, off offset:2048
	v_pk_mul_f32 v[82:83], v[108:109], v[88:89] op_sel_hi:[0,1]
	v_pk_mul_f32 v[82:83], v[82:83], v[4:5]
	v_pk_mul_f32 v[86:87], v[86:87], v[8:9]
	v_med3_f32 v80, v82, s60, v115
	v_med3_f32 v81, v83, s60, v115
	v_cvt_pk_fp8_f32 v106, v80, v81 op_sel:[0,0,1]
	v_pk_mul_f32 v[80:81], v[108:109], v[98:99] op_sel_hi:[0,1]
	v_pk_mul_f32 v[80:81], v[80:81], v[6:7]
	v_mov_b32_e32 v98, 0
	v_med3_f32 v88, v80, s60, v115
	v_med3_f32 v89, v81, s60, v115
	v_cvt_pk_fp8_f32 v98, v88, v89
	v_med3_f32 v88, v86, s60, v115
	v_med3_f32 v89, v87, s60, v115
	v_mov_b32_e32 v99, 0
	v_cvt_pk_fp8_f32 v98, v88, v89 op_sel:[0,0,1]
	v_pk_mul_f32 v[88:89], v[108:109], v[120:121] op_sel_hi:[0,1]
	v_pk_mul_f32 v[90:91], v[88:89], v[10:11]
	v_pk_mul_f32 v[92:93], v[108:109], v[122:123] op_sel_hi:[0,1]
	v_med3_f32 v88, v90, s60, v115
	v_med3_f32 v89, v91, s60, v115
	v_cvt_pk_fp8_f32 v99, v88, v89
	v_pk_mul_f32 v[88:89], v[92:93], v[12:13]
	v_pk_mul_f32 v[96:97], v[108:109], v[96:97] op_sel_hi:[0,1]
	v_med3_f32 v92, v88, s60, v115
	v_med3_f32 v93, v89, s60, v115
	v_cvt_pk_fp8_f32 v99, v92, v93 op_sel:[0,0,1]
	v_mov_b32_e32 v92, v124
	v_mov_b32_e32 v93, v126
	v_pk_mul_f32 v[92:93], v[108:109], v[92:93] op_sel_hi:[0,1]
	v_pk_mul_f32 v[92:93], v[92:93], v[18:19]
	v_mov_b32_e32 v126, v125
	v_med3_f32 v100, v92, s60, v115
	v_med3_f32 v101, v93, s60, v115
	v_cvt_pk_fp8_f32 v117, v100, v101
	v_pk_mul_f32 v[94:95], v[108:109], v[126:127] op_sel_hi:[0,1]
	v_pk_mul_f32 v[94:95], v[94:95], v[20:21]
	v_pk_mul_f32 v[96:97], v[96:97], v[26:27]
	v_med3_f32 v100, v94, s60, v115
	v_med3_f32 v101, v95, s60, v115
	v_cvt_pk_fp8_f32 v117, v100, v101 op_sel:[0,0,1]
	global_store_dword v[74:75], v106, off offset:2304
	global_store_dword v[74:75], v98, off offset:2560
	global_store_dword v[74:75], v99, off offset:2816
	global_store_dword v[74:75], v117, off offset:3072
	v_mov_b32_e32 v98, v128
	v_mov_b32_e32 v99, v130
	v_pk_mul_f32 v[98:99], v[108:109], v[98:99] op_sel_hi:[0,1]
	v_pk_mul_f32 v[100:101], v[98:99], v[22:23]
	v_mov_b32_e32 v117, 0
	v_med3_f32 v98, v100, s60, v115
	v_med3_f32 v99, v101, s60, v115
	v_mov_b32_e32 v130, v129
	v_cvt_pk_fp8_f32 v117, v98, v99
	v_pk_mul_f32 v[118:119], v[108:109], v[130:131] op_sel_hi:[0,1]
	v_pk_mul_f32 v[98:99], v[118:119], v[24:25]
	v_mov_b32_e32 v122, 0
	v_med3_f32 v106, v98, s60, v115
	v_med3_f32 v118, v99, s60, v115
	v_cvt_pk_fp8_f32 v117, v106, v118 op_sel:[0,0,1]
	v_med3_f32 v106, v96, s60, v115
	v_med3_f32 v118, v97, s60, v115
	v_cvt_pk_fp8_f32 v122, v106, v118
	v_pk_mul_f32 v[102:103], v[108:109], v[102:103] op_sel_hi:[0,1]
	v_pk_mul_f32 v[102:103], v[102:103], v[28:29]
	v_mov_b32_e32 v123, 0
	v_med3_f32 v106, v102, s60, v115
	v_med3_f32 v118, v103, s60, v115
	v_cvt_pk_fp8_f32 v122, v106, v118 op_sel:[0,0,1]
	v_mov_b32_e32 v106, v109
	v_pk_mul_f32 v[106:107], v[108:109], v[106:107] op_sel_hi:[0,1]
	v_pk_mul_f32 v[108:109], v[108:109], v[104:105] op_sel_hi:[0,1]
	v_pk_mul_f32 v[104:105], v[106:107], v[30:31]
	ds_read_b128 v[118:121], v34
	v_med3_f32 v106, v104, s60, v115
	v_med3_f32 v107, v105, s60, v115
	v_cvt_pk_fp8_f32 v123, v106, v107
	v_pk_mul_f32 v[106:107], v[108:109], v[32:33]
	s_nop 0
	v_med3_f32 v108, v106, s60, v115
	v_med3_f32 v109, v107, s60, v115
	v_cvt_pk_fp8_f32 v123, v108, v109 op_sel:[0,0,1]
	global_store_dword v[74:75], v117, off offset:3328
	global_store_dword v[74:75], v122, off offset:3584
	global_store_dword v[74:75], v123, off offset:3840
	ds_read_b128 v[122:125], v34 offset:1024
	s_waitcnt lgkmcnt(1)
	v_mul_f32_e32 v74, v119, v77
	v_mul_f32_e32 v75, v121, v79
	v_fmac_f32_e32 v74, v118, v76
	v_fmac_f32_e32 v75, v120, v78
	ds_read_b128 v[118:121], v34 offset:2048
	v_add_f32_e32 v74, v74, v75
	s_waitcnt lgkmcnt(1)
	v_mul_f32_e32 v75, v123, v85
	v_mul_f32_e32 v108, v125, v83
	v_fmac_f32_e32 v75, v122, v84
	v_fmac_f32_e32 v108, v124, v82
	ds_read_b128 v[122:125], v34 offset:3072
	v_add_f32_e32 v74, 0, v74
	v_add_f32_e32 v75, v75, v108
	v_add_f32_e32 v74, v74, v75
	s_waitcnt lgkmcnt(1)
	v_mul_f32_e32 v75, v119, v81
	v_mul_f32_e32 v108, v121, v87
	v_fmac_f32_e32 v75, v118, v80
	v_fmac_f32_e32 v108, v120, v86
	ds_read_b128 v[118:121], v34 offset:4096
	v_add_f32_e32 v75, v75, v108
	v_add_f32_e32 v74, v74, v75
	s_waitcnt lgkmcnt(1)
	v_mul_f32_e32 v75, v123, v91
	v_mul_f32_e32 v108, v125, v89
	v_fmac_f32_e32 v75, v122, v90
	v_fmac_f32_e32 v108, v124, v88
	ds_read_b128 v[122:125], v34 offset:5120
	v_add_f32_e32 v75, v75, v108
	v_add_f32_e32 v74, v74, v75
	s_waitcnt lgkmcnt(1)
	v_mul_f32_e32 v75, v119, v93
	v_mul_f32_e32 v108, v121, v95
	v_fmac_f32_e32 v75, v118, v92
	v_fmac_f32_e32 v108, v120, v94
	ds_read_b128 v[118:121], v34 offset:6144
	v_add_f32_e32 v75, v75, v108
	v_add_f32_e32 v74, v74, v75
	s_waitcnt lgkmcnt(1)
	v_mul_f32_e32 v75, v123, v101
	v_mul_f32_e32 v108, v125, v99
	v_fmac_f32_e32 v75, v122, v100
	v_fmac_f32_e32 v108, v124, v98
	ds_read_b128 v[122:125], v34 offset:7168
	v_add_f32_e32 v75, v75, v108
	v_add_f32_e32 v74, v74, v75
	s_waitcnt lgkmcnt(1)
	v_mul_f32_e32 v75, v119, v97
	v_mul_f32_e32 v108, v121, v103
	v_fmac_f32_e32 v75, v118, v96
	v_fmac_f32_e32 v108, v120, v102
	v_add_f32_e32 v75, v75, v108
	v_add_f32_e32 v74, v74, v75
	ds_read_b128 v[118:121], v34 offset:8192
	s_waitcnt lgkmcnt(1)
	v_mul_f32_e32 v75, v123, v105
	v_mul_f32_e32 v108, v125, v107
	v_fmac_f32_e32 v75, v122, v104
	v_fmac_f32_e32 v108, v124, v106
	v_add_f32_e32 v75, v75, v108
	v_add_f32_e32 v74, v74, v75
	ds_read_b128 v[122:125], v34 offset:9216
	s_waitcnt lgkmcnt(1)
	v_mul_f32_e32 v75, v121, v79
	v_add_f32_dpp v74, v74, v74 quad_perm:[1,0,3,2] row_mask:0xf bank_mask:0xf bound_ctrl:1
	v_fmac_f32_e32 v75, v120, v78
	s_nop 0
	v_add_f32_dpp v74, v74, v74 quad_perm:[2,3,0,1] row_mask:0xf bank_mask:0xf bound_ctrl:1
	s_nop 1
	v_add_f32_dpp v74, v74, v74 row_half_mirror row_mask:0xf bank_mask:0xf bound_ctrl:1
	s_nop 1
	v_add_f32_dpp v74, v74, v74 row_mirror row_mask:0xf bank_mask:0xf bound_ctrl:1
	s_nop 0
	v_readlane_b32 s0, v74, 0
	v_readlane_b32 s39, v74, 16
	v_readlane_b32 s1, v74, 32
	v_readlane_b32 s63, v74, 48
	v_mul_f32_e32 v74, v119, v77
	v_fmac_f32_e32 v74, v118, v76
	ds_read_b128 v[118:121], v34 offset:10240
	v_add_f32_e32 v74, v74, v75
	s_waitcnt lgkmcnt(1)
	v_mul_f32_e32 v75, v123, v85
	v_mul_f32_e32 v108, v125, v83
	v_fmac_f32_e32 v75, v122, v84
	v_fmac_f32_e32 v108, v124, v82
	ds_read_b128 v[122:125], v34 offset:11264
	v_add_f32_e32 v74, 0, v74
	v_add_f32_e32 v75, v75, v108
	v_add_f32_e32 v74, v74, v75
	s_waitcnt lgkmcnt(1)
	v_mul_f32_e32 v75, v119, v81
	v_mul_f32_e32 v108, v121, v87
	v_fmac_f32_e32 v75, v118, v80
	v_fmac_f32_e32 v108, v120, v86
	ds_read_b128 v[118:121], v34 offset:12288
	v_add_f32_e32 v75, v75, v108
	v_add_f32_e32 v74, v74, v75
	s_waitcnt lgkmcnt(1)
	v_mul_f32_e32 v75, v123, v91
	v_mul_f32_e32 v108, v125, v89
	v_fmac_f32_e32 v75, v122, v90
	v_fmac_f32_e32 v108, v124, v88
	ds_read_b128 v[122:125], v34 offset:13312
	v_add_f32_e32 v75, v75, v108
	v_add_f32_e32 v74, v74, v75
	s_waitcnt lgkmcnt(1)
	v_mul_f32_e32 v75, v119, v93
	v_mul_f32_e32 v108, v121, v95
	v_fmac_f32_e32 v75, v118, v92
	v_fmac_f32_e32 v108, v120, v94
	ds_read_b128 v[118:121], v34 offset:14336
	v_add_f32_e32 v75, v75, v108
	v_add_f32_e32 v74, v74, v75
	s_waitcnt lgkmcnt(1)
	v_mul_f32_e32 v75, v123, v101
	v_mul_f32_e32 v108, v125, v99
	v_fmac_f32_e32 v75, v122, v100
	v_fmac_f32_e32 v108, v124, v98
	ds_read_b128 v[122:125], v34 offset:15360
	v_add_f32_e32 v75, v75, v108
	v_add_f32_e32 v74, v74, v75
	s_waitcnt lgkmcnt(1)
	v_mul_f32_e32 v75, v119, v97
	v_mul_f32_e32 v108, v121, v103
	v_fmac_f32_e32 v75, v118, v96
	v_fmac_f32_e32 v108, v120, v102
	v_add_f32_e32 v75, v75, v108
	v_add_f32_e32 v74, v74, v75
	ds_read_b128 v[118:121], v34 offset:16384
	s_waitcnt lgkmcnt(1)
	v_mul_f32_e32 v75, v123, v105
	v_mul_f32_e32 v108, v125, v107
	v_fmac_f32_e32 v75, v122, v104
	v_fmac_f32_e32 v108, v124, v106
	v_add_f32_e32 v75, v75, v108
	v_add_f32_e32 v74, v74, v75
	ds_read_b128 v[122:125], v34 offset:17408
	s_waitcnt lgkmcnt(1)
	v_mul_f32_e32 v75, v121, v79
	v_add_f32_dpp v74, v74, v74 quad_perm:[1,0,3,2] row_mask:0xf bank_mask:0xf bound_ctrl:1
	v_fmac_f32_e32 v75, v120, v78
	s_nop 0
	v_add_f32_dpp v74, v74, v74 quad_perm:[2,3,0,1] row_mask:0xf bank_mask:0xf bound_ctrl:1
	s_nop 1
	v_add_f32_dpp v74, v74, v74 row_half_mirror row_mask:0xf bank_mask:0xf bound_ctrl:1
	s_nop 1
	v_add_f32_dpp v74, v74, v74 row_mirror row_mask:0xf bank_mask:0xf bound_ctrl:1
	s_nop 0
	v_readlane_b32 s6, v74, 0
	v_readlane_b32 s64, v74, 16
	v_readlane_b32 s7, v74, 32
	v_readlane_b32 s65, v74, 48
	v_mul_f32_e32 v74, v119, v77
	v_fmac_f32_e32 v74, v118, v76
	ds_read_b128 v[118:121], v34 offset:18432
	v_add_f32_e32 v74, v74, v75
	s_waitcnt lgkmcnt(1)
	v_mul_f32_e32 v75, v123, v85
	v_mul_f32_e32 v108, v125, v83
	v_fmac_f32_e32 v75, v122, v84
	v_fmac_f32_e32 v108, v124, v82
	ds_read_b128 v[122:125], v34 offset:19456
	v_add_f32_e32 v74, 0, v74
	v_add_f32_e32 v75, v75, v108
	v_add_f32_e32 v74, v74, v75
	s_waitcnt lgkmcnt(1)
	v_mul_f32_e32 v75, v119, v81
	v_mul_f32_e32 v108, v121, v87
	v_fmac_f32_e32 v75, v118, v80
	v_fmac_f32_e32 v108, v120, v86
	ds_read_b128 v[118:121], v34 offset:20480
	v_add_f32_e32 v75, v75, v108
	v_add_f32_e32 v74, v74, v75
	s_waitcnt lgkmcnt(1)
	v_mul_f32_e32 v75, v123, v91
	v_mul_f32_e32 v108, v125, v89
	v_fmac_f32_e32 v75, v122, v90
	v_fmac_f32_e32 v108, v124, v88
	ds_read_b128 v[122:125], v34 offset:21504
	v_add_f32_e32 v75, v75, v108
	v_add_f32_e32 v74, v74, v75
	s_waitcnt lgkmcnt(1)
	v_mul_f32_e32 v75, v119, v93
	v_mul_f32_e32 v108, v121, v95
	v_fmac_f32_e32 v75, v118, v92
	v_fmac_f32_e32 v108, v120, v94
	ds_read_b128 v[118:121], v34 offset:22528
	v_add_f32_e32 v75, v75, v108
	v_add_f32_e32 v74, v74, v75
	s_waitcnt lgkmcnt(1)
	v_mul_f32_e32 v75, v123, v101
	v_mul_f32_e32 v108, v125, v99
	v_fmac_f32_e32 v75, v122, v100
	v_fmac_f32_e32 v108, v124, v98
	ds_read_b128 v[122:125], v34 offset:23552
	v_add_f32_e32 v75, v75, v108
	v_add_f32_e32 v74, v74, v75
	s_waitcnt lgkmcnt(1)
	v_mul_f32_e32 v75, v119, v97
	v_mul_f32_e32 v108, v121, v103
	v_fmac_f32_e32 v75, v118, v96
	v_fmac_f32_e32 v108, v120, v102
	v_add_f32_e32 v75, v75, v108
	v_add_f32_e32 v74, v74, v75
	ds_read_b128 v[118:121], v34 offset:24576
	s_waitcnt lgkmcnt(1)
	v_mul_f32_e32 v75, v123, v105
	v_mul_f32_e32 v108, v125, v107
	v_fmac_f32_e32 v75, v122, v104
	v_fmac_f32_e32 v108, v124, v106
	v_add_f32_e32 v75, v75, v108
	v_add_f32_e32 v74, v74, v75
	ds_read_b128 v[122:125], v34 offset:25600
	s_waitcnt lgkmcnt(1)
	v_mul_f32_e32 v75, v121, v79
	v_add_f32_dpp v74, v74, v74 quad_perm:[1,0,3,2] row_mask:0xf bank_mask:0xf bound_ctrl:1
	v_fmac_f32_e32 v75, v120, v78
	s_nop 0
	v_add_f32_dpp v74, v74, v74 quad_perm:[2,3,0,1] row_mask:0xf bank_mask:0xf bound_ctrl:1
	s_nop 1
	v_add_f32_dpp v74, v74, v74 row_half_mirror row_mask:0xf bank_mask:0xf bound_ctrl:1
	s_nop 1
	v_add_f32_dpp v74, v74, v74 row_mirror row_mask:0xf bank_mask:0xf bound_ctrl:1
	s_nop 0
	v_readlane_b32 s8, v74, 0
	v_readlane_b32 s66, v74, 16
	v_readlane_b32 s9, v74, 32
	v_readlane_b32 s67, v74, 48
	v_mul_f32_e32 v74, v119, v77
	v_fmac_f32_e32 v74, v118, v76
	ds_read_b128 v[118:121], v34 offset:26624
	v_add_f32_e32 v74, v74, v75
	s_waitcnt lgkmcnt(1)
	v_mul_f32_e32 v75, v123, v85
	v_mul_f32_e32 v108, v125, v83
	v_fmac_f32_e32 v75, v122, v84
	v_fmac_f32_e32 v108, v124, v82
	ds_read_b128 v[122:125], v34 offset:27648
	v_add_f32_e32 v74, 0, v74
	v_add_f32_e32 v75, v75, v108
	v_add_f32_e32 v74, v74, v75
	s_waitcnt lgkmcnt(1)
	v_mul_f32_e32 v75, v119, v81
	v_mul_f32_e32 v108, v121, v87
	v_fmac_f32_e32 v75, v118, v80
	v_fmac_f32_e32 v108, v120, v86
	ds_read_b128 v[118:121], v34 offset:28672
	v_add_f32_e32 v75, v75, v108
	v_add_f32_e32 v74, v74, v75
	s_waitcnt lgkmcnt(1)
	v_mul_f32_e32 v75, v123, v91
	v_mul_f32_e32 v108, v125, v89
	v_fmac_f32_e32 v75, v122, v90
	v_fmac_f32_e32 v108, v124, v88
	ds_read_b128 v[122:125], v34 offset:29696
	v_add_f32_e32 v75, v75, v108
	v_add_f32_e32 v74, v74, v75
	s_waitcnt lgkmcnt(1)
	v_mul_f32_e32 v75, v119, v93
	v_mul_f32_e32 v108, v121, v95
	v_fmac_f32_e32 v75, v118, v92
	v_fmac_f32_e32 v108, v120, v94
	ds_read_b128 v[118:121], v34 offset:30720
	v_add_f32_e32 v75, v75, v108
	v_add_f32_e32 v74, v74, v75
	s_waitcnt lgkmcnt(1)
	v_mul_f32_e32 v75, v123, v101
	v_mul_f32_e32 v108, v125, v99
	v_fmac_f32_e32 v75, v122, v100
	v_fmac_f32_e32 v108, v124, v98
	ds_read_b128 v[122:125], v34 offset:31744
	v_add_f32_e32 v75, v75, v108
	v_add_f32_e32 v74, v74, v75
	s_waitcnt lgkmcnt(1)
	v_mul_f32_e32 v75, v119, v97
	v_mul_f32_e32 v108, v121, v103
	v_fmac_f32_e32 v75, v118, v96
	v_fmac_f32_e32 v108, v120, v102
	v_add_f32_e32 v75, v75, v108
	v_add_f32_e32 v74, v74, v75
	s_waitcnt lgkmcnt(0)
	v_mul_f32_e32 v75, v123, v105
	v_mul_f32_e32 v108, v125, v107
	v_fmac_f32_e32 v75, v122, v104
	v_fmac_f32_e32 v108, v124, v106
	v_add_f32_e32 v75, v75, v108
	v_add_f32_e32 v74, v74, v75
	ds_read_b128 v[118:121], v34 offset:32768
	ds_read_b128 v[122:125], v34 offset:33792
	v_add_f32_dpp v74, v74, v74 quad_perm:[1,0,3,2] row_mask:0xf bank_mask:0xf bound_ctrl:1
	s_waitcnt lgkmcnt(1)
	v_mul_f32_e32 v75, v121, v79
	v_add_f32_dpp v74, v74, v74 quad_perm:[2,3,0,1] row_mask:0xf bank_mask:0xf bound_ctrl:1
	v_fmac_f32_e32 v75, v120, v78
	s_waitcnt lgkmcnt(0)
	v_mul_f32_e32 v108, v125, v83
	v_add_f32_dpp v74, v74, v74 row_half_mirror row_mask:0xf bank_mask:0xf bound_ctrl:1
	v_fmac_f32_e32 v108, v124, v82
	s_nop 0
	v_add_f32_dpp v74, v74, v74 row_mirror row_mask:0xf bank_mask:0xf bound_ctrl:1
	s_nop 0
	v_readlane_b32 s14, v74, 0
	v_readlane_b32 s69, v74, 16
	v_readlane_b32 s15, v74, 32
	v_readlane_b32 s70, v74, 48
	v_mul_f32_e32 v74, v119, v77
	v_fmac_f32_e32 v74, v118, v76
	ds_read_b128 v[118:121], v34 offset:34816
	v_add_f32_e32 v74, v74, v75
	v_mul_f32_e32 v75, v123, v85
	v_fmac_f32_e32 v75, v122, v84
	ds_read_b128 v[122:125], v34 offset:35840
	v_add_f32_e32 v74, 0, v74
	v_add_f32_e32 v75, v75, v108
	v_add_f32_e32 v74, v74, v75
	s_waitcnt lgkmcnt(1)
	v_mul_f32_e32 v75, v119, v81
	v_mul_f32_e32 v108, v121, v87
	v_fmac_f32_e32 v75, v118, v80
	v_fmac_f32_e32 v108, v120, v86
	ds_read_b128 v[118:121], v34 offset:36864
	v_add_f32_e32 v75, v75, v108
	v_add_f32_e32 v74, v74, v75
	s_waitcnt lgkmcnt(1)
	v_mul_f32_e32 v75, v123, v91
	v_mul_f32_e32 v108, v125, v89
	v_fmac_f32_e32 v75, v122, v90
	v_fmac_f32_e32 v108, v124, v88
	ds_read_b128 v[122:125], v34 offset:37888
	v_add_f32_e32 v75, v75, v108
	v_add_f32_e32 v74, v74, v75
	s_waitcnt lgkmcnt(1)
	v_mul_f32_e32 v75, v119, v93
	v_mul_f32_e32 v108, v121, v95
	v_fmac_f32_e32 v75, v118, v92
	v_fmac_f32_e32 v108, v120, v94
	ds_read_b128 v[118:121], v34 offset:38912
	v_add_f32_e32 v75, v75, v108
	v_add_f32_e32 v74, v74, v75
	s_waitcnt lgkmcnt(1)
	v_mul_f32_e32 v75, v123, v101
	v_mul_f32_e32 v108, v125, v99
	v_fmac_f32_e32 v75, v122, v100
	v_fmac_f32_e32 v108, v124, v98
	ds_read_b128 v[122:125], v34 offset:39936
	v_add_f32_e32 v75, v75, v108
	v_add_f32_e32 v74, v74, v75
	s_waitcnt lgkmcnt(1)
	v_mul_f32_e32 v75, v119, v97
	v_mul_f32_e32 v108, v121, v103
	v_fmac_f32_e32 v75, v118, v96
	v_fmac_f32_e32 v108, v120, v102
	v_add_f32_e32 v75, v75, v108
	v_add_f32_e32 v74, v74, v75
	s_waitcnt lgkmcnt(0)
	v_mul_f32_e32 v75, v123, v105
	v_mul_f32_e32 v108, v125, v107
	v_fmac_f32_e32 v75, v122, v104
	v_fmac_f32_e32 v108, v124, v106
	v_add_f32_e32 v75, v75, v108
	v_add_f32_e32 v74, v74, v75
	ds_read_b128 v[118:121], v34 offset:40960
	ds_read_b128 v[122:125], v34 offset:41984
	v_add_f32_dpp v74, v74, v74 quad_perm:[1,0,3,2] row_mask:0xf bank_mask:0xf bound_ctrl:1
	s_waitcnt lgkmcnt(1)
	v_mul_f32_e32 v75, v121, v79
	v_add_f32_dpp v74, v74, v74 quad_perm:[2,3,0,1] row_mask:0xf bank_mask:0xf bound_ctrl:1
	v_fmac_f32_e32 v75, v120, v78
	s_waitcnt lgkmcnt(0)
	v_mul_f32_e32 v108, v125, v83
	v_add_f32_dpp v74, v74, v74 row_half_mirror row_mask:0xf bank_mask:0xf bound_ctrl:1
	v_fmac_f32_e32 v108, v124, v82
	s_nop 0
	v_add_f32_dpp v74, v74, v74 row_mirror row_mask:0xf bank_mask:0xf bound_ctrl:1
	s_nop 0
	v_readlane_b32 s16, v74, 0
	v_readlane_b32 s71, v74, 16
	v_readlane_b32 s17, v74, 32
	v_readlane_b32 s72, v74, 48
	v_mul_f32_e32 v74, v119, v77
	v_fmac_f32_e32 v74, v118, v76
	ds_read_b128 v[118:121], v34 offset:43008
	v_add_f32_e32 v74, v74, v75
	v_mul_f32_e32 v75, v123, v85
	v_fmac_f32_e32 v75, v122, v84
	ds_read_b128 v[122:125], v34 offset:44032
	v_add_f32_e32 v74, 0, v74
	v_add_f32_e32 v75, v75, v108
	v_add_f32_e32 v74, v74, v75
	s_waitcnt lgkmcnt(1)
	v_mul_f32_e32 v75, v119, v81
	v_mul_f32_e32 v108, v121, v87
	v_fmac_f32_e32 v75, v118, v80
	v_fmac_f32_e32 v108, v120, v86
	ds_read_b128 v[118:121], v34 offset:45056
	v_add_f32_e32 v75, v75, v108
	v_add_f32_e32 v74, v74, v75
	s_waitcnt lgkmcnt(1)
	v_mul_f32_e32 v75, v123, v91
	v_mul_f32_e32 v108, v125, v89
	v_fmac_f32_e32 v75, v122, v90
	v_fmac_f32_e32 v108, v124, v88
	ds_read_b128 v[122:125], v34 offset:46080
	v_add_f32_e32 v75, v75, v108
	v_add_f32_e32 v74, v74, v75
	s_waitcnt lgkmcnt(1)
	v_mul_f32_e32 v75, v119, v93
	v_mul_f32_e32 v108, v121, v95
	v_fmac_f32_e32 v75, v118, v92
	v_fmac_f32_e32 v108, v120, v94
	ds_read_b128 v[118:121], v34 offset:47104
	v_add_f32_e32 v75, v75, v108
	v_add_f32_e32 v74, v74, v75
	s_waitcnt lgkmcnt(1)
	v_mul_f32_e32 v75, v123, v101
	v_mul_f32_e32 v108, v125, v99
	v_fmac_f32_e32 v75, v122, v100
	v_fmac_f32_e32 v108, v124, v98
	ds_read_b128 v[122:125], v34 offset:48128
	v_add_f32_e32 v75, v75, v108
	v_add_f32_e32 v74, v74, v75
	s_waitcnt lgkmcnt(1)
	v_mul_f32_e32 v75, v119, v97
	v_mul_f32_e32 v108, v121, v103
	v_fmac_f32_e32 v75, v118, v96
	v_fmac_f32_e32 v108, v120, v102
	v_add_f32_e32 v75, v75, v108
	v_add_f32_e32 v74, v74, v75
	s_waitcnt lgkmcnt(0)
	v_mul_f32_e32 v75, v123, v105
	v_mul_f32_e32 v108, v125, v107
	v_fmac_f32_e32 v75, v122, v104
	v_fmac_f32_e32 v108, v124, v106
	v_add_f32_e32 v75, v75, v108
	v_add_f32_e32 v74, v74, v75
	ds_read_b128 v[118:121], v34 offset:49152
	ds_read_b128 v[122:125], v34 offset:50176
	v_add_f32_dpp v74, v74, v74 quad_perm:[1,0,3,2] row_mask:0xf bank_mask:0xf bound_ctrl:1
	s_waitcnt lgkmcnt(1)
	v_mul_f32_e32 v75, v121, v79
	v_add_f32_dpp v74, v74, v74 quad_perm:[2,3,0,1] row_mask:0xf bank_mask:0xf bound_ctrl:1
	v_fmac_f32_e32 v75, v120, v78
	s_waitcnt lgkmcnt(0)
	v_mul_f32_e32 v108, v125, v83
	v_add_f32_dpp v74, v74, v74 row_half_mirror row_mask:0xf bank_mask:0xf bound_ctrl:1
	v_fmac_f32_e32 v108, v124, v82
	s_nop 0
	v_add_f32_dpp v74, v74, v74 row_mirror row_mask:0xf bank_mask:0xf bound_ctrl:1
	s_nop 0
	v_readlane_b32 s18, v74, 0
	v_readlane_b32 s73, v74, 16
	v_readlane_b32 s19, v74, 32
	v_readlane_b32 s74, v74, 48
	v_mul_f32_e32 v74, v119, v77
	v_fmac_f32_e32 v74, v118, v76
	ds_read_b128 v[118:121], v34 offset:51200
	v_add_f32_e32 v74, v74, v75
	v_mul_f32_e32 v75, v123, v85
	v_fmac_f32_e32 v75, v122, v84
	ds_read_b128 v[122:125], v34 offset:52224
	v_add_f32_e32 v74, 0, v74
	v_add_f32_e32 v75, v75, v108
	v_add_f32_e32 v74, v74, v75
	s_waitcnt lgkmcnt(1)
	v_mul_f32_e32 v75, v119, v81
	v_mul_f32_e32 v108, v121, v87
	v_fmac_f32_e32 v75, v118, v80
	v_fmac_f32_e32 v108, v120, v86
	ds_read_b128 v[118:121], v34 offset:53248
	v_add_f32_e32 v75, v75, v108
	v_add_f32_e32 v74, v74, v75
	s_waitcnt lgkmcnt(1)
	v_mul_f32_e32 v75, v123, v91
	v_mul_f32_e32 v108, v125, v89
	v_fmac_f32_e32 v75, v122, v90
	v_fmac_f32_e32 v108, v124, v88
	ds_read_b128 v[122:125], v34 offset:54272
	v_add_f32_e32 v75, v75, v108
	v_add_f32_e32 v74, v74, v75
	s_waitcnt lgkmcnt(1)
	v_mul_f32_e32 v75, v119, v93
	v_mul_f32_e32 v108, v121, v95
	v_fmac_f32_e32 v75, v118, v92
	v_fmac_f32_e32 v108, v120, v94
	ds_read_b128 v[118:121], v34 offset:55296
	v_add_f32_e32 v75, v75, v108
	v_add_f32_e32 v74, v74, v75
	s_waitcnt lgkmcnt(1)
	v_mul_f32_e32 v75, v123, v101
	v_mul_f32_e32 v108, v125, v99
	v_fmac_f32_e32 v75, v122, v100
	v_fmac_f32_e32 v108, v124, v98
	ds_read_b128 v[122:125], v34 offset:56320
	v_add_f32_e32 v75, v75, v108
	v_add_f32_e32 v74, v74, v75
	s_waitcnt lgkmcnt(1)
	v_mul_f32_e32 v75, v119, v97
	v_mul_f32_e32 v108, v121, v103
	v_fmac_f32_e32 v75, v118, v96
	v_fmac_f32_e32 v108, v120, v102
	v_add_f32_e32 v75, v75, v108
	v_add_f32_e32 v74, v74, v75
	s_waitcnt lgkmcnt(0)
	v_mul_f32_e32 v75, v123, v105
	v_mul_f32_e32 v108, v125, v107
	v_fmac_f32_e32 v75, v122, v104
	v_fmac_f32_e32 v108, v124, v106
	v_add_f32_e32 v75, v75, v108
	v_add_f32_e32 v74, v74, v75
	ds_read_b128 v[118:121], v34 offset:57344
	ds_read_b128 v[122:125], v34 offset:58368
	v_add_f32_dpp v74, v74, v74 quad_perm:[1,0,3,2] row_mask:0xf bank_mask:0xf bound_ctrl:1
	s_waitcnt lgkmcnt(1)
	v_mul_f32_e32 v75, v121, v79
	v_add_f32_dpp v74, v74, v74 quad_perm:[2,3,0,1] row_mask:0xf bank_mask:0xf bound_ctrl:1
	v_fmac_f32_e32 v75, v120, v78
	s_waitcnt lgkmcnt(0)
	v_mul_f32_e32 v79, v123, v85
	v_add_f32_dpp v74, v74, v74 row_half_mirror row_mask:0xf bank_mask:0xf bound_ctrl:1
	v_mul_f32_e32 v83, v125, v83
	v_fmac_f32_e32 v79, v122, v84
	v_add_f32_dpp v74, v74, v74 row_mirror row_mask:0xf bank_mask:0xf bound_ctrl:1
	v_fmac_f32_e32 v83, v124, v82
	v_readlane_b32 s20, v74, 0
	v_readlane_b32 s75, v74, 16
	v_readlane_b32 s21, v74, 32
	v_readlane_b32 s76, v74, 48
	v_mul_f32_e32 v74, v119, v77
	v_fmac_f32_e32 v74, v118, v76
	v_add_f32_e32 v74, v74, v75
	v_add_f32_e32 v78, 0, v74
	ds_read_b128 v[74:77], v34 offset:59392
	v_add_f32_e32 v79, v79, v83
	ds_read_b128 v[82:85], v34 offset:60416
	v_add_f32_e32 v78, v78, v79
	s_waitcnt lgkmcnt(1)
	v_mul_f32_e32 v75, v75, v81
	v_fmac_f32_e32 v75, v74, v80
	v_mul_f32_e32 v74, v77, v87
	v_fmac_f32_e32 v74, v76, v86
	v_add_f32_e32 v74, v75, v74
	v_add_f32_e32 v78, v78, v74
	s_waitcnt lgkmcnt(0)
	v_mul_f32_e32 v79, v83, v91
	v_mul_f32_e32 v80, v85, v89
	ds_read_b128 v[74:77], v34 offset:61440
	v_fmac_f32_e32 v79, v82, v90
	v_fmac_f32_e32 v80, v84, v88
	v_add_f32_e32 v79, v79, v80
	v_add_f32_e32 v82, v78, v79
	ds_read_b128 v[78:81], v34 offset:62464
	s_waitcnt lgkmcnt(1)
	v_mul_f32_e32 v75, v75, v93
	v_fmac_f32_e32 v75, v74, v92
	v_mul_f32_e32 v74, v77, v95
	v_fmac_f32_e32 v74, v76, v94
	v_add_f32_e32 v74, v75, v74
	s_waitcnt lgkmcnt(0)
	v_mul_f32_e32 v79, v79, v101
	v_add_f32_e32 v82, v82, v74
	v_fmac_f32_e32 v79, v78, v100
	v_mul_f32_e32 v78, v81, v99
	ds_read_b128 v[74:77], v34 offset:63488
	v_fmac_f32_e32 v78, v80, v98
	v_add_f32_e32 v78, v79, v78
	v_add_f32_e32 v82, v82, v78
	ds_read_b128 v[78:81], v34 offset:64512
	s_waitcnt lgkmcnt(1)
	v_mul_f32_e32 v75, v75, v97
	v_fmac_f32_e32 v75, v74, v96
	v_mul_f32_e32 v74, v77, v103
	v_fmac_f32_e32 v74, v76, v102
	v_add_f32_e32 v74, v75, v74
	s_waitcnt lgkmcnt(0)
	v_mul_f32_e32 v75, v79, v105
	v_mul_f32_e32 v76, v81, v107
	v_fmac_f32_e32 v75, v78, v104
	v_fmac_f32_e32 v76, v80, v106
	v_add_f32_e32 v74, v82, v74
	v_add_f32_e32 v75, v75, v76
	v_add_f32_e32 v74, v74, v75
	s_nop 1
	v_add_f32_dpp v74, v74, v74 quad_perm:[1,0,3,2] row_mask:0xf bank_mask:0xf bound_ctrl:1
	s_nop 1
	v_add_f32_dpp v74, v74, v74 quad_perm:[2,3,0,1] row_mask:0xf bank_mask:0xf bound_ctrl:1
	s_nop 1
	v_add_f32_dpp v74, v74, v74 row_half_mirror row_mask:0xf bank_mask:0xf bound_ctrl:1
	s_nop 1
	v_add_f32_dpp v74, v74, v74 row_mirror row_mask:0xf bank_mask:0xf bound_ctrl:1
	s_nop 0
	v_readlane_b32 s52, v74, 0
	v_readlane_b32 s77, v74, 16
	v_readlane_b32 s53, v74, 32
	v_readlane_b32 s78, v74, 48
	s_and_saveexec_b64 s[48:49], s[4:5]
	s_cbranch_execz .LBB0_1375
	v_readlane_b32 s80, v251, 0
	v_readlane_b32 s82, v251, 2
	v_readlane_b32 s83, v251, 3
	s_nop 4
	v_mov_b32_e32 v74, v234
	v_mov_b32_e32 v75, v235
	v_mov_b32_e32 v76, v236
	v_mov_b32_e32 v77, v237
	v_mov_b32_e32 v78, v238
	v_mov_b32_e32 v79, v239
	v_mov_b32_e32 v80, v240
	v_mov_b32_e32 v81, v241
	v_mov_b32_e32 v82, s77
	v_mov_b32_e32 v83, s78
	v_mov_b32_e32 v94, s64
	v_mov_b32_e32 v95, s65
	v_mov_b32_e32 v96, s39
	v_mov_b32_e32 v97, s63
	v_mov_b32_e32 v84, s75
	v_mov_b32_e32 v85, s76
	v_mov_b32_e32 v86, s73
	v_mov_b32_e32 v87, s74
	v_mov_b32_e32 v88, s71
	v_mov_b32_e32 v89, s72
	v_pk_add_f32 v[82:83], s[52:53], v[82:83]
	v_pk_add_f32 v[94:95], s[6:7], v[94:95]
	v_pk_add_f32 v[96:97], s[0:1], v[96:97]
	v_pk_add_f32 v[84:85], s[20:21], v[84:85]
	v_pk_add_f32 v[86:87], s[18:19], v[86:87]
	v_pk_add_f32 v[88:89], s[16:17], v[88:89]
	v_add_f32_e32 v98, v82, v83
	v_mov_b32_e32 v82, v96
	v_mov_b32_e32 v83, v94
	v_mov_b32_e32 v94, v97
	v_mov_b32_e32 v92, s66
	v_mov_b32_e32 v93, s67
	v_add_f32_e32 v84, v84, v85
	v_add_f32_e32 v85, v86, v87
	v_add_f32_e32 v86, v88, v89
	v_pk_add_f32 v[82:83], v[82:83], v[94:95]
	v_pk_add_f32 v[92:93], s[8:9], v[92:93]
	v_mov_b32_e32 v90, s69
	v_mov_b32_e32 v91, s70
	v_add_f32_e32 v88, v92, v93
	v_pk_add_f32 v[90:91], s[14:15], v[90:91]
	s_mov_b64 s[50:51], exec
	v_add_f32_e32 v87, v90, v91
	v_readlane_b32 s81, v251, 1
	v_readlane_b32 s84, v251, 4
	v_readlane_b32 s85, v251, 5
	v_readlane_b32 s86, v251, 6
	v_readlane_b32 s87, v251, 7
	s_waitcnt vmcnt(0)
	v_add_f32_e32 v76, v76, v84
	v_add_f32_e32 v84, v75, v85
	v_add_f32_e32 v85, v74, v86
	v_pk_add_f32 v[74:75], v[78:79], v[82:83]
	v_add_f32_e32 v80, v80, v88
	v_cmp_gt_f32_e32 vcc, v75, v74
	v_add_f32_e32 v81, v81, v87
	v_add_f32_e32 v77, v77, v98
	v_cndmask_b32_e32 v78, v74, v75, vcc
	v_cmp_gt_f32_e64 s[6:7], v80, v78
	v_cndmask_b32_e64 v79, 0, 1, vcc
	v_cmp_nlt_f32_e64 s[0:1], s62, v74
	v_cndmask_b32_e64 v78, v78, v80, s[6:7]
	v_cmp_gt_f32_e32 vcc, v81, v78
	v_readfirstlane_b32 s39, v79
	s_nop 0
	v_cndmask_b32_e32 v78, v78, v81, vcc
	v_cmp_gt_f32_e64 s[8:9], v85, v78
	s_nop 1
	v_cndmask_b32_e64 v78, v78, v85, s[8:9]
	v_cmp_gt_f32_e64 s[14:15], v84, v78
	s_nop 1
	v_cndmask_b32_e64 v78, v78, v84, s[14:15]
	v_cmp_gt_f32_e64 s[16:17], v76, v78
	s_nop 1
	v_cndmask_b32_e64 v78, v78, v76, s[16:17]
	v_cmp_ngt_f32_e64 s[18:19], v77, v78
	s_and_b64 s[20:21], s[18:19], s[16:17]
	s_and_b64 s[6:7], s[6:7], exec
	s_cselect_b32 s39, 2, s39
	s_and_b64 s[6:7], vcc, exec
	s_cselect_b32 s39, 3, s39
	s_and_b64 s[6:7], s[8:9], exec
	s_cselect_b32 s8, 4, s39
	s_and_b64 s[6:7], s[14:15], exec
	s_cselect_b32 s8, 5, s8
	s_and_b64 s[6:7], s[16:17], exec
	s_cselect_b32 s8, 6, s8
	s_and_b64 s[6:7], s[18:19], exec
	s_cselect_b32 s52, s8, 7
	s_cmp_lg_u32 s52, 5
	s_cselect_b64 s[16:17], -1, 0
	s_cmp_lg_u32 s52, 4
	s_cselect_b64 s[14:15], -1, 0
	s_cmp_lg_u32 s52, 3
	s_cselect_b64 s[8:9], -1, 0
	s_cmp_lg_u32 s52, 2
	s_cselect_b64 s[6:7], -1, 0
	s_cmp_lg_u32 s52, 1
	s_cselect_b64 s[64:65], -1, 0
	s_cmp_eq_u32 s52, 0
	s_cselect_b64 s[66:67], -1, 0
	s_or_b64 vcc, s[66:67], s[0:1]
	v_cndmask_b32_e32 v74, v74, v116, vcc
	v_cmp_gt_f32_e64 s[0:1], v75, v74
	v_cndmask_b32_e64 v79, 0, -1, vcc
	s_and_b64 vcc, s[64:65], s[0:1]
	v_cndmask_b32_e32 v74, v74, v75, vcc
	v_cmp_gt_f32_e64 s[0:1], v80, v74
	s_and_b64 s[0:1], s[6:7], s[0:1]
	v_cndmask_b32_e64 v78, v77, v78, s[18:19]
	v_cndmask_b32_e64 v74, v74, v80, s[0:1]
	v_cmp_gt_f32_e64 s[6:7], v81, v74
	s_and_b64 s[6:7], s[8:9], s[6:7]
	v_readfirstlane_b32 s39, v79
	v_cndmask_b32_e64 v74, v74, v81, s[6:7]
	v_cmp_gt_f32_e64 s[8:9], v85, v74
	s_and_b64 s[8:9], s[14:15], s[8:9]
	s_nop 0
	v_cndmask_b32_e64 v74, v74, v85, s[8:9]
	v_cmp_gt_f32_e64 s[14:15], v84, v74
	s_and_b64 s[14:15], s[16:17], s[14:15]
	s_nop 0
	v_cndmask_b32_e64 v74, v74, v84, s[14:15]
	v_cmp_ngt_f32_e64 s[16:17], v76, v74
	s_or_b64 s[16:17], s[20:21], s[16:17]
	s_nop 0
	v_cndmask_b32_e64 v74, v76, v74, s[16:17]
	v_cmp_gt_f32_e64 s[20:21], v77, v74
	s_and_b64 s[18:19], s[18:19], s[20:21]
	v_cndmask_b32_e64 v74, v74, v77, s[18:19]
	v_sub_f32_e32 v74, v74, v78
	v_mul_f32_e32 v74, 0x3fb8aa3b, v74
	v_exp_f32_e32 v74, v74
	s_and_b64 s[20:21], vcc, exec
	s_cselect_b32 s20, 1, s39
	s_and_b64 s[0:1], s[0:1], exec
	v_add_f32_e32 v74, 1.0, v74
	v_div_scale_f32 v75, s[0:1], v74, v74, 1.0
	v_rcp_f32_e32 v76, v75
	s_cselect_b32 s20, 2, s20
	s_and_b64 s[0:1], s[6:7], exec
	s_cselect_b32 s6, 3, s20
	s_and_b64 s[0:1], s[8:9], exec
	s_cselect_b32 s6, 4, s6
	s_and_b64 s[0:1], s[14:15], exec
	s_cselect_b32 s6, 5, s6
	s_and_b64 s[0:1], s[16:17], exec
	v_fma_f32 v77, -v75, v76, 1.0
	s_cselect_b32 s6, s6, 6
	s_and_b64 s[0:1], s[18:19], exec
	v_fmac_f32_e32 v76, v77, v76
	v_div_scale_f32 v77, vcc, 1.0, v74, 1.0
	s_cselect_b32 s6, 7, s6
	v_mul_f32_e32 v78, v77, v76
	v_fma_f32 v79, -v75, v78, v77
	s_lshl_b32 s0, s6, 8
	v_fmac_f32_e32 v78, v79, v76
	s_add_i32 s7, s0, s52
	v_fma_f32 v75, -v75, v78, v77
	s_add_u32 s0, s56, s28
	v_div_fmas_f32 v75, v75, v76, v78
	s_addc_u32 s1, s57, s29
	v_mov_b32_e32 v76, s7
	s_ashr_i32 s39, s38, 31
	global_store_dword v113, v76, s[0:1] offset:4
	s_lshl_b64 s[0:1], s[38:39], 2
	v_div_fixup_f32 v74, v75, v74, 1.0
	s_add_u32 s0, s30, s0
	v_sub_f32_e32 v75, 1.0, v74
	s_addc_u32 s1, s31, s1
	global_store_dwordx2 v35, v[74:75], s[0:1]
	v_mbcnt_lo_u32_b32 v74, s50, 0
	v_mbcnt_hi_u32_b32 v74, s51, v74
	v_cmp_eq_u32_e32 vcc, 0, v74
	s_and_saveexec_b64 s[0:1], vcc
	s_cbranch_execz .LBB0_1386
	s_lshl_b32 s7, s52, 2
	s_add_i32 s7, s7, 0
	s_add_i32 s7, s7, 0x10000
	s_bcnt1_i32_b64 s8, s[50:51]
	v_mov_b32_e32 v74, s7
	v_mov_b32_e32 v75, s8
	ds_add_u32 v74, v75

.LBB0_1619:
	s_lshl_b32 s16, s15, 8
	v_add_u32_e32 v2, s16, v182
	v_ashrrev_i32_e32 v3, 31, v2
	s_nop 15
	s_nop 7
	v_lshl_add_u64 v[2:3], v[2:3], 2, s[28:29]
	global_load_dword v6, v[2:3], off
	v_add_u32_e32 v240, s16, v184
	v_ashrrev_i32_e32 v241, 31, v240
	v_lshl_add_u64 v[240:241], v[240:241], 2, s[28:29]
	global_load_dword v232, v[240:241], off
	v_add_u32_e32 v240, s16, v185
	v_ashrrev_i32_e32 v241, 31, v240
	v_lshl_add_u64 v[240:241], v[240:241], 2, s[28:29]
	global_load_dword v233, v[240:241], off
	v_add_u32_e32 v240, s16, v186
	v_ashrrev_i32_e32 v241, 31, v240
	v_lshl_add_u64 v[240:241], v[240:241], 2, s[28:29]
	global_load_dword v234, v[240:241], off
	v_add_u32_e32 v240, s16, v187
	v_ashrrev_i32_e32 v241, 31, v240
	v_lshl_add_u64 v[240:241], v[240:241], 2, s[28:29]
	global_load_dword v235, v[240:241], off
	v_add_u32_e32 v240, s16, v188
	v_ashrrev_i32_e32 v241, 31, v240
	v_lshl_add_u64 v[240:241], v[240:241], 2, s[28:29]
	global_load_dword v236, v[240:241], off
	v_add_u32_e32 v240, s16, v189
	v_ashrrev_i32_e32 v241, 31, v240
	v_lshl_add_u64 v[240:241], v[240:241], 2, s[28:29]
	global_load_dword v237, v[240:241], off
	v_add_u32_e32 v240, s16, v190
	v_ashrrev_i32_e32 v241, 31, v240
	v_lshl_add_u64 v[240:241], v[240:241], 2, s[28:29]
	global_load_dword v238, v[240:241], off
	s_ashr_i32 s15, s14, 31
	s_lshl_b64 s[14:15], s[14:15], 18
	v_add_u32_e32 v4, s16, v184
	v_lshl_add_u64 v[2:3], v[178:179], 0, s[14:15]
	v_ashrrev_i32_e32 v5, 31, v4
	v_lshl_add_u64 v[20:21], v[162:163], 2, v[2:3]
	v_lshl_add_u64 v[22:23], v[4:5], 2, s[28:29]
	s_andn2_b64 vcc, exec, s[8:9]
	s_mov_b64 s[8:9], -1
	s_waitcnt vmcnt(0)
	v_mul_f32_e32 v16, 0x3c000000, v6
	v_pk_mul_f32 v[6:7], v[148:149], v[16:17] op_sel_hi:[1,0]
	v_pk_mul_f32 v[4:5], v[146:147], v[16:17] op_sel_hi:[1,0]
	v_pk_mul_f32 v[10:11], v[152:153], v[16:17] op_sel_hi:[1,0]
	v_pk_mul_f32 v[8:9], v[150:151], v[16:17] op_sel_hi:[1,0]
	v_pk_mul_f32 v[14:15], v[156:157], v[16:17] op_sel_hi:[1,0]
	v_pk_mul_f32 v[12:13], v[154:155], v[16:17] op_sel_hi:[1,0]
	v_pk_mul_f32 v[18:19], v[160:161], v[16:17] op_sel_hi:[1,0]
	v_pk_mul_f32 v[16:17], v[158:159], v[16:17] op_sel_hi:[1,0]
	global_store_dwordx4 v[20:21], v[4:7], off
	global_store_dwordx4 v[20:21], v[8:11], off offset:16
	global_store_dwordx4 v[20:21], v[12:15], off offset:512
	global_store_dwordx4 v[20:21], v[16:19], off offset:528
	v_add_u32_e32 v4, s16, v185
	v_ashrrev_i32_e32 v5, 31, v4
	v_lshl_add_u64 v[20:21], v[164:165], 2, v[2:3]
	v_lshl_add_u64 v[22:23], v[4:5], 2, s[28:29]
	v_mov_b32_e32 v6, v232
	v_mul_f32_e32 v16, 0x3c000000, v6
	v_pk_mul_f32 v[6:7], v[144:145], v[16:17] op_sel_hi:[1,0]
	v_pk_mul_f32 v[4:5], v[142:143], v[16:17] op_sel_hi:[1,0]
	v_pk_mul_f32 v[10:11], v[140:141], v[16:17] op_sel_hi:[1,0]
	v_pk_mul_f32 v[8:9], v[138:139], v[16:17] op_sel_hi:[1,0]
	v_pk_mul_f32 v[14:15], v[136:137], v[16:17] op_sel_hi:[1,0]
	v_pk_mul_f32 v[12:13], v[134:135], v[16:17] op_sel_hi:[1,0]
	v_pk_mul_f32 v[18:19], v[132:133], v[16:17] op_sel_hi:[1,0]
	v_pk_mul_f32 v[16:17], v[130:131], v[16:17] op_sel_hi:[1,0]
	global_store_dwordx4 v[20:21], v[4:7], off
	global_store_dwordx4 v[20:21], v[8:11], off offset:16
	global_store_dwordx4 v[20:21], v[12:15], off offset:512
	global_store_dwordx4 v[20:21], v[16:19], off offset:528
	v_add_u32_e32 v4, s16, v186
	v_ashrrev_i32_e32 v5, 31, v4
	v_lshl_add_u64 v[20:21], v[166:167], 2, v[2:3]
	v_lshl_add_u64 v[22:23], v[4:5], 2, s[28:29]
	v_mov_b32_e32 v6, v233
	v_mul_f32_e32 v16, 0x3c000000, v6
	v_pk_mul_f32 v[6:7], v[128:129], v[16:17] op_sel_hi:[1,0]
	v_pk_mul_f32 v[4:5], v[126:127], v[16:17] op_sel_hi:[1,0]
	v_pk_mul_f32 v[10:11], v[124:125], v[16:17] op_sel_hi:[1,0]
	v_pk_mul_f32 v[8:9], v[122:123], v[16:17] op_sel_hi:[1,0]
	v_pk_mul_f32 v[14:15], v[120:121], v[16:17] op_sel_hi:[1,0]
	v_pk_mul_f32 v[12:13], v[118:119], v[16:17] op_sel_hi:[1,0]
	v_pk_mul_f32 v[18:19], v[116:117], v[16:17] op_sel_hi:[1,0]
	v_pk_mul_f32 v[16:17], v[114:115], v[16:17] op_sel_hi:[1,0]
	global_store_dwordx4 v[20:21], v[4:7], off
	global_store_dwordx4 v[20:21], v[8:11], off offset:16
	global_store_dwordx4 v[20:21], v[12:15], off offset:512
	global_store_dwordx4 v[20:21], v[16:19], off offset:528
	v_add_u32_e32 v4, s16, v187
	v_ashrrev_i32_e32 v5, 31, v4
	v_lshl_add_u64 v[20:21], v[168:169], 2, v[2:3]
	v_lshl_add_u64 v[22:23], v[4:5], 2, s[28:29]
	v_mov_b32_e32 v6, v234
	v_mul_f32_e32 v16, 0x3c000000, v6
	v_pk_mul_f32 v[6:7], v[112:113], v[16:17] op_sel_hi:[1,0]
	v_pk_mul_f32 v[4:5], v[110:111], v[16:17] op_sel_hi:[1,0]
	v_pk_mul_f32 v[10:11], v[108:109], v[16:17] op_sel_hi:[1,0]
	v_pk_mul_f32 v[8:9], v[106:107], v[16:17] op_sel_hi:[1,0]
	v_pk_mul_f32 v[14:15], v[104:105], v[16:17] op_sel_hi:[1,0]
	v_pk_mul_f32 v[12:13], v[102:103], v[16:17] op_sel_hi:[1,0]
	v_pk_mul_f32 v[18:19], v[100:101], v[16:17] op_sel_hi:[1,0]
	v_pk_mul_f32 v[16:17], v[98:99], v[16:17] op_sel_hi:[1,0]
	global_store_dwordx4 v[20:21], v[4:7], off
	global_store_dwordx4 v[20:21], v[8:11], off offset:16
	global_store_dwordx4 v[20:21], v[12:15], off offset:512
	global_store_dwordx4 v[20:21], v[16:19], off offset:528
	v_add_u32_e32 v4, s16, v188
	v_ashrrev_i32_e32 v5, 31, v4
	v_lshl_add_u64 v[20:21], v[170:171], 2, v[2:3]
	v_lshl_add_u64 v[22:23], v[4:5], 2, s[28:29]
	v_mov_b32_e32 v6, v235
	v_mul_f32_e32 v16, 0x3c000000, v6
	v_pk_mul_f32 v[6:7], v[96:97], v[16:17] op_sel_hi:[1,0]
	v_pk_mul_f32 v[4:5], v[94:95], v[16:17] op_sel_hi:[1,0]
	v_pk_mul_f32 v[10:11], v[92:93], v[16:17] op_sel_hi:[1,0]
	v_pk_mul_f32 v[8:9], v[90:91], v[16:17] op_sel_hi:[1,0]
	v_pk_mul_f32 v[14:15], v[88:89], v[16:17] op_sel_hi:[1,0]
	v_pk_mul_f32 v[12:13], v[86:87], v[16:17] op_sel_hi:[1,0]
	v_pk_mul_f32 v[18:19], v[84:85], v[16:17] op_sel_hi:[1,0]
	v_pk_mul_f32 v[16:17], v[82:83], v[16:17] op_sel_hi:[1,0]
	global_store_dwordx4 v[20:21], v[4:7], off
	global_store_dwordx4 v[20:21], v[8:11], off offset:16
	global_store_dwordx4 v[20:21], v[12:15], off offset:512
	global_store_dwordx4 v[20:21], v[16:19], off offset:528
	v_add_u32_e32 v4, s16, v189
	v_ashrrev_i32_e32 v5, 31, v4
	v_lshl_add_u64 v[20:21], v[172:173], 2, v[2:3]
	v_lshl_add_u64 v[22:23], v[4:5], 2, s[28:29]
	v_mov_b32_e32 v6, v236
	v_mul_f32_e32 v16, 0x3c000000, v6
	v_pk_mul_f32 v[6:7], v[80:81], v[16:17] op_sel_hi:[1,0]
	v_pk_mul_f32 v[4:5], v[78:79], v[16:17] op_sel_hi:[1,0]
	v_pk_mul_f32 v[10:11], v[76:77], v[16:17] op_sel_hi:[1,0]
	v_pk_mul_f32 v[8:9], v[74:75], v[16:17] op_sel_hi:[1,0]
	v_pk_mul_f32 v[14:15], v[72:73], v[16:17] op_sel_hi:[1,0]
	v_pk_mul_f32 v[12:13], v[70:71], v[16:17] op_sel_hi:[1,0]
	v_pk_mul_f32 v[18:19], v[68:69], v[16:17] op_sel_hi:[1,0]
	v_pk_mul_f32 v[16:17], v[66:67], v[16:17] op_sel_hi:[1,0]
	global_store_dwordx4 v[20:21], v[4:7], off
	global_store_dwordx4 v[20:21], v[8:11], off offset:16
	global_store_dwordx4 v[20:21], v[12:15], off offset:512
	global_store_dwordx4 v[20:21], v[16:19], off offset:528
	v_add_u32_e32 v4, s16, v190
	v_ashrrev_i32_e32 v5, 31, v4
	v_lshl_add_u64 v[20:21], v[174:175], 2, v[2:3]
	v_lshl_add_u64 v[22:23], v[4:5], 2, s[28:29]
	v_mov_b32_e32 v6, v237
	v_mul_f32_e32 v16, 0x3c000000, v6
	v_pk_mul_f32 v[6:7], v[64:65], v[16:17] op_sel_hi:[1,0]
	v_pk_mul_f32 v[4:5], v[62:63], v[16:17] op_sel_hi:[1,0]
	v_pk_mul_f32 v[10:11], v[60:61], v[16:17] op_sel_hi:[1,0]
	v_pk_mul_f32 v[8:9], v[58:59], v[16:17] op_sel_hi:[1,0]
	v_pk_mul_f32 v[14:15], v[56:57], v[16:17] op_sel_hi:[1,0]
	v_pk_mul_f32 v[12:13], v[54:55], v[16:17] op_sel_hi:[1,0]
	v_pk_mul_f32 v[18:19], v[52:53], v[16:17] op_sel_hi:[1,0]
	v_pk_mul_f32 v[16:17], v[50:51], v[16:17] op_sel_hi:[1,0]
	global_store_dwordx4 v[20:21], v[4:7], off
	global_store_dwordx4 v[20:21], v[8:11], off offset:16
	global_store_dwordx4 v[20:21], v[12:15], off offset:512
	global_store_dwordx4 v[20:21], v[16:19], off offset:528
	v_mov_b32_e32 v4, v238
	v_mul_f32_e32 v14, 0x3c000000, v4
	v_lshl_add_u64 v[18:19], v[176:177], 2, v[2:3]
	v_pk_mul_f32 v[4:5], v[48:49], v[14:15] op_sel_hi:[1,0]
	v_pk_mul_f32 v[2:3], v[46:47], v[14:15] op_sel_hi:[1,0]
	v_pk_mul_f32 v[8:9], v[44:45], v[14:15] op_sel_hi:[1,0]
	v_pk_mul_f32 v[6:7], v[42:43], v[14:15] op_sel_hi:[1,0]
	v_pk_mul_f32 v[12:13], v[40:41], v[14:15] op_sel_hi:[1,0]
	v_pk_mul_f32 v[10:11], v[38:39], v[14:15] op_sel_hi:[1,0]
	v_pk_mul_f32 v[16:17], v[36:37], v[14:15] op_sel_hi:[1,0]
	v_pk_mul_f32 v[14:15], v[34:35], v[14:15] op_sel_hi:[1,0]
	global_store_dwordx4 v[18:19], v[2:5], off
	global_store_dwordx4 v[18:19], v[6:9], off offset:16
	global_store_dwordx4 v[18:19], v[10:13], off offset:512
	global_store_dwordx4 v[18:19], v[14:17], off offset:528
	s_cbranch_vccnz .LBB0_1612
	s_andn2_b64 vcc, exec, s[0:1]
	s_cbranch_vccnz .LBB0_1611
	s_barrier
	s_branch .LBB0_1611
